# v15 + removed the 60 adjacent s_setprio 0 / s_setprio 1 pairs between MFMA groups inside compute segments
# speedup vs baseline: 1.0161x; 1.0070x over previous
; #define PG8_STAGE(bufoff, rs_, soff_, voff) do { _Pragma("unroll") for (int _i = 0; _i < 2; ++_i) \
;         __builtin_amdgcn_raw_ptr_buffer_load_lds(rs_, (LAS void*)(lds + (bufoff) + ldsw + _i * 8192), 16, (int)(voff)[_i], (int)(soff_), 0, 0); } while (0)
; #define PG8_LDA(dst, b, h) do { _Pragma("unroll") for (int m = 0; m < 4; ++m) dst[m] = PG8_LD2(lds + PG8_SA(b, h) + aoff + m * 2048); } while (0)
; #define PG8_LDB(dst, b, h) do { _Pragma("unroll") for (int n = 0; n < 2; ++n) dst[n] = PG8_LD2(lds + PG8_SB(b, h) + boff + n * 2048); } while (0)
; #define PG8_WAIT_V(n) asm volatile("s_waitcnt vmcnt(" #n ")" ::: "memory")
; #define PG8_WAIT_L(n) asm volatile("s_waitcnt lgkmcnt(" #n ")" ::: "memory")
; #define PG8_BAR __builtin_amdgcn_s_barrier()
; #define PG8_SCHED __builtin_amdgcn_sched_barrier(0)
; template <class Epi, class Sched, bool ALIGN_EPI = false, bool SP2 = false, bool FP8 = false>
; __device__ __forceinline__ void gemm_phase(LAS unsigned char* lds, const Gemm g, const Sched& S, const Epi& E, int wbase) {
;     ...
;             PG8_LDB(B0, 0, 0); PG8_LDB(B1, 0, 1); PG8_SCHED; PG8_LDA(At, 0, 0); PG8_STAGE(PG8_SA(1, 1), rAc, a1 + hstep, voffA);
;             PG8_WAIT_V(8); PG8_WAIT_L(0); PG8_BAR; PG8_MMA(0, 0, At, B0); PG8_MMA(0, 1, At, B1); PG8_BAR; PG8_SCHED;
;             PG8_LDA(At, 0, 1); PG8_STAGE(PG8_SB(0, 0), rB2, b2, voffB); PG8_STAGE(PG8_SB(0, 1), rB2, b2 + hstep, voffB); PG8_STAGE(PG8_SA(0, 0), rA2, a2, voffA);
;             PG8_WAIT_V(8); PG8_WAIT_L(0); PG8_BAR; PG8_MMA(1, 0, At, B0); PG8_MMA(1, 1, At, B1); PG8_BAR; PG8_SCHED;
.LBB0_258:
	ds_read_b128 v[128:131], v252
	ds_read_b128 v[132:135], v252 offset:1024
	ds_read_b128 v[136:139], v252 offset:2048
	ds_read_b128 v[140:143], v252 offset:3072
	ds_read_b128 v[144:147], v225
	ds_read_b128 v[148:151], v225 offset:1024
	ds_read_b128 v[152:155], v225 offset:2048
	ds_read_b128 v[156:159], v225 offset:3072
	s_add_i32 s6, s16, 0x80
	s_cmp_eq_u32 s18, s29
	s_cselect_b32 s46, s2, s6
	s_cselect_b32 s31, s3, s28
	s_or_b32 s30, s46, 0x80
	s_add_i32 s6, s41, s16
	s_mov_b32 m0, s19
	ds_read_b128 v[176:179], v172
	ds_read_b128 v[180:183], v172 offset:1024
	ds_read_b128 v[184:187], v172 offset:2048
	ds_read_b128 v[188:191], v172 offset:3072
	ds_read_b128 v[194:197], v172 offset:4096
	ds_read_b128 v[198:201], v172 offset:5120
	ds_read_b128 v[202:205], v172 offset:6144
	ds_read_b128 v[206:209], v172 offset:7168
	buffer_load_dwordx4 v192, s[36:39], s6 offen lds
	s_mov_b32 m0, s20
	s_nop 0
	buffer_load_dwordx4 v223, s[36:39], s6 offen lds
	s_waitcnt vmcnt(8)
	s_waitcnt lgkmcnt(0)
	s_barrier
	s_setprio 1
	v_mfma_f32_16x16x128_f8f6f4 v[124:127], v[128:135], v[176:183], v[124:127]
	v_mfma_f32_16x16x128_f8f6f4 v[120:123], v[136:143], v[176:183], v[120:123]
	v_mfma_f32_16x16x128_f8f6f4 v[108:111], v[128:135], v[184:191], v[108:111]
	v_mfma_f32_16x16x128_f8f6f4 v[104:107], v[136:143], v[184:191], v[104:107]
	v_mfma_f32_16x16x128_f8f6f4 v[160:163], v[128:135], v[194:201], v[92:95]
	v_mfma_f32_16x16x128_f8f6f4 v[210:213], v[136:143], v[194:201], v[88:91]
	v_mfma_f32_16x16x128_f8f6f4 v[214:217], v[128:135], v[202:209], v[76:79]
	v_mfma_f32_16x16x128_f8f6f4 v[218:221], v[136:143], v[202:209], v[72:75]
	v_mfma_f32_16x16x128_f8f6f4 v[116:119], v[144:151], v[176:183], v[116:119]
	v_mfma_f32_16x16x128_f8f6f4 v[112:115], v[152:159], v[176:183], v[112:115]
	v_mfma_f32_16x16x128_f8f6f4 v[100:103], v[144:151], v[184:191], v[100:103]
	v_mfma_f32_16x16x128_f8f6f4 v[96:99], v[152:159], v[184:191], v[96:99]
	v_mfma_f32_16x16x128_f8f6f4 v[176:179], v[144:151], v[194:201], v[84:87]
	v_mfma_f32_16x16x128_f8f6f4 v[180:183], v[152:159], v[194:201], v[80:83]
	v_mfma_f32_16x16x128_f8f6f4 v[184:187], v[144:151], v[202:209], v[68:71]
	v_mfma_f32_16x16x128_f8f6f4 v[188:191], v[152:159], v[202:209], v[64:67]
	s_setprio 0
	s_barrier
	s_mov_b32 m0, s43
	s_mov_b32 s6, s38
	s_mov_b32 s7, s39
	s_nop 1
	ds_read_b128 v[64:67], v172 offset:16384
	ds_read_b128 v[68:71], v172 offset:17408
	ds_read_b128 v[72:75], v172 offset:18432
	ds_read_b128 v[76:79], v172 offset:19456
	ds_read_b128 v[80:83], v172 offset:20480
	ds_read_b128 v[84:87], v172 offset:21504
	ds_read_b128 v[88:91], v172 offset:22528
	ds_read_b128 v[92:95], v172 offset:23552
	buffer_load_dwordx4 v222, s[4:7], s31 offen lds
	s_mov_b32 m0, s44
	s_add_i32 s47, s31, s41
	buffer_load_dwordx4 v193, s[4:7], s31 offen lds
	s_mov_b32 m0, s45
	s_nop 0
	buffer_load_dwordx4 v222, s[4:7], s47 offen lds
	s_mov_b32 m0, s52
	s_nop 0
	buffer_load_dwordx4 v193, s[4:7], s47 offen lds
	s_mov_b32 m0, s42
	s_nop 0
	buffer_load_dwordx4 v192, s[36:39], s46 offen lds
	s_mov_b32 m0, s53
	s_nop 0
	buffer_load_dwordx4 v223, s[36:39], s46 offen lds
	s_waitcnt vmcnt(8)
	s_waitcnt lgkmcnt(0)
	s_barrier
	s_setprio 1
	v_mfma_f32_16x16x128_f8f6f4 v[60:63], v[128:135], v[64:71], v[60:63]
	v_mfma_f32_16x16x128_f8f6f4 v[56:59], v[136:143], v[64:71], v[56:59]
	v_mfma_f32_16x16x128_f8f6f4 v[194:197], v[128:135], v[72:79], v[44:47]
	v_mfma_f32_16x16x128_f8f6f4 v[198:201], v[136:143], v[72:79], v[40:43]
	v_mfma_f32_16x16x128_f8f6f4 v[202:205], v[128:135], v[80:87], v[28:31]
	v_mfma_f32_16x16x128_f8f6f4 v[206:209], v[136:143], v[80:87], v[24:27]
	v_mfma_f32_16x16x128_f8f6f4 v[236:239], v[128:135], v[88:95], v[12:15]
	v_mfma_f32_16x16x128_f8f6f4 v[240:243], v[136:143], v[88:95], v[8:11]
	v_mfma_f32_16x16x128_f8f6f4 v[52:55], v[144:151], v[64:71], v[52:55]
	v_mfma_f32_16x16x128_f8f6f4 v[48:51], v[152:159], v[64:71], v[48:51]
	v_mfma_f32_16x16x128_f8f6f4 v[244:247], v[144:151], v[72:79], v[36:39]
	v_mfma_f32_16x16x128_f8f6f4 v[248:251], v[152:159], v[72:79], v[32:35]
	v_mfma_f32_16x16x128_f8f6f4 v[226:229], v[144:151], v[80:87], v[20:23]
	v_mfma_f32_16x16x128_f8f6f4 v[232:235], v[152:159], v[80:87], v[16:19]
	v_mfma_f32_16x16x128_f8f6f4 v[164:167], v[144:151], v[88:95], v[4:7]
	v_mfma_f32_16x16x128_f8f6f4 v[168:171], v[152:159], v[88:95], v[0:3]
	s_setprio 0
	s_barrier
; #define PG8_STAGE(bufoff, rs_, soff_, voff) do { _Pragma("unroll") for (int _i = 0; _i < 2; ++_i) \
;         __builtin_amdgcn_raw_ptr_buffer_load_lds(rs_, (LAS void*)(lds + (bufoff) + ldsw + _i * 8192), 16, (int)(voff)[_i], (int)(soff_), 0, 0); } while (0)
; #define PG8_LDA(dst, b, h) do { _Pragma("unroll") for (int m = 0; m < 4; ++m) dst[m] = PG8_LD2(lds + PG8_SA(b, h) + aoff + m * 2048); } while (0)
; #define PG8_LDB(dst, b, h) do { _Pragma("unroll") for (int n = 0; n < 2; ++n) dst[n] = PG8_LD2(lds + PG8_SB(b, h) + boff + n * 2048); } while (0)
; #define PG8_WAIT_V(n) asm volatile("s_waitcnt vmcnt(" #n ")" ::: "memory")
; #define PG8_WAIT_L(n) asm volatile("s_waitcnt lgkmcnt(" #n ")" ::: "memory")
; #define PG8_BAR __builtin_amdgcn_s_barrier()
; #define PG8_SCHED __builtin_amdgcn_sched_barrier(0)
; template <class Epi, class Sched, bool ALIGN_EPI = false, bool SP2 = false, bool FP8 = false>
; __device__ __forceinline__ void gemm_phase(LAS unsigned char* lds, const Gemm g, const Sched& S, const Epi& E, int wbase) {
;     ...
;             PG8_LDB(B0, 1, 0); PG8_LDB(B1, 1, 1); PG8_SCHED; PG8_LDA(At, 1, 0); PG8_STAGE(PG8_SA(0, 1), rA2, a2 + hstep, voffA);
;             PG8_WAIT_V(8); PG8_WAIT_L(0); PG8_BAR; PG8_MMA(0, 0, At, B0); PG8_MMA(0, 1, At, B1); PG8_BAR; PG8_SCHED;
;             PG8_LDA(At, 1, 1); PG8_STAGE(PG8_SB(1, 0), rB2, b3, voffB); PG8_STAGE(PG8_SB(1, 1), rB2, b3 + hstep, voffB); PG8_STAGE(PG8_SA(1, 0), rA2, a3, voffA);
;             PG8_WAIT_V(8); PG8_WAIT_L(0); PG8_BAR; PG8_MMA(1, 0, At, B0); PG8_MMA(1, 1, At, B1); PG8_BAR; PG8_SCHED;
	s_nop 4
	ds_read_b128 v[0:3], v173
	ds_read_b128 v[4:7], v173 offset:1024
	ds_read_b128 v[16:19], v173 offset:2048
	ds_read_b128 v[20:23], v173 offset:3072
	ds_read_b128 v[128:131], v174
	ds_read_b128 v[132:135], v174 offset:1024
	ds_read_b128 v[136:139], v174 offset:2048
	ds_read_b128 v[140:143], v174 offset:3072
	s_add_i32 s46, s46, s41
	s_mov_b32 m0, s56
	ds_read_b128 v[8:11], v172 offset:32768
	ds_read_b128 v[12:15], v172 offset:33792
	ds_read_b128 v[24:27], v172 offset:34816
	ds_read_b128 v[28:31], v172 offset:35840
	ds_read_b128 v[32:35], v172 offset:36864
	ds_read_b128 v[36:39], v172 offset:37888
	ds_read_b128 v[40:43], v172 offset:38912
	ds_read_b128 v[44:47], v172 offset:39936
	buffer_load_dwordx4 v192, s[36:39], s46 offen lds
	s_mov_b32 m0, s57
	s_nop 0
	buffer_load_dwordx4 v223, s[36:39], s46 offen lds
	s_waitcnt vmcnt(8)
	s_waitcnt lgkmcnt(0)
	s_barrier
	s_setprio 1
	v_mfma_f32_16x16x128_f8f6f4 v[124:127], v[0:7], v[8:15], v[124:127]
	v_mfma_f32_16x16x128_f8f6f4 v[120:123], v[16:23], v[8:15], v[120:123]
	v_mfma_f32_16x16x128_f8f6f4 v[108:111], v[0:7], v[24:31], v[108:111]
	v_mfma_f32_16x16x128_f8f6f4 v[104:107], v[16:23], v[24:31], v[104:107]
	v_mfma_f32_16x16x128_f8f6f4 v[92:95], v[0:7], v[32:39], v[160:163]
	v_mfma_f32_16x16x128_f8f6f4 v[88:91], v[16:23], v[32:39], v[210:213]
	v_mfma_f32_16x16x128_f8f6f4 v[76:79], v[0:7], v[40:47], v[214:217]
	v_mfma_f32_16x16x128_f8f6f4 v[72:75], v[16:23], v[40:47], v[218:221]
	v_mfma_f32_16x16x128_f8f6f4 v[116:119], v[128:135], v[8:15], v[116:119]
	v_mfma_f32_16x16x128_f8f6f4 v[112:115], v[136:143], v[8:15], v[112:115]
	v_mfma_f32_16x16x128_f8f6f4 v[100:103], v[128:135], v[24:31], v[100:103]
	v_mfma_f32_16x16x128_f8f6f4 v[96:99], v[136:143], v[24:31], v[96:99]
	v_mfma_f32_16x16x128_f8f6f4 v[84:87], v[128:135], v[32:39], v[176:179]
	v_mfma_f32_16x16x128_f8f6f4 v[80:83], v[136:143], v[32:39], v[180:183]
	v_mfma_f32_16x16x128_f8f6f4 v[68:71], v[128:135], v[40:47], v[184:187]
	v_mfma_f32_16x16x128_f8f6f4 v[64:67], v[136:143], v[40:47], v[188:191]
	s_setprio 0
	s_barrier
	s_mov_b32 m0, s58
	s_bitset1_b32 s31, 7
	ds_read_b128 v[32:35], v172 offset:49152
	ds_read_b128 v[36:39], v172 offset:50176
	ds_read_b128 v[144:147], v172 offset:51200
	ds_read_b128 v[148:151], v172 offset:52224
	ds_read_b128 v[152:155], v172 offset:53248
	ds_read_b128 v[156:159], v172 offset:54272
	ds_read_b128 v[176:179], v172 offset:55296
	ds_read_b128 v[180:183], v172 offset:56320
	buffer_load_dwordx4 v222, s[4:7], s31 offen lds
	s_mov_b32 m0, s59
	s_nop 0
	buffer_load_dwordx4 v193, s[4:7], s31 offen lds
	s_add_i32 s31, s31, s41
	s_mov_b32 m0, s65
	s_nop 0
	buffer_load_dwordx4 v222, s[4:7], s31 offen lds
	s_mov_b32 m0, s33
	s_nop 0
	buffer_load_dwordx4 v193, s[4:7], s31 offen lds
	s_mov_b32 m0, s12
	s_nop 0
	buffer_load_dwordx4 v192, s[36:39], s30 offen lds
	s_mov_b32 m0, s13
	s_nop 0
	buffer_load_dwordx4 v223, s[36:39], s30 offen lds
	s_waitcnt vmcnt(8)
	s_waitcnt lgkmcnt(0)
	s_barrier
	s_setprio 1
	v_mfma_f32_16x16x128_f8f6f4 v[60:63], v[0:7], v[32:39], v[60:63]
	v_mfma_f32_16x16x128_f8f6f4 v[56:59], v[16:23], v[32:39], v[56:59]
	v_mfma_f32_16x16x128_f8f6f4 v[44:47], v[0:7], v[144:151], v[194:197]
	v_mfma_f32_16x16x128_f8f6f4 v[40:43], v[16:23], v[144:151], v[198:201]
	v_mfma_f32_16x16x128_f8f6f4 v[28:31], v[0:7], v[152:159], v[202:205]
	v_mfma_f32_16x16x128_f8f6f4 v[24:27], v[16:23], v[152:159], v[206:209]
	v_mfma_f32_16x16x128_f8f6f4 v[12:15], v[0:7], v[176:183], v[236:239]
	v_mfma_f32_16x16x128_f8f6f4 v[8:11], v[16:23], v[176:183], v[240:243]
	v_mfma_f32_16x16x128_f8f6f4 v[52:55], v[128:135], v[32:39], v[52:55]
	v_mfma_f32_16x16x128_f8f6f4 v[48:51], v[136:143], v[32:39], v[48:51]
	v_mfma_f32_16x16x128_f8f6f4 v[36:39], v[128:135], v[144:151], v[244:247]
	v_mfma_f32_16x16x128_f8f6f4 v[32:35], v[136:143], v[144:151], v[248:251]
	v_mfma_f32_16x16x128_f8f6f4 v[20:23], v[128:135], v[152:159], v[226:229]
	v_mfma_f32_16x16x128_f8f6f4 v[16:19], v[136:143], v[152:159], v[232:235]
	v_mfma_f32_16x16x128_f8f6f4 v[4:7], v[128:135], v[176:183], v[164:167]
	v_mfma_f32_16x16x128_f8f6f4 v[0:3], v[136:143], v[176:183], v[168:171]
	s_setprio 0
	s_barrier
	s_add_i32 s29, s29, 2
	s_addk_i32 s16, 0x100
	s_addk_i32 s28, 0x100
	s_cmp_ge_i32 s29, s77
	s_cbranch_scc0 .LBB0_258
	v_mov_b32_e32 v233, v175
	v_mov_b32_e32 v234, v230
	v_mov_b32_e32 v164, v231
	v_mov_b32_e32 v231, 1
	v_mov_b32_e32 v230, 0x358637bd
	s_and_b64 vcc, exec, s[78:79]
	s_cbranch_vccnz .LBB0_261
	s_branch .LBB0_262

; #define PG8_STAGE(bufoff, rs_, soff_, voff) do { _Pragma("unroll") for (int _i = 0; _i < 2; ++_i) \
;         __builtin_amdgcn_raw_ptr_buffer_load_lds(rs_, (LAS void*)(lds + (bufoff) + ldsw + _i * 8192), 16, (int)(voff)[_i], (int)(soff_), 0, 0); } while (0)
; #define PG8_LDA(dst, b, h) do { _Pragma("unroll") for (int m = 0; m < 4; ++m) dst[m] = PG8_LD2(lds + PG8_SA(b, h) + aoff + m * 2048); } while (0)
; #define PG8_LDB(dst, b, h) do { _Pragma("unroll") for (int n = 0; n < 2; ++n) dst[n] = PG8_LD2(lds + PG8_SB(b, h) + boff + n * 2048); } while (0)
; #define PG8_WAIT_V(n) asm volatile("s_waitcnt vmcnt(" #n ")" ::: "memory")
; #define PG8_WAIT_L(n) asm volatile("s_waitcnt lgkmcnt(" #n ")" ::: "memory")
; #define PG8_BAR __builtin_amdgcn_s_barrier()
; #define PG8_SCHED __builtin_amdgcn_sched_barrier(0)
; template <class Epi, class Sched, bool ALIGN_EPI = false, bool SP2 = false, bool FP8 = false>
; __device__ __forceinline__ void gemm_phase(LAS unsigned char* lds, const Gemm g, const Sched& S, const Epi& E, int wbase) {
;     ...
;             PG8_LDB(B0, 0, 0); PG8_LDB(B1, 0, 1); PG8_SCHED; PG8_LDA(At, 0, 0); PG8_STAGE(PG8_SA(1, 1), rAc, a1 + hstep, voffA);
;             PG8_WAIT_V(8); PG8_WAIT_L(0); PG8_BAR; PG8_MMA(0, 0, At, B0); PG8_MMA(0, 1, At, B1); PG8_BAR; PG8_SCHED;
;             PG8_LDA(At, 0, 1); PG8_STAGE(PG8_SB(0, 0), rB2, b2, voffB); PG8_STAGE(PG8_SB(0, 1), rB2, b2 + hstep, voffB); PG8_STAGE(PG8_SA(0, 0), rA2, a2, voffA);
;             PG8_WAIT_V(8); PG8_WAIT_L(0); PG8_BAR; PG8_MMA(1, 0, At, B0); PG8_MMA(1, 1, At, B1); PG8_BAR; PG8_SCHED;
.LBB0_352:
	v_add_u32_e32 v140, 0x10000, v170
	v_add_u32_e32 v156, 0x14000, v170
	ds_read_b128 v[128:131], v140
	ds_read_b128 v[132:135], v140 offset:1024
	ds_read_b128 v[136:139], v140 offset:2048
	ds_read_b128 v[140:143], v140 offset:3072
	ds_read_b128 v[144:147], v156
	ds_read_b128 v[148:151], v156 offset:1024
	ds_read_b128 v[152:155], v156 offset:2048
	ds_read_b128 v[156:159], v156 offset:3072
	s_add_i32 s6, s16, 0x80
	s_cmp_eq_u32 s12, s29
	s_cselect_b32 s46, s2, s6
	s_cselect_b32 s31, s3, s28
	s_or_b32 s30, s46, 0x80
	s_add_i32 s6, s33, s16
	s_mov_b32 m0, s13
	ds_read_b128 v[160:163], v171
	ds_read_b128 v[172:175], v171 offset:1024
	ds_read_b128 v[176:179], v171 offset:2048
	ds_read_b128 v[180:183], v171 offset:3072
	ds_read_b128 v[184:187], v171 offset:4096
	ds_read_b128 v[188:191], v171 offset:5120
	ds_read_b128 v[194:197], v171 offset:6144
	ds_read_b128 v[198:201], v171 offset:7168
	buffer_load_dwordx4 v164, s[36:39], s6 offen lds
	s_mov_b32 m0, s83
	s_nop 0
	buffer_load_dwordx4 v166, s[36:39], s6 offen lds
	s_waitcnt vmcnt(8)
	s_waitcnt lgkmcnt(0)
	s_barrier
	s_setprio 1
	v_mfma_f32_16x16x32_bf16 v[124:127], v[128:131], v[160:163], v[124:127]
	v_mfma_f32_16x16x32_bf16 v[120:123], v[136:139], v[160:163], v[120:123]
	v_mfma_f32_16x16x32_bf16 v[108:111], v[128:131], v[176:179], v[108:111]
	v_mfma_f32_16x16x32_bf16 v[104:107], v[136:139], v[176:179], v[104:107]
	v_mfma_f32_16x16x32_bf16 v[92:95], v[128:131], v[184:187], v[92:95]
	v_mfma_f32_16x16x32_bf16 v[88:91], v[136:139], v[184:187], v[88:91]
	v_mfma_f32_16x16x32_bf16 v[76:79], v[128:131], v[194:197], v[76:79]
	v_mfma_f32_16x16x32_bf16 v[72:75], v[136:139], v[194:197], v[72:75]
	v_mfma_f32_16x16x32_bf16 v[124:127], v[132:135], v[172:175], v[124:127]
	v_mfma_f32_16x16x32_bf16 v[120:123], v[140:143], v[172:175], v[120:123]
	v_mfma_f32_16x16x32_bf16 v[108:111], v[132:135], v[180:183], v[108:111]
	v_mfma_f32_16x16x32_bf16 v[104:107], v[140:143], v[180:183], v[104:107]
	v_mfma_f32_16x16x32_bf16 v[92:95], v[132:135], v[188:191], v[92:95]
	v_mfma_f32_16x16x32_bf16 v[88:91], v[140:143], v[188:191], v[88:91]
	v_mfma_f32_16x16x32_bf16 v[76:79], v[132:135], v[198:201], v[76:79]
	v_mfma_f32_16x16x32_bf16 v[72:75], v[140:143], v[198:201], v[72:75]
	v_mfma_f32_16x16x32_bf16 v[116:119], v[144:147], v[160:163], v[116:119]
	v_mfma_f32_16x16x32_bf16 v[112:115], v[152:155], v[160:163], v[112:115]
	v_mfma_f32_16x16x32_bf16 v[100:103], v[144:147], v[176:179], v[100:103]
	v_mfma_f32_16x16x32_bf16 v[96:99], v[152:155], v[176:179], v[96:99]
	v_mfma_f32_16x16x32_bf16 v[84:87], v[144:147], v[184:187], v[84:87]
	v_mfma_f32_16x16x32_bf16 v[80:83], v[152:155], v[184:187], v[80:83]
	v_mfma_f32_16x16x32_bf16 v[68:71], v[144:147], v[194:197], v[68:71]
	v_mfma_f32_16x16x32_bf16 v[64:67], v[152:155], v[194:197], v[64:67]
	v_mfma_f32_16x16x32_bf16 v[116:119], v[148:151], v[172:175], v[116:119]
	v_mfma_f32_16x16x32_bf16 v[112:115], v[156:159], v[172:175], v[112:115]
	v_mfma_f32_16x16x32_bf16 v[100:103], v[148:151], v[180:183], v[100:103]
	v_mfma_f32_16x16x32_bf16 v[96:99], v[156:159], v[180:183], v[96:99]
	v_mfma_f32_16x16x32_bf16 v[84:87], v[148:151], v[188:191], v[84:87]
	v_mfma_f32_16x16x32_bf16 v[80:83], v[156:159], v[188:191], v[80:83]
	v_mfma_f32_16x16x32_bf16 v[68:71], v[148:151], v[198:201], v[68:71]
	v_mfma_f32_16x16x32_bf16 v[64:67], v[156:159], v[198:201], v[64:67]
	s_setprio 0
	s_barrier
	s_mov_b32 m0, s42
	s_mov_b32 s6, s38
	s_mov_b32 s7, s39
	ds_read_b128 v[160:163], v171 offset:16384
	ds_read_b128 v[172:175], v171 offset:17408
	ds_read_b128 v[176:179], v171 offset:18432
	ds_read_b128 v[180:183], v171 offset:19456
	ds_read_b128 v[184:187], v171 offset:20480
	ds_read_b128 v[188:191], v171 offset:21504
	ds_read_b128 v[194:197], v171 offset:22528
	ds_read_b128 v[198:201], v171 offset:23552
	buffer_load_dwordx4 v165, s[4:7], s31 offen lds
	s_mov_b32 m0, s43
	s_add_i32 s47, s31, s33
	buffer_load_dwordx4 v167, s[4:7], s31 offen lds
	s_mov_b32 m0, s44
	s_nop 0
	buffer_load_dwordx4 v165, s[4:7], s47 offen lds
	s_mov_b32 m0, s45
	s_nop 0
	buffer_load_dwordx4 v167, s[4:7], s47 offen lds
	s_mov_b32 m0, s41
	s_nop 0
	buffer_load_dwordx4 v164, s[36:39], s46 offen lds
	s_mov_b32 m0, s52
	s_nop 0
	buffer_load_dwordx4 v166, s[36:39], s46 offen lds
	s_waitcnt vmcnt(8)
	s_waitcnt lgkmcnt(0)
	s_barrier
	s_setprio 1
	v_mfma_f32_16x16x32_bf16 v[60:63], v[128:131], v[160:163], v[60:63]
	v_mfma_f32_16x16x32_bf16 v[56:59], v[136:139], v[160:163], v[56:59]
	v_mfma_f32_16x16x32_bf16 v[44:47], v[128:131], v[176:179], v[44:47]
	v_mfma_f32_16x16x32_bf16 v[40:43], v[136:139], v[176:179], v[40:43]
	v_mfma_f32_16x16x32_bf16 v[28:31], v[128:131], v[184:187], v[28:31]
	v_mfma_f32_16x16x32_bf16 v[24:27], v[136:139], v[184:187], v[24:27]
	v_mfma_f32_16x16x32_bf16 v[12:15], v[128:131], v[194:197], v[12:15]
	v_mfma_f32_16x16x32_bf16 v[8:11], v[136:139], v[194:197], v[8:11]
	v_mfma_f32_16x16x32_bf16 v[60:63], v[132:135], v[172:175], v[60:63]
	v_mfma_f32_16x16x32_bf16 v[56:59], v[140:143], v[172:175], v[56:59]
	v_mfma_f32_16x16x32_bf16 v[44:47], v[132:135], v[180:183], v[44:47]
	v_mfma_f32_16x16x32_bf16 v[40:43], v[140:143], v[180:183], v[40:43]
	v_mfma_f32_16x16x32_bf16 v[28:31], v[132:135], v[188:191], v[28:31]
	v_mfma_f32_16x16x32_bf16 v[24:27], v[140:143], v[188:191], v[24:27]
	v_mfma_f32_16x16x32_bf16 v[12:15], v[132:135], v[198:201], v[12:15]
	v_mfma_f32_16x16x32_bf16 v[8:11], v[140:143], v[198:201], v[8:11]
	v_mfma_f32_16x16x32_bf16 v[52:55], v[144:147], v[160:163], v[52:55]
	v_mfma_f32_16x16x32_bf16 v[48:51], v[152:155], v[160:163], v[48:51]
	v_mfma_f32_16x16x32_bf16 v[36:39], v[144:147], v[176:179], v[36:39]
	v_mfma_f32_16x16x32_bf16 v[32:35], v[152:155], v[176:179], v[32:35]
	v_mfma_f32_16x16x32_bf16 v[20:23], v[144:147], v[184:187], v[20:23]
	v_mfma_f32_16x16x32_bf16 v[16:19], v[152:155], v[184:187], v[16:19]
	v_mfma_f32_16x16x32_bf16 v[4:7], v[144:147], v[194:197], v[4:7]
	v_mfma_f32_16x16x32_bf16 v[0:3], v[152:155], v[194:197], v[0:3]
	v_mfma_f32_16x16x32_bf16 v[52:55], v[148:151], v[172:175], v[52:55]
	v_mfma_f32_16x16x32_bf16 v[48:51], v[156:159], v[172:175], v[48:51]
	v_mfma_f32_16x16x32_bf16 v[36:39], v[148:151], v[180:183], v[36:39]
	v_mfma_f32_16x16x32_bf16 v[32:35], v[156:159], v[180:183], v[32:35]
	v_mfma_f32_16x16x32_bf16 v[20:23], v[148:151], v[188:191], v[20:23]
	v_mfma_f32_16x16x32_bf16 v[16:19], v[156:159], v[188:191], v[16:19]
	v_mfma_f32_16x16x32_bf16 v[4:7], v[148:151], v[198:201], v[4:7]
	v_mfma_f32_16x16x32_bf16 v[0:3], v[156:159], v[198:201], v[0:3]
	s_setprio 0
	s_barrier
; #define PG8_STAGE(bufoff, rs_, soff_, voff) do { _Pragma("unroll") for (int _i = 0; _i < 2; ++_i) \
;         __builtin_amdgcn_raw_ptr_buffer_load_lds(rs_, (LAS void*)(lds + (bufoff) + ldsw + _i * 8192), 16, (int)(voff)[_i], (int)(soff_), 0, 0); } while (0)
; #define PG8_LDA(dst, b, h) do { _Pragma("unroll") for (int m = 0; m < 4; ++m) dst[m] = PG8_LD2(lds + PG8_SA(b, h) + aoff + m * 2048); } while (0)
; #define PG8_LDB(dst, b, h) do { _Pragma("unroll") for (int n = 0; n < 2; ++n) dst[n] = PG8_LD2(lds + PG8_SB(b, h) + boff + n * 2048); } while (0)
; #define PG8_WAIT_V(n) asm volatile("s_waitcnt vmcnt(" #n ")" ::: "memory")
; #define PG8_WAIT_L(n) asm volatile("s_waitcnt lgkmcnt(" #n ")" ::: "memory")
; #define PG8_BAR __builtin_amdgcn_s_barrier()
; #define PG8_SCHED __builtin_amdgcn_sched_barrier(0)
; template <class Epi, class Sched, bool ALIGN_EPI = false, bool SP2 = false, bool FP8 = false>
; __device__ __forceinline__ void gemm_phase(LAS unsigned char* lds, const Gemm g, const Sched& S, const Epi& E, int wbase) {
;     ...
;             PG8_LDB(B0, 1, 0); PG8_LDB(B1, 1, 1); PG8_SCHED; PG8_LDA(At, 1, 0); PG8_STAGE(PG8_SA(0, 1), rA2, a2 + hstep, voffA);
;             PG8_WAIT_V(8); PG8_WAIT_L(0); PG8_BAR; PG8_MMA(0, 0, At, B0); PG8_MMA(0, 1, At, B1); PG8_BAR; PG8_SCHED;
;             PG8_LDA(At, 1, 1); PG8_STAGE(PG8_SB(1, 0), rB2, b3, voffB); PG8_STAGE(PG8_SB(1, 1), rB2, b3 + hstep, voffB); PG8_STAGE(PG8_SA(1, 0), rA2, a3, voffA);
;             PG8_WAIT_V(8); PG8_WAIT_L(0); PG8_BAR; PG8_MMA(1, 0, At, B0); PG8_MMA(1, 1, At, B1); PG8_BAR; PG8_SCHED;
	v_add_u32_e32 v140, 0x18000, v170
	v_add_u32_e32 v156, 0x1c000, v170
	ds_read_b128 v[128:131], v140
	ds_read_b128 v[132:135], v140 offset:1024
	ds_read_b128 v[136:139], v140 offset:2048
	ds_read_b128 v[140:143], v140 offset:3072
	ds_read_b128 v[144:147], v156
	ds_read_b128 v[148:151], v156 offset:1024
	ds_read_b128 v[152:155], v156 offset:2048
	ds_read_b128 v[156:159], v156 offset:3072
	s_add_i32 s46, s46, s33
	s_mov_b32 m0, s53
	ds_read_b128 v[160:163], v171 offset:32768
	ds_read_b128 v[172:175], v171 offset:33792
	ds_read_b128 v[176:179], v171 offset:34816
	ds_read_b128 v[180:183], v171 offset:35840
	ds_read_b128 v[184:187], v171 offset:36864
	ds_read_b128 v[188:191], v171 offset:37888
	ds_read_b128 v[194:197], v171 offset:38912
	ds_read_b128 v[198:201], v171 offset:39936
	buffer_load_dwordx4 v164, s[36:39], s46 offen lds
	s_mov_b32 m0, s1
	s_nop 0
	buffer_load_dwordx4 v166, s[36:39], s46 offen lds
	s_waitcnt vmcnt(8)
	s_waitcnt lgkmcnt(0)
	s_barrier
	s_setprio 1
	v_mfma_f32_16x16x32_bf16 v[124:127], v[128:131], v[160:163], v[124:127]
	v_mfma_f32_16x16x32_bf16 v[120:123], v[136:139], v[160:163], v[120:123]
	v_mfma_f32_16x16x32_bf16 v[108:111], v[128:131], v[176:179], v[108:111]
	v_mfma_f32_16x16x32_bf16 v[104:107], v[136:139], v[176:179], v[104:107]
	v_mfma_f32_16x16x32_bf16 v[92:95], v[128:131], v[184:187], v[92:95]
	v_mfma_f32_16x16x32_bf16 v[88:91], v[136:139], v[184:187], v[88:91]
	v_mfma_f32_16x16x32_bf16 v[76:79], v[128:131], v[194:197], v[76:79]
	v_mfma_f32_16x16x32_bf16 v[72:75], v[136:139], v[194:197], v[72:75]
	v_mfma_f32_16x16x32_bf16 v[124:127], v[132:135], v[172:175], v[124:127]
	v_mfma_f32_16x16x32_bf16 v[120:123], v[140:143], v[172:175], v[120:123]
	v_mfma_f32_16x16x32_bf16 v[108:111], v[132:135], v[180:183], v[108:111]
	v_mfma_f32_16x16x32_bf16 v[104:107], v[140:143], v[180:183], v[104:107]
	v_mfma_f32_16x16x32_bf16 v[92:95], v[132:135], v[188:191], v[92:95]
	v_mfma_f32_16x16x32_bf16 v[88:91], v[140:143], v[188:191], v[88:91]
	v_mfma_f32_16x16x32_bf16 v[76:79], v[132:135], v[198:201], v[76:79]
	v_mfma_f32_16x16x32_bf16 v[72:75], v[140:143], v[198:201], v[72:75]
	v_mfma_f32_16x16x32_bf16 v[116:119], v[144:147], v[160:163], v[116:119]
	v_mfma_f32_16x16x32_bf16 v[112:115], v[152:155], v[160:163], v[112:115]
	v_mfma_f32_16x16x32_bf16 v[100:103], v[144:147], v[176:179], v[100:103]
	v_mfma_f32_16x16x32_bf16 v[96:99], v[152:155], v[176:179], v[96:99]
	v_mfma_f32_16x16x32_bf16 v[84:87], v[144:147], v[184:187], v[84:87]
	v_mfma_f32_16x16x32_bf16 v[80:83], v[152:155], v[184:187], v[80:83]
	v_mfma_f32_16x16x32_bf16 v[68:71], v[144:147], v[194:197], v[68:71]
	v_mfma_f32_16x16x32_bf16 v[64:67], v[152:155], v[194:197], v[64:67]
	v_mfma_f32_16x16x32_bf16 v[116:119], v[148:151], v[172:175], v[116:119]
	v_mfma_f32_16x16x32_bf16 v[112:115], v[156:159], v[172:175], v[112:115]
	v_mfma_f32_16x16x32_bf16 v[100:103], v[148:151], v[180:183], v[100:103]
	v_mfma_f32_16x16x32_bf16 v[96:99], v[156:159], v[180:183], v[96:99]
	v_mfma_f32_16x16x32_bf16 v[84:87], v[148:151], v[188:191], v[84:87]
	v_mfma_f32_16x16x32_bf16 v[80:83], v[156:159], v[188:191], v[80:83]
	v_mfma_f32_16x16x32_bf16 v[68:71], v[148:151], v[198:201], v[68:71]
	v_mfma_f32_16x16x32_bf16 v[64:67], v[156:159], v[198:201], v[64:67]
	s_setprio 0
	s_barrier
	s_mov_b32 m0, s56
	s_bitset1_b32 s31, 7
	ds_read_b128 v[160:163], v171 offset:49152
	ds_read_b128 v[172:175], v171 offset:50176
	ds_read_b128 v[176:179], v171 offset:51200
	ds_read_b128 v[180:183], v171 offset:52224
	ds_read_b128 v[184:187], v171 offset:53248
	ds_read_b128 v[188:191], v171 offset:54272
	ds_read_b128 v[194:197], v171 offset:55296
	ds_read_b128 v[198:201], v171 offset:56320
	buffer_load_dwordx4 v165, s[4:7], s31 offen lds
	s_mov_b32 m0, s57
	s_nop 0
	buffer_load_dwordx4 v167, s[4:7], s31 offen lds
	s_add_i32 s31, s31, s33
	s_mov_b32 m0, s65
	s_nop 0
	buffer_load_dwordx4 v165, s[4:7], s31 offen lds
	s_mov_b32 m0, s76
	s_nop 0
	buffer_load_dwordx4 v167, s[4:7], s31 offen lds
	s_mov_b32 m0, s58
	s_nop 0
	buffer_load_dwordx4 v164, s[36:39], s30 offen lds
	s_mov_b32 m0, s59
	s_nop 0
	buffer_load_dwordx4 v166, s[36:39], s30 offen lds
	s_waitcnt vmcnt(8)
	s_waitcnt lgkmcnt(0)
	s_barrier
	s_setprio 1
	v_mfma_f32_16x16x32_bf16 v[60:63], v[128:131], v[160:163], v[60:63]
	v_mfma_f32_16x16x32_bf16 v[56:59], v[136:139], v[160:163], v[56:59]
	v_mfma_f32_16x16x32_bf16 v[44:47], v[128:131], v[176:179], v[44:47]
	v_mfma_f32_16x16x32_bf16 v[40:43], v[136:139], v[176:179], v[40:43]
	v_mfma_f32_16x16x32_bf16 v[28:31], v[128:131], v[184:187], v[28:31]
	v_mfma_f32_16x16x32_bf16 v[24:27], v[136:139], v[184:187], v[24:27]
	v_mfma_f32_16x16x32_bf16 v[12:15], v[128:131], v[194:197], v[12:15]
	v_mfma_f32_16x16x32_bf16 v[8:11], v[136:139], v[194:197], v[8:11]
	v_mfma_f32_16x16x32_bf16 v[60:63], v[132:135], v[172:175], v[60:63]
	v_mfma_f32_16x16x32_bf16 v[56:59], v[140:143], v[172:175], v[56:59]
	v_mfma_f32_16x16x32_bf16 v[44:47], v[132:135], v[180:183], v[44:47]
	v_mfma_f32_16x16x32_bf16 v[40:43], v[140:143], v[180:183], v[40:43]
	v_mfma_f32_16x16x32_bf16 v[28:31], v[132:135], v[188:191], v[28:31]
	v_mfma_f32_16x16x32_bf16 v[24:27], v[140:143], v[188:191], v[24:27]
	v_mfma_f32_16x16x32_bf16 v[12:15], v[132:135], v[198:201], v[12:15]
	v_mfma_f32_16x16x32_bf16 v[8:11], v[140:143], v[198:201], v[8:11]
	v_mfma_f32_16x16x32_bf16 v[52:55], v[144:147], v[160:163], v[52:55]
	v_mfma_f32_16x16x32_bf16 v[48:51], v[152:155], v[160:163], v[48:51]
	v_mfma_f32_16x16x32_bf16 v[36:39], v[144:147], v[176:179], v[36:39]
	v_mfma_f32_16x16x32_bf16 v[32:35], v[152:155], v[176:179], v[32:35]
	v_mfma_f32_16x16x32_bf16 v[20:23], v[144:147], v[184:187], v[20:23]
	v_mfma_f32_16x16x32_bf16 v[16:19], v[152:155], v[184:187], v[16:19]
	v_mfma_f32_16x16x32_bf16 v[4:7], v[144:147], v[194:197], v[4:7]
	v_mfma_f32_16x16x32_bf16 v[0:3], v[152:155], v[194:197], v[0:3]
	v_mfma_f32_16x16x32_bf16 v[52:55], v[148:151], v[172:175], v[52:55]
	v_mfma_f32_16x16x32_bf16 v[48:51], v[156:159], v[172:175], v[48:51]
	v_mfma_f32_16x16x32_bf16 v[36:39], v[148:151], v[180:183], v[36:39]
	v_mfma_f32_16x16x32_bf16 v[32:35], v[156:159], v[180:183], v[32:35]
	v_mfma_f32_16x16x32_bf16 v[20:23], v[148:151], v[188:191], v[20:23]
	v_mfma_f32_16x16x32_bf16 v[16:19], v[156:159], v[188:191], v[16:19]
	v_mfma_f32_16x16x32_bf16 v[4:7], v[148:151], v[198:201], v[4:7]
	v_mfma_f32_16x16x32_bf16 v[0:3], v[156:159], v[198:201], v[0:3]
	s_setprio 0
	s_barrier
	s_add_i32 s29, s29, 2
	s_addk_i32 s16, 0x100
	s_addk_i32 s28, 0x100
	s_cmp_ge_i32 s29, s82
	s_cbranch_scc0 .LBB0_352
	s_and_b64 vcc, exec, s[78:79]
	s_cbranch_vccz .LBB0_355

; #define PG8_STAGE(bufoff, rs_, soff_, voff) do { _Pragma("unroll") for (int _i = 0; _i < 2; ++_i) \
;         __builtin_amdgcn_raw_ptr_buffer_load_lds(rs_, (LAS void*)(lds + (bufoff) + ldsw + _i * 8192), 16, (int)(voff)[_i], (int)(soff_), 0, 0); } while (0)
; #define PG8_LDA(dst, b, h) do { _Pragma("unroll") for (int m = 0; m < 4; ++m) dst[m] = PG8_LD2(lds + PG8_SA(b, h) + aoff + m * 2048); } while (0)
; #define PG8_LDB(dst, b, h) do { _Pragma("unroll") for (int n = 0; n < 2; ++n) dst[n] = PG8_LD2(lds + PG8_SB(b, h) + boff + n * 2048); } while (0)
; #define PG8_WAIT_V(n) asm volatile("s_waitcnt vmcnt(" #n ")" ::: "memory")
; #define PG8_WAIT_L(n) asm volatile("s_waitcnt lgkmcnt(" #n ")" ::: "memory")
; #define PG8_BAR __builtin_amdgcn_s_barrier()
; #define PG8_SCHED __builtin_amdgcn_sched_barrier(0)
; template <class Epi, class Sched, bool ALIGN_EPI = false, bool SP2 = false, bool FP8 = false>
; __device__ __forceinline__ void gemm_phase(LAS unsigned char* lds, const Gemm g, const Sched& S, const Epi& E, int wbase) {
;     ...
;             PG8_LDB(B0, 0, 0); PG8_LDB(B1, 0, 1); PG8_SCHED; PG8_LDA(At, 0, 0); PG8_STAGE(PG8_SA(1, 1), rAc, a1 + hstep, voffA);
;             PG8_WAIT_V(8); PG8_WAIT_L(0); PG8_BAR; PG8_MMA(0, 0, At, B0); PG8_MMA(0, 1, At, B1); PG8_BAR; PG8_SCHED;
;             PG8_LDA(At, 0, 1); PG8_STAGE(PG8_SB(0, 0), rB2, b2, voffB); PG8_STAGE(PG8_SB(0, 1), rB2, b2 + hstep, voffB); PG8_STAGE(PG8_SA(0, 0), rA2, a2, voffA);
;             PG8_WAIT_V(8); PG8_WAIT_L(0); PG8_BAR; PG8_MMA(1, 0, At, B0); PG8_MMA(1, 1, At, B1); PG8_BAR; PG8_SCHED;
.LBB0_450:
	v_add_u32_e32 v148, 0x10000, v138
	v_add_u32_e32 v164, 0x14000, v138
	ds_read_b128 v[128:131], v148
	ds_read_b128 v[140:143], v148 offset:1024
	ds_read_b128 v[144:147], v148 offset:2048
	ds_read_b128 v[148:151], v148 offset:3072
	ds_read_b128 v[152:155], v164
	ds_read_b128 v[156:159], v164 offset:1024
	ds_read_b128 v[160:163], v164 offset:2048
	ds_read_b128 v[164:167], v164 offset:3072
	s_add_i32 s6, s58, 0x80
	s_cmp_eq_u32 s42, s60
	s_cselect_b32 s61, s56, s6
	s_cselect_b32 s55, s57, s59
	s_or_b32 s54, s61, 0x80
	s_add_i32 s6, s19, s58
	s_mov_b32 m0, s43
	ds_read_b128 v[168:171], v139
	ds_read_b128 v[172:175], v139 offset:1024
	ds_read_b128 v[176:179], v139 offset:2048
	ds_read_b128 v[180:183], v139 offset:3072
	ds_read_b128 v[184:187], v139 offset:4096
	ds_read_b128 v[188:191], v139 offset:5120
	ds_read_b128 v[194:197], v139 offset:6144
	ds_read_b128 v[198:201], v139 offset:7168
	buffer_load_dwordx4 v132, s[36:39], s6 offen lds
	s_mov_b32 m0, s44
	s_nop 0
	buffer_load_dwordx4 v134, s[36:39], s6 offen lds
	s_waitcnt vmcnt(8)
	s_waitcnt lgkmcnt(0)
	s_barrier
	s_setprio 1
	v_mfma_f32_16x16x32_bf16 v[124:127], v[128:131], v[168:171], v[124:127]
	v_mfma_f32_16x16x32_bf16 v[120:123], v[144:147], v[168:171], v[120:123]
	v_mfma_f32_16x16x32_bf16 v[108:111], v[128:131], v[176:179], v[108:111]
	v_mfma_f32_16x16x32_bf16 v[104:107], v[144:147], v[176:179], v[104:107]
	v_mfma_f32_16x16x32_bf16 v[92:95], v[128:131], v[184:187], v[92:95]
	v_mfma_f32_16x16x32_bf16 v[88:91], v[144:147], v[184:187], v[88:91]
	v_mfma_f32_16x16x32_bf16 v[76:79], v[128:131], v[194:197], v[76:79]
	v_mfma_f32_16x16x32_bf16 v[72:75], v[144:147], v[194:197], v[72:75]
	v_mfma_f32_16x16x32_bf16 v[124:127], v[140:143], v[172:175], v[124:127]
	v_mfma_f32_16x16x32_bf16 v[120:123], v[148:151], v[172:175], v[120:123]
	v_mfma_f32_16x16x32_bf16 v[108:111], v[140:143], v[180:183], v[108:111]
	v_mfma_f32_16x16x32_bf16 v[104:107], v[148:151], v[180:183], v[104:107]
	v_mfma_f32_16x16x32_bf16 v[92:95], v[140:143], v[188:191], v[92:95]
	v_mfma_f32_16x16x32_bf16 v[88:91], v[148:151], v[188:191], v[88:91]
	v_mfma_f32_16x16x32_bf16 v[76:79], v[140:143], v[198:201], v[76:79]
	v_mfma_f32_16x16x32_bf16 v[72:75], v[148:151], v[198:201], v[72:75]
	v_mfma_f32_16x16x32_bf16 v[116:119], v[152:155], v[168:171], v[116:119]
	v_mfma_f32_16x16x32_bf16 v[112:115], v[160:163], v[168:171], v[112:115]
	v_mfma_f32_16x16x32_bf16 v[100:103], v[152:155], v[176:179], v[100:103]
	v_mfma_f32_16x16x32_bf16 v[96:99], v[160:163], v[176:179], v[96:99]
	v_mfma_f32_16x16x32_bf16 v[84:87], v[152:155], v[184:187], v[84:87]
	v_mfma_f32_16x16x32_bf16 v[80:83], v[160:163], v[184:187], v[80:83]
	v_mfma_f32_16x16x32_bf16 v[68:71], v[152:155], v[194:197], v[68:71]
	v_mfma_f32_16x16x32_bf16 v[64:67], v[160:163], v[194:197], v[64:67]
	v_mfma_f32_16x16x32_bf16 v[116:119], v[156:159], v[172:175], v[116:119]
	v_mfma_f32_16x16x32_bf16 v[112:115], v[164:167], v[172:175], v[112:115]
	v_mfma_f32_16x16x32_bf16 v[100:103], v[156:159], v[180:183], v[100:103]
	v_mfma_f32_16x16x32_bf16 v[96:99], v[164:167], v[180:183], v[96:99]
	v_mfma_f32_16x16x32_bf16 v[84:87], v[156:159], v[188:191], v[84:87]
	v_mfma_f32_16x16x32_bf16 v[80:83], v[164:167], v[188:191], v[80:83]
	v_mfma_f32_16x16x32_bf16 v[68:71], v[156:159], v[198:201], v[68:71]
	v_mfma_f32_16x16x32_bf16 v[64:67], v[164:167], v[198:201], v[64:67]
	s_setprio 0
	s_barrier
	s_mov_b32 m0, s21
	s_mov_b32 s6, s38
	s_mov_b32 s7, s39
	ds_read_b128 v[168:171], v139 offset:16384
	ds_read_b128 v[172:175], v139 offset:17408
	ds_read_b128 v[176:179], v139 offset:18432
	ds_read_b128 v[180:183], v139 offset:19456
	ds_read_b128 v[184:187], v139 offset:20480
	ds_read_b128 v[188:191], v139 offset:21504
	ds_read_b128 v[194:197], v139 offset:22528
	ds_read_b128 v[198:201], v139 offset:23552
	buffer_load_dwordx4 v133, s[4:7], s55 offen lds
	s_mov_b32 m0, s22
	s_add_i32 s62, s55, s19
	buffer_load_dwordx4 v135, s[4:7], s55 offen lds
	s_mov_b32 m0, s23
	s_nop 0
	buffer_load_dwordx4 v133, s[4:7], s62 offen lds
	s_mov_b32 m0, s24
	s_nop 0
	buffer_load_dwordx4 v135, s[4:7], s62 offen lds
	s_mov_b32 m0, s20
	s_nop 0
	buffer_load_dwordx4 v132, s[36:39], s61 offen lds
	s_mov_b32 m0, s25
	s_nop 0
	buffer_load_dwordx4 v134, s[36:39], s61 offen lds
	s_waitcnt vmcnt(8)
	s_waitcnt lgkmcnt(0)
	s_barrier
	s_setprio 1
	v_mfma_f32_16x16x32_bf16 v[60:63], v[128:131], v[168:171], v[60:63]
	v_mfma_f32_16x16x32_bf16 v[56:59], v[144:147], v[168:171], v[56:59]
	v_mfma_f32_16x16x32_bf16 v[44:47], v[128:131], v[176:179], v[44:47]
	v_mfma_f32_16x16x32_bf16 v[40:43], v[144:147], v[176:179], v[40:43]
	v_mfma_f32_16x16x32_bf16 v[28:31], v[128:131], v[184:187], v[28:31]
	v_mfma_f32_16x16x32_bf16 v[24:27], v[144:147], v[184:187], v[24:27]
	v_mfma_f32_16x16x32_bf16 v[12:15], v[128:131], v[194:197], v[12:15]
	v_mfma_f32_16x16x32_bf16 v[8:11], v[144:147], v[194:197], v[8:11]
	v_mfma_f32_16x16x32_bf16 v[60:63], v[140:143], v[172:175], v[60:63]
	v_mfma_f32_16x16x32_bf16 v[56:59], v[148:151], v[172:175], v[56:59]
	v_mfma_f32_16x16x32_bf16 v[44:47], v[140:143], v[180:183], v[44:47]
	v_mfma_f32_16x16x32_bf16 v[40:43], v[148:151], v[180:183], v[40:43]
	v_mfma_f32_16x16x32_bf16 v[28:31], v[140:143], v[188:191], v[28:31]
	v_mfma_f32_16x16x32_bf16 v[24:27], v[148:151], v[188:191], v[24:27]
	v_mfma_f32_16x16x32_bf16 v[12:15], v[140:143], v[198:201], v[12:15]
	v_mfma_f32_16x16x32_bf16 v[8:11], v[148:151], v[198:201], v[8:11]
	v_mfma_f32_16x16x32_bf16 v[52:55], v[152:155], v[168:171], v[52:55]
	v_mfma_f32_16x16x32_bf16 v[48:51], v[160:163], v[168:171], v[48:51]
	v_mfma_f32_16x16x32_bf16 v[36:39], v[152:155], v[176:179], v[36:39]
	v_mfma_f32_16x16x32_bf16 v[32:35], v[160:163], v[176:179], v[32:35]
	v_mfma_f32_16x16x32_bf16 v[20:23], v[152:155], v[184:187], v[20:23]
	v_mfma_f32_16x16x32_bf16 v[16:19], v[160:163], v[184:187], v[16:19]
	v_mfma_f32_16x16x32_bf16 v[4:7], v[152:155], v[194:197], v[4:7]
	v_mfma_f32_16x16x32_bf16 v[0:3], v[160:163], v[194:197], v[0:3]
	v_mfma_f32_16x16x32_bf16 v[52:55], v[156:159], v[172:175], v[52:55]
	v_mfma_f32_16x16x32_bf16 v[48:51], v[164:167], v[172:175], v[48:51]
	v_mfma_f32_16x16x32_bf16 v[36:39], v[156:159], v[180:183], v[36:39]
	v_mfma_f32_16x16x32_bf16 v[32:35], v[164:167], v[180:183], v[32:35]
	v_mfma_f32_16x16x32_bf16 v[20:23], v[156:159], v[188:191], v[20:23]
	v_mfma_f32_16x16x32_bf16 v[16:19], v[164:167], v[188:191], v[16:19]
	v_mfma_f32_16x16x32_bf16 v[4:7], v[156:159], v[198:201], v[4:7]
	v_mfma_f32_16x16x32_bf16 v[0:3], v[164:167], v[198:201], v[0:3]
	s_setprio 0
	s_barrier
; #define PG8_STAGE(bufoff, rs_, soff_, voff) do { _Pragma("unroll") for (int _i = 0; _i < 2; ++_i) \
;         __builtin_amdgcn_raw_ptr_buffer_load_lds(rs_, (LAS void*)(lds + (bufoff) + ldsw + _i * 8192), 16, (int)(voff)[_i], (int)(soff_), 0, 0); } while (0)
; #define PG8_LDA(dst, b, h) do { _Pragma("unroll") for (int m = 0; m < 4; ++m) dst[m] = PG8_LD2(lds + PG8_SA(b, h) + aoff + m * 2048); } while (0)
; #define PG8_LDB(dst, b, h) do { _Pragma("unroll") for (int n = 0; n < 2; ++n) dst[n] = PG8_LD2(lds + PG8_SB(b, h) + boff + n * 2048); } while (0)
; #define PG8_WAIT_V(n) asm volatile("s_waitcnt vmcnt(" #n ")" ::: "memory")
; #define PG8_WAIT_L(n) asm volatile("s_waitcnt lgkmcnt(" #n ")" ::: "memory")
; #define PG8_BAR __builtin_amdgcn_s_barrier()
; #define PG8_SCHED __builtin_amdgcn_sched_barrier(0)
; template <class Epi, class Sched, bool ALIGN_EPI = false, bool SP2 = false, bool FP8 = false>
; __device__ __forceinline__ void gemm_phase(LAS unsigned char* lds, const Gemm g, const Sched& S, const Epi& E, int wbase) {
;     ...
;             PG8_LDB(B0, 1, 0); PG8_LDB(B1, 1, 1); PG8_SCHED; PG8_LDA(At, 1, 0); PG8_STAGE(PG8_SA(0, 1), rA2, a2 + hstep, voffA);
;             PG8_WAIT_V(8); PG8_WAIT_L(0); PG8_BAR; PG8_MMA(0, 0, At, B0); PG8_MMA(0, 1, At, B1); PG8_BAR; PG8_SCHED;
;             PG8_LDA(At, 1, 1); PG8_STAGE(PG8_SB(1, 0), rB2, b3, voffB); PG8_STAGE(PG8_SB(1, 1), rB2, b3 + hstep, voffB); PG8_STAGE(PG8_SA(1, 0), rA2, a3, voffA);
;             PG8_WAIT_V(8); PG8_WAIT_L(0); PG8_BAR; PG8_MMA(1, 0, At, B0); PG8_MMA(1, 1, At, B1); PG8_BAR; PG8_SCHED;
	v_add_u32_e32 v148, 0x18000, v138
	v_add_u32_e32 v164, 0x1c000, v138
	ds_read_b128 v[128:131], v148
	ds_read_b128 v[140:143], v148 offset:1024
	ds_read_b128 v[144:147], v148 offset:2048
	ds_read_b128 v[148:151], v148 offset:3072
	ds_read_b128 v[152:155], v164
	ds_read_b128 v[156:159], v164 offset:1024
	ds_read_b128 v[160:163], v164 offset:2048
	ds_read_b128 v[164:167], v164 offset:3072
	s_add_i32 s61, s61, s19
	s_mov_b32 m0, s26
	ds_read_b128 v[168:171], v139 offset:32768
	ds_read_b128 v[172:175], v139 offset:33792
	ds_read_b128 v[176:179], v139 offset:34816
	ds_read_b128 v[180:183], v139 offset:35840
	ds_read_b128 v[184:187], v139 offset:36864
	ds_read_b128 v[188:191], v139 offset:37888
	ds_read_b128 v[194:197], v139 offset:38912
	ds_read_b128 v[198:201], v139 offset:39936
	buffer_load_dwordx4 v132, s[36:39], s61 offen lds
	s_mov_b32 m0, s27
	s_nop 0
	buffer_load_dwordx4 v134, s[36:39], s61 offen lds
	s_waitcnt vmcnt(8)
	s_waitcnt lgkmcnt(0)
	s_barrier
	s_setprio 1
	v_mfma_f32_16x16x32_bf16 v[124:127], v[128:131], v[168:171], v[124:127]
	v_mfma_f32_16x16x32_bf16 v[120:123], v[144:147], v[168:171], v[120:123]
	v_mfma_f32_16x16x32_bf16 v[108:111], v[128:131], v[176:179], v[108:111]
	v_mfma_f32_16x16x32_bf16 v[104:107], v[144:147], v[176:179], v[104:107]
	v_mfma_f32_16x16x32_bf16 v[92:95], v[128:131], v[184:187], v[92:95]
	v_mfma_f32_16x16x32_bf16 v[88:91], v[144:147], v[184:187], v[88:91]
	v_mfma_f32_16x16x32_bf16 v[76:79], v[128:131], v[194:197], v[76:79]
	v_mfma_f32_16x16x32_bf16 v[72:75], v[144:147], v[194:197], v[72:75]
	v_mfma_f32_16x16x32_bf16 v[124:127], v[140:143], v[172:175], v[124:127]
	v_mfma_f32_16x16x32_bf16 v[120:123], v[148:151], v[172:175], v[120:123]
	v_mfma_f32_16x16x32_bf16 v[108:111], v[140:143], v[180:183], v[108:111]
	v_mfma_f32_16x16x32_bf16 v[104:107], v[148:151], v[180:183], v[104:107]
	v_mfma_f32_16x16x32_bf16 v[92:95], v[140:143], v[188:191], v[92:95]
	v_mfma_f32_16x16x32_bf16 v[88:91], v[148:151], v[188:191], v[88:91]
	v_mfma_f32_16x16x32_bf16 v[76:79], v[140:143], v[198:201], v[76:79]
	v_mfma_f32_16x16x32_bf16 v[72:75], v[148:151], v[198:201], v[72:75]
	v_mfma_f32_16x16x32_bf16 v[116:119], v[152:155], v[168:171], v[116:119]
	v_mfma_f32_16x16x32_bf16 v[112:115], v[160:163], v[168:171], v[112:115]
	v_mfma_f32_16x16x32_bf16 v[100:103], v[152:155], v[176:179], v[100:103]
	v_mfma_f32_16x16x32_bf16 v[96:99], v[160:163], v[176:179], v[96:99]
	v_mfma_f32_16x16x32_bf16 v[84:87], v[152:155], v[184:187], v[84:87]
	v_mfma_f32_16x16x32_bf16 v[80:83], v[160:163], v[184:187], v[80:83]
	v_mfma_f32_16x16x32_bf16 v[68:71], v[152:155], v[194:197], v[68:71]
	v_mfma_f32_16x16x32_bf16 v[64:67], v[160:163], v[194:197], v[64:67]
	v_mfma_f32_16x16x32_bf16 v[116:119], v[156:159], v[172:175], v[116:119]
	v_mfma_f32_16x16x32_bf16 v[112:115], v[164:167], v[172:175], v[112:115]
	v_mfma_f32_16x16x32_bf16 v[100:103], v[156:159], v[180:183], v[100:103]
	v_mfma_f32_16x16x32_bf16 v[96:99], v[164:167], v[180:183], v[96:99]
	v_mfma_f32_16x16x32_bf16 v[84:87], v[156:159], v[188:191], v[84:87]
	v_mfma_f32_16x16x32_bf16 v[80:83], v[164:167], v[188:191], v[80:83]
	v_mfma_f32_16x16x32_bf16 v[68:71], v[156:159], v[198:201], v[68:71]
	v_mfma_f32_16x16x32_bf16 v[64:67], v[164:167], v[198:201], v[64:67]
	s_setprio 0
	s_barrier
	s_mov_b32 m0, s28
	s_bitset1_b32 s55, 7
	ds_read_b128 v[168:171], v139 offset:49152
	ds_read_b128 v[172:175], v139 offset:50176
	ds_read_b128 v[176:179], v139 offset:51200
	ds_read_b128 v[180:183], v139 offset:52224
	ds_read_b128 v[184:187], v139 offset:53248
	ds_read_b128 v[188:191], v139 offset:54272
	ds_read_b128 v[194:197], v139 offset:55296
	ds_read_b128 v[198:201], v139 offset:56320
	buffer_load_dwordx4 v133, s[4:7], s55 offen lds
	s_mov_b32 m0, s29
	s_nop 0
	buffer_load_dwordx4 v135, s[4:7], s55 offen lds
	s_add_i32 s55, s55, s19
	s_mov_b32 m0, s33
	s_nop 0
	buffer_load_dwordx4 v133, s[4:7], s55 offen lds
	s_mov_b32 m0, s34
	s_nop 0
	buffer_load_dwordx4 v135, s[4:7], s55 offen lds
	s_mov_b32 m0, s30
	s_nop 0
	buffer_load_dwordx4 v132, s[36:39], s54 offen lds
	s_mov_b32 m0, s31
	s_nop 0
	buffer_load_dwordx4 v134, s[36:39], s54 offen lds
	s_waitcnt vmcnt(8)
	s_waitcnt lgkmcnt(0)
	s_barrier
	s_setprio 1
	v_mfma_f32_16x16x32_bf16 v[60:63], v[128:131], v[168:171], v[60:63]
	v_mfma_f32_16x16x32_bf16 v[56:59], v[144:147], v[168:171], v[56:59]
	v_mfma_f32_16x16x32_bf16 v[44:47], v[128:131], v[176:179], v[44:47]
	v_mfma_f32_16x16x32_bf16 v[40:43], v[144:147], v[176:179], v[40:43]
	v_mfma_f32_16x16x32_bf16 v[28:31], v[128:131], v[184:187], v[28:31]
	v_mfma_f32_16x16x32_bf16 v[24:27], v[144:147], v[184:187], v[24:27]
	v_mfma_f32_16x16x32_bf16 v[12:15], v[128:131], v[194:197], v[12:15]
	v_mfma_f32_16x16x32_bf16 v[8:11], v[144:147], v[194:197], v[8:11]
	v_mfma_f32_16x16x32_bf16 v[60:63], v[140:143], v[172:175], v[60:63]
	v_mfma_f32_16x16x32_bf16 v[56:59], v[148:151], v[172:175], v[56:59]
	v_mfma_f32_16x16x32_bf16 v[44:47], v[140:143], v[180:183], v[44:47]
	v_mfma_f32_16x16x32_bf16 v[40:43], v[148:151], v[180:183], v[40:43]
	v_mfma_f32_16x16x32_bf16 v[28:31], v[140:143], v[188:191], v[28:31]
	v_mfma_f32_16x16x32_bf16 v[24:27], v[148:151], v[188:191], v[24:27]
	v_mfma_f32_16x16x32_bf16 v[12:15], v[140:143], v[198:201], v[12:15]
	v_mfma_f32_16x16x32_bf16 v[8:11], v[148:151], v[198:201], v[8:11]
	v_mfma_f32_16x16x32_bf16 v[52:55], v[152:155], v[168:171], v[52:55]
	v_mfma_f32_16x16x32_bf16 v[48:51], v[160:163], v[168:171], v[48:51]
	v_mfma_f32_16x16x32_bf16 v[36:39], v[152:155], v[176:179], v[36:39]
	v_mfma_f32_16x16x32_bf16 v[32:35], v[160:163], v[176:179], v[32:35]
	v_mfma_f32_16x16x32_bf16 v[20:23], v[152:155], v[184:187], v[20:23]
	v_mfma_f32_16x16x32_bf16 v[16:19], v[160:163], v[184:187], v[16:19]
	v_mfma_f32_16x16x32_bf16 v[4:7], v[152:155], v[194:197], v[4:7]
	v_mfma_f32_16x16x32_bf16 v[0:3], v[160:163], v[194:197], v[0:3]
	v_mfma_f32_16x16x32_bf16 v[52:55], v[156:159], v[172:175], v[52:55]
	v_mfma_f32_16x16x32_bf16 v[48:51], v[164:167], v[172:175], v[48:51]
	v_mfma_f32_16x16x32_bf16 v[36:39], v[156:159], v[180:183], v[36:39]
	v_mfma_f32_16x16x32_bf16 v[32:35], v[164:167], v[180:183], v[32:35]
	v_mfma_f32_16x16x32_bf16 v[20:23], v[156:159], v[188:191], v[20:23]
	v_mfma_f32_16x16x32_bf16 v[16:19], v[164:167], v[188:191], v[16:19]
	v_mfma_f32_16x16x32_bf16 v[4:7], v[156:159], v[198:201], v[4:7]
	v_mfma_f32_16x16x32_bf16 v[0:3], v[164:167], v[198:201], v[0:3]
	s_setprio 0
	s_barrier
	s_add_i32 s60, s60, 2
	s_addk_i32 s58, 0x100
	s_addk_i32 s59, 0x100
	s_cmp_ge_i32 s60, s35
	s_cbranch_scc0 .LBB0_450
	s_and_b64 vcc, exec, s[12:13]
	s_cbranch_vccz .LBB0_453

; #define PG8_STAGE(bufoff, rs_, soff_, voff) do { _Pragma("unroll") for (int _i = 0; _i < 2; ++_i) \
;         __builtin_amdgcn_raw_ptr_buffer_load_lds(rs_, (LAS void*)(lds + (bufoff) + ldsw + _i * 8192), 16, (int)(voff)[_i], (int)(soff_), 0, 0); } while (0)
; #define PG8_LDA(dst, b, h) do { _Pragma("unroll") for (int m = 0; m < 4; ++m) dst[m] = PG8_LD2(lds + PG8_SA(b, h) + aoff + m * 2048); } while (0)
; #define PG8_LDB(dst, b, h) do { _Pragma("unroll") for (int n = 0; n < 2; ++n) dst[n] = PG8_LD2(lds + PG8_SB(b, h) + boff + n * 2048); } while (0)
; #define PG8_WAIT_V(n) asm volatile("s_waitcnt vmcnt(" #n ")" ::: "memory")
; #define PG8_WAIT_L(n) asm volatile("s_waitcnt lgkmcnt(" #n ")" ::: "memory")
; #define PG8_BAR __builtin_amdgcn_s_barrier()
; #define PG8_SCHED __builtin_amdgcn_sched_barrier(0)
; template <class Epi, class Sched, bool ALIGN_EPI = false, bool SP2 = false, bool FP8 = false>
; __device__ __forceinline__ void gemm_phase(LAS unsigned char* lds, const Gemm g, const Sched& S, const Epi& E, int wbase) {
;     ...
;             const unsigned a2 = last ? nA : cA + (unsigned)(t + 2) * kstep, b2 = last ? nB : cB + (unsigned)(t + 2) * kstep; const rsrc_t rA2 = (Sched::TWO && last) ? rAn : rAc, rB2 = (Sched::TWO && last) ? rBn : rBc;
;             const unsigned a3 = a2 + kstep, b3 = b2 + kstep;
;             if (last && has_next) S.a_ready(nxt);
;             if constexpr (SP2) {
;             PG8_LDB(B0, 0, 0); PG8_LDB(B1, 0, 1); PG8_SCHED; PG8_LDA(At, 0, 0); PG8_STAGE(PG8_SA(1, 1), rAc, a1 + hstep, voffA);
;             PG8_WAIT_V(8); PG8_WAIT_L(0); PG8_BAR; PG8_MMA(0, 0, At, B0); PG8_MMA(0, 1, At, B1); PG8_BAR; PG8_SCHED;
;             PG8_LDA(At, 0, 1); PG8_STAGE(PG8_SB(0, 0), rB2, b2, voffB); PG8_STAGE(PG8_SB(0, 1), rB2, b2 + hstep, voffB); PG8_STAGE(PG8_SA(0, 0), rA2, a2, voffA);
;             PG8_WAIT_V(8); PG8_WAIT_L(0); PG8_BAR; PG8_MMA(1, 0, At, B0); PG8_MMA(1, 1, At, B1); PG8_BAR; PG8_SCHED;
.LBB0_813:
	s_add_i32 s20, vcc_hi, 0x80
	v_add_u32_e32 v140, 0x10000, v240
	v_add_u32_e32 v156, 0x14000, v240
	s_cmp_eq_u32 s41, s78
	ds_read_b128 v[128:131], v140
	ds_read_b128 v[132:135], v140 offset:1024
	ds_read_b128 v[136:139], v140 offset:2048
	ds_read_b128 v[140:143], v140 offset:3072
	ds_read_b128 v[144:147], v156
	ds_read_b128 v[148:151], v156 offset:1024
	ds_read_b128 v[152:155], v156 offset:2048
	ds_read_b128 v[156:159], v156 offset:3072
	s_cselect_b64 s[16:17], -1, 0
	s_and_b64 s[18:19], s[16:17], exec
	s_cselect_b32 s68, s67, s20
	s_cselect_b32 s54, vcc_lo, s3
	s_and_b64 s[20:21], s[44:45], s[16:17]
	s_and_b64 s[16:17], s[20:21], exec
	s_cselect_b32 s18, s52, s14
	s_cselect_b32 s19, s53, s15
	s_cselect_b32 s17, s35, s13
	s_cselect_b32 s16, s34, s12
	s_or_b32 s55, s68, 0x80
	s_and_b64 s[20:21], s[20:21], exec
	s_cselect_b32 s23, s53, s31
	s_cselect_b32 s22, s52, s30
	s_cselect_b32 s21, s11, s59
	s_cselect_b32 s20, s10, s58
	s_add_i32 s69, s46, vcc_hi
	s_mov_b32 m0, s61
	ds_read_b128 v[160:163], v241
	ds_read_b128 v[164:167], v241 offset:1024
	ds_read_b128 v[168:171], v241 offset:2048
	ds_read_b128 v[172:175], v241 offset:3072
	ds_read_b128 v[176:179], v241 offset:4096
	ds_read_b128 v[180:183], v241 offset:5120
	ds_read_b128 v[184:187], v241 offset:6144
	ds_read_b128 v[188:191], v241 offset:7168
	buffer_load_dwordx4 v192, s[12:15], s69 offen lds
	s_mov_b32 m0, s62
	s_nop 0
	buffer_load_dwordx4 v236, s[12:15], s69 offen lds
	s_waitcnt vmcnt(8)
	s_waitcnt lgkmcnt(0)
	s_barrier
	s_setprio 1
	v_mfma_f32_16x16x128_f8f6f4 v[124:127], v[128:135], v[160:167], v[124:127]
	v_mfma_f32_16x16x128_f8f6f4 v[120:123], v[136:143], v[160:167], v[120:123]
	v_mfma_f32_16x16x128_f8f6f4 v[116:119], v[128:135], v[168:175], v[116:119]
	v_mfma_f32_16x16x128_f8f6f4 v[112:115], v[136:143], v[168:175], v[112:115]
	v_mfma_f32_16x16x128_f8f6f4 v[108:111], v[128:135], v[176:183], v[108:111]
	v_mfma_f32_16x16x128_f8f6f4 v[104:107], v[136:143], v[176:183], v[104:107]
	v_mfma_f32_16x16x128_f8f6f4 v[100:103], v[128:135], v[184:191], v[100:103]
	v_mfma_f32_16x16x128_f8f6f4 v[96:99], v[136:143], v[184:191], v[96:99]
	v_mfma_f32_16x16x128_f8f6f4 v[194:197], v[144:151], v[160:167], v[92:95]
	v_mfma_f32_16x16x128_f8f6f4 v[160:163], v[152:159], v[160:167], v[88:91]
	v_mfma_f32_16x16x128_f8f6f4 v[164:167], v[144:151], v[168:175], v[84:87]
	v_mfma_f32_16x16x128_f8f6f4 v[168:171], v[152:159], v[168:175], v[80:83]
	v_mfma_f32_16x16x128_f8f6f4 v[172:175], v[144:151], v[176:183], v[76:79]
	v_mfma_f32_16x16x128_f8f6f4 v[176:179], v[152:159], v[176:183], v[72:75]
	v_mfma_f32_16x16x128_f8f6f4 v[180:183], v[144:151], v[184:191], v[68:71]
	v_mfma_f32_16x16x128_f8f6f4 v[184:187], v[152:159], v[184:191], v[64:67]
	s_setprio 0
	s_barrier
	s_mov_b32 m0, s48
	s_nop 3
	ds_read_b128 v[64:67], v241 offset:16384
	ds_read_b128 v[68:71], v241 offset:17408
	ds_read_b128 v[72:75], v241 offset:18432
	ds_read_b128 v[76:79], v241 offset:19456
	ds_read_b128 v[80:83], v241 offset:20480
	ds_read_b128 v[84:87], v241 offset:21504
	ds_read_b128 v[88:91], v241 offset:22528
	ds_read_b128 v[92:95], v241 offset:23552
	buffer_load_dwordx4 v235, s[20:23], s54 offen lds
	s_mov_b32 m0, s56
	s_add_i32 s69, s54, s46
	buffer_load_dwordx4 v237, s[20:23], s54 offen lds
	s_mov_b32 m0, s57
	s_nop 0
	buffer_load_dwordx4 v235, s[20:23], s69 offen lds
	s_mov_b32 m0, s65
	s_nop 0
	buffer_load_dwordx4 v237, s[20:23], s69 offen lds
	s_mov_b32 m0, s47
	s_nop 0
	buffer_load_dwordx4 v192, s[16:19], s68 offen lds
	s_mov_b32 m0, s76
	s_nop 0
	buffer_load_dwordx4 v236, s[16:19], s68 offen lds
	s_waitcnt vmcnt(8)
	s_waitcnt lgkmcnt(0)
	s_barrier
	s_setprio 1
	v_mfma_f32_16x16x128_f8f6f4 v[60:63], v[128:135], v[64:71], v[60:63]
	v_mfma_f32_16x16x128_f8f6f4 v[56:59], v[136:143], v[64:71], v[56:59]
	v_mfma_f32_16x16x128_f8f6f4 v[52:55], v[128:135], v[72:79], v[52:55]
	v_mfma_f32_16x16x128_f8f6f4 v[48:51], v[136:143], v[72:79], v[48:51]
	v_mfma_f32_16x16x128_f8f6f4 v[188:191], v[128:135], v[80:87], v[44:47]
	v_mfma_f32_16x16x128_f8f6f4 v[198:201], v[136:143], v[80:87], v[40:43]
	v_mfma_f32_16x16x128_f8f6f4 v[202:205], v[128:135], v[88:95], v[36:39]
	v_mfma_f32_16x16x128_f8f6f4 v[206:209], v[136:143], v[88:95], v[32:35]
	v_mfma_f32_16x16x128_f8f6f4 v[210:213], v[144:151], v[64:71], v[28:31]
	v_mfma_f32_16x16x128_f8f6f4 v[214:217], v[152:159], v[64:71], v[24:27]
	v_mfma_f32_16x16x128_f8f6f4 v[218:221], v[144:151], v[72:79], v[20:23]
	v_mfma_f32_16x16x128_f8f6f4 v[226:229], v[152:159], v[72:79], v[16:19]
	v_mfma_f32_16x16x128_f8f6f4 v[242:245], v[144:151], v[80:87], v[12:15]
	v_mfma_f32_16x16x128_f8f6f4 v[246:249], v[152:159], v[80:87], v[8:11]
	v_mfma_f32_16x16x128_f8f6f4 v[250:253], v[144:151], v[88:95], v[4:7]
	v_mfma_f32_16x16x128_f8f6f4 v[230:233], v[152:159], v[88:95], v[0:3]
	s_setprio 0
	s_barrier
; #define PG8_STAGE(bufoff, rs_, soff_, voff) do { _Pragma("unroll") for (int _i = 0; _i < 2; ++_i) \
;         __builtin_amdgcn_raw_ptr_buffer_load_lds(rs_, (LAS void*)(lds + (bufoff) + ldsw + _i * 8192), 16, (int)(voff)[_i], (int)(soff_), 0, 0); } while (0)
; #define PG8_LDA(dst, b, h) do { _Pragma("unroll") for (int m = 0; m < 4; ++m) dst[m] = PG8_LD2(lds + PG8_SA(b, h) + aoff + m * 2048); } while (0)
; #define PG8_LDB(dst, b, h) do { _Pragma("unroll") for (int n = 0; n < 2; ++n) dst[n] = PG8_LD2(lds + PG8_SB(b, h) + boff + n * 2048); } while (0)
; #define PG8_WAIT_V(n) asm volatile("s_waitcnt vmcnt(" #n ")" ::: "memory")
; #define PG8_WAIT_L(n) asm volatile("s_waitcnt lgkmcnt(" #n ")" ::: "memory")
; #define PG8_BAR __builtin_amdgcn_s_barrier()
; #define PG8_SCHED __builtin_amdgcn_sched_barrier(0)
; template <class Epi, class Sched, bool ALIGN_EPI = false, bool SP2 = false, bool FP8 = false>
; __device__ __forceinline__ void gemm_phase(LAS unsigned char* lds, const Gemm g, const Sched& S, const Epi& E, int wbase) {
;     ...
;             PG8_LDB(B0, 1, 0); PG8_LDB(B1, 1, 1); PG8_SCHED; PG8_LDA(At, 1, 0); PG8_STAGE(PG8_SA(0, 1), rA2, a2 + hstep, voffA);
;             PG8_WAIT_V(8); PG8_WAIT_L(0); PG8_BAR; PG8_MMA(0, 0, At, B0); PG8_MMA(0, 1, At, B1); PG8_BAR; PG8_SCHED;
;             PG8_LDA(At, 1, 1); PG8_STAGE(PG8_SB(1, 0), rB2, b3, voffB); PG8_STAGE(PG8_SB(1, 1), rB2, b3 + hstep, voffB); PG8_STAGE(PG8_SA(1, 0), rA2, a3, voffA);
;             PG8_WAIT_V(8); PG8_WAIT_L(0); PG8_BAR; PG8_MMA(1, 0, At, B0); PG8_MMA(1, 1, At, B1); PG8_BAR; PG8_SCHED;
	s_nop 1
	v_add_u32_e32 v12, 0x18000, v240
	v_add_u32_e32 v16, 0x1c000, v240
	s_nop 0
	ds_read_b128 v[0:3], v12
	ds_read_b128 v[4:7], v12 offset:1024
	ds_read_b128 v[8:11], v12 offset:2048
	ds_read_b128 v[12:15], v12 offset:3072
	ds_read_b128 v[128:131], v16
	ds_read_b128 v[132:135], v16 offset:1024
	ds_read_b128 v[136:139], v16 offset:2048
	ds_read_b128 v[140:143], v16 offset:3072
	s_add_i32 s68, s68, s46
	s_mov_b32 m0, s77
	ds_read_b128 v[16:19], v241 offset:32768
	ds_read_b128 v[20:23], v241 offset:33792
	ds_read_b128 v[24:27], v241 offset:34816
	ds_read_b128 v[28:31], v241 offset:35840
	ds_read_b128 v[32:35], v241 offset:36864
	ds_read_b128 v[36:39], v241 offset:37888
	ds_read_b128 v[40:43], v241 offset:38912
	ds_read_b128 v[44:47], v241 offset:39936
	buffer_load_dwordx4 v192, s[16:19], s68 offen lds
	s_mov_b32 m0, s79
	s_nop 0
	buffer_load_dwordx4 v236, s[16:19], s68 offen lds
	s_waitcnt vmcnt(8)
	s_waitcnt lgkmcnt(0)
	s_barrier
	s_setprio 1
	v_mfma_f32_16x16x128_f8f6f4 v[124:127], v[0:7], v[16:23], v[124:127]
	v_mfma_f32_16x16x128_f8f6f4 v[120:123], v[8:15], v[16:23], v[120:123]
	v_mfma_f32_16x16x128_f8f6f4 v[116:119], v[0:7], v[24:31], v[116:119]
	v_mfma_f32_16x16x128_f8f6f4 v[112:115], v[8:15], v[24:31], v[112:115]
	v_mfma_f32_16x16x128_f8f6f4 v[108:111], v[0:7], v[32:39], v[108:111]
	v_mfma_f32_16x16x128_f8f6f4 v[104:107], v[8:15], v[32:39], v[104:107]
	v_mfma_f32_16x16x128_f8f6f4 v[100:103], v[0:7], v[40:47], v[100:103]
	v_mfma_f32_16x16x128_f8f6f4 v[96:99], v[8:15], v[40:47], v[96:99]
	v_mfma_f32_16x16x128_f8f6f4 v[92:95], v[128:135], v[16:23], v[194:197]
	v_mfma_f32_16x16x128_f8f6f4 v[88:91], v[136:143], v[16:23], v[160:163]
	v_mfma_f32_16x16x128_f8f6f4 v[84:87], v[128:135], v[24:31], v[164:167]
	v_mfma_f32_16x16x128_f8f6f4 v[80:83], v[136:143], v[24:31], v[168:171]
	v_mfma_f32_16x16x128_f8f6f4 v[76:79], v[128:135], v[32:39], v[172:175]
	v_mfma_f32_16x16x128_f8f6f4 v[72:75], v[136:143], v[32:39], v[176:179]
	v_mfma_f32_16x16x128_f8f6f4 v[68:71], v[128:135], v[40:47], v[180:183]
	v_mfma_f32_16x16x128_f8f6f4 v[64:67], v[136:143], v[40:47], v[184:187]
	s_setprio 0
	s_barrier
	s_mov_b32 m0, s84
	s_bitset1_b32 s54, 7
	ds_read_b128 v[16:19], v241 offset:49152
	ds_read_b128 v[20:23], v241 offset:50176
	ds_read_b128 v[144:147], v241 offset:51200
	ds_read_b128 v[148:151], v241 offset:52224
	ds_read_b128 v[152:155], v241 offset:53248
	ds_read_b128 v[156:159], v241 offset:54272
	ds_read_b128 v[160:163], v241 offset:55296
	ds_read_b128 v[164:167], v241 offset:56320
	buffer_load_dwordx4 v235, s[20:23], s54 offen lds
	s_mov_b32 m0, s85
	s_nop 0
	buffer_load_dwordx4 v237, s[20:23], s54 offen lds
	s_add_i32 s54, s54, s46
	s_mov_b32 m0, s96
	s_nop 0
	buffer_load_dwordx4 v235, s[20:23], s54 offen lds
	s_mov_b32 m0, s97
	s_nop 0
	buffer_load_dwordx4 v237, s[20:23], s54 offen lds
	s_mov_b32 m0, s94
	s_nop 0
	buffer_load_dwordx4 v192, s[16:19], s55 offen lds
	s_mov_b32 m0, s95
	s_nop 0
	buffer_load_dwordx4 v236, s[16:19], s55 offen lds
	s_waitcnt vmcnt(8)
	s_waitcnt lgkmcnt(0)
	s_barrier
	s_setprio 1
	v_mfma_f32_16x16x128_f8f6f4 v[60:63], v[0:7], v[16:23], v[60:63]
	v_mfma_f32_16x16x128_f8f6f4 v[56:59], v[8:15], v[16:23], v[56:59]
	v_mfma_f32_16x16x128_f8f6f4 v[52:55], v[0:7], v[144:151], v[52:55]
	v_mfma_f32_16x16x128_f8f6f4 v[48:51], v[8:15], v[144:151], v[48:51]
	v_mfma_f32_16x16x128_f8f6f4 v[44:47], v[0:7], v[152:159], v[188:191]
	v_mfma_f32_16x16x128_f8f6f4 v[40:43], v[8:15], v[152:159], v[198:201]
	v_mfma_f32_16x16x128_f8f6f4 v[36:39], v[0:7], v[160:167], v[202:205]
	v_mfma_f32_16x16x128_f8f6f4 v[32:35], v[8:15], v[160:167], v[206:209]
	v_mfma_f32_16x16x128_f8f6f4 v[28:31], v[128:135], v[16:23], v[210:213]
	v_mfma_f32_16x16x128_f8f6f4 v[24:27], v[136:143], v[16:23], v[214:217]
	v_mfma_f32_16x16x128_f8f6f4 v[20:23], v[128:135], v[144:151], v[218:221]
	v_mfma_f32_16x16x128_f8f6f4 v[16:19], v[136:143], v[144:151], v[226:229]
	v_mfma_f32_16x16x128_f8f6f4 v[12:15], v[128:135], v[152:159], v[242:245]
	v_mfma_f32_16x16x128_f8f6f4 v[8:11], v[136:143], v[152:159], v[246:249]
	v_mfma_f32_16x16x128_f8f6f4 v[4:7], v[128:135], v[160:167], v[250:253]
	v_mfma_f32_16x16x128_f8f6f4 v[0:3], v[136:143], v[160:167], v[230:233]
	s_setprio 0
	s_barrier
	s_add_i32 s78, s78, 2
	s_addk_i32 vcc_hi, 0x100
	s_addk_i32 s3, 0x100
	s_cmp_ge_i32 s78, s60
	s_cbranch_scc0 .LBB0_813
	v_readlane_b32 s68, v255, 22
	v_readlane_b32 s54, v255, 25
	v_readlane_b32 s69, v255, 23
	v_readlane_b32 s55, v255, 26
	v_mov_b32_e32 v230, v193
	v_mov_b32_e32 v231, v222

; #define PG8_STAGE(bufoff, rs_, soff_, voff) do { _Pragma("unroll") for (int _i = 0; _i < 2; ++_i) \
;         __builtin_amdgcn_raw_ptr_buffer_load_lds(rs_, (LAS void*)(lds + (bufoff) + ldsw + _i * 8192), 16, (int)(voff)[_i], (int)(soff_), 0, 0); } while (0)
; #define PG8_LDA(dst, b, h) do { _Pragma("unroll") for (int m = 0; m < 4; ++m) dst[m] = PG8_LD2(lds + PG8_SA(b, h) + aoff + m * 2048); } while (0)
; #define PG8_LDB(dst, b, h) do { _Pragma("unroll") for (int n = 0; n < 2; ++n) dst[n] = PG8_LD2(lds + PG8_SB(b, h) + boff + n * 2048); } while (0)
; #define PG8_WAIT_V(n) asm volatile("s_waitcnt vmcnt(" #n ")" ::: "memory")
; #define PG8_WAIT_L(n) asm volatile("s_waitcnt lgkmcnt(" #n ")" ::: "memory")
; #define PG8_BAR __builtin_amdgcn_s_barrier()
; #define PG8_SCHED __builtin_amdgcn_sched_barrier(0)
; template <class Epi, class Sched, bool ALIGN_EPI = false, bool SP2 = false, bool FP8 = false>
; __device__ __forceinline__ void gemm_phase(LAS unsigned char* lds, const Gemm g, const Sched& S, const Epi& E, int wbase) {
;     ...
;             const unsigned a2 = last ? nA : cA + (unsigned)(t + 2) * kstep, b2 = last ? nB : cB + (unsigned)(t + 2) * kstep; const rsrc_t rA2 = (Sched::TWO && last) ? rAn : rAc, rB2 = (Sched::TWO && last) ? rBn : rBc;
;             const unsigned a3 = a2 + kstep, b3 = b2 + kstep;
;             if (last && has_next) S.a_ready(nxt);
;             if constexpr (SP2) {
;             PG8_LDB(B0, 0, 0); PG8_LDB(B1, 0, 1); PG8_SCHED; PG8_LDA(At, 0, 0); PG8_STAGE(PG8_SA(1, 1), rAc, a1 + hstep, voffA);
;             PG8_WAIT_V(8); PG8_WAIT_L(0); PG8_BAR; PG8_MMA(0, 0, At, B0); PG8_MMA(0, 1, At, B1); PG8_BAR; PG8_SCHED;
;             PG8_LDA(At, 0, 1); PG8_STAGE(PG8_SB(0, 0), rB2, b2, voffB); PG8_STAGE(PG8_SB(0, 1), rB2, b2 + hstep, voffB); PG8_STAGE(PG8_SA(0, 0), rA2, a2, voffA);
.LBB0_847:
	s_add_i32 s20, vcc_lo, 0x80
	v_add_u32_e32 v140, 0x10000, v238
	v_add_u32_e32 v156, 0x14000, v238
	s_cmp_eq_u32 s88, s85
	ds_read_b128 v[128:131], v140
	ds_read_b128 v[132:135], v140 offset:1024
	ds_read_b128 v[136:139], v140 offset:2048
	ds_read_b128 v[140:143], v140 offset:3072
	ds_read_b128 v[144:147], v156
	ds_read_b128 v[148:151], v156 offset:1024
	ds_read_b128 v[152:155], v156 offset:2048
	ds_read_b128 v[156:159], v156 offset:3072
	s_cselect_b64 s[16:17], -1, 0
	s_and_b64 s[18:19], s[16:17], exec
	s_cselect_b32 s68, s67, s20
	s_cselect_b32 s54, s78, vcc_hi
	s_and_b64 s[20:21], s[58:59], s[16:17]
	s_and_b64 s[16:17], s[20:21], exec
	s_cselect_b32 s18, s30, s14
	s_cselect_b32 s19, s31, s15
	s_cselect_b32 s17, s35, s13
	s_cselect_b32 s16, s34, s12
	s_or_b32 s55, s68, 0x80
	s_and_b64 s[20:21], s[20:21], exec
	s_cselect_b32 s23, s31, s53
	s_cselect_b32 s22, s30, s52
	s_cselect_b32 s21, s45, s11
	s_cselect_b32 s20, s44, s10
	s_add_i32 s69, s41, vcc_lo
	s_mov_b32 m0, s89
	ds_read_b128 v[160:163], v239
	ds_read_b128 v[164:167], v239 offset:1024
	ds_read_b128 v[168:171], v239 offset:2048
	ds_read_b128 v[172:175], v239 offset:3072
	ds_read_b128 v[176:179], v239 offset:4096
	ds_read_b128 v[180:183], v239 offset:5120
	ds_read_b128 v[184:187], v239 offset:6144
	ds_read_b128 v[188:191], v239 offset:7168
	buffer_load_dwordx4 v192, s[12:15], s69 offen lds
	s_mov_b32 m0, s92
	s_nop 0
	buffer_load_dwordx4 v223, s[12:15], s69 offen lds
	s_waitcnt vmcnt(8)
	s_waitcnt lgkmcnt(0)
	s_barrier
	s_setprio 1
	v_mfma_f32_16x16x32_bf16 v[124:127], v[128:131], v[160:163], v[124:127]
	v_mfma_f32_16x16x32_bf16 v[120:123], v[136:139], v[160:163], v[120:123]
	v_mfma_f32_16x16x32_bf16 v[116:119], v[128:131], v[168:171], v[116:119]
	v_mfma_f32_16x16x32_bf16 v[112:115], v[136:139], v[168:171], v[112:115]
	v_mfma_f32_16x16x32_bf16 v[108:111], v[128:131], v[176:179], v[108:111]
	v_mfma_f32_16x16x32_bf16 v[104:107], v[136:139], v[176:179], v[104:107]
	v_mfma_f32_16x16x32_bf16 v[100:103], v[128:131], v[184:187], v[100:103]
	v_mfma_f32_16x16x32_bf16 v[96:99], v[136:139], v[184:187], v[96:99]
	v_mfma_f32_16x16x32_bf16 v[124:127], v[132:135], v[164:167], v[124:127]
	v_mfma_f32_16x16x32_bf16 v[120:123], v[140:143], v[164:167], v[120:123]
	v_mfma_f32_16x16x32_bf16 v[116:119], v[132:135], v[172:175], v[116:119]
	v_mfma_f32_16x16x32_bf16 v[112:115], v[140:143], v[172:175], v[112:115]
	v_mfma_f32_16x16x32_bf16 v[108:111], v[132:135], v[180:183], v[108:111]
	v_mfma_f32_16x16x32_bf16 v[104:107], v[140:143], v[180:183], v[104:107]
	v_mfma_f32_16x16x32_bf16 v[100:103], v[132:135], v[188:191], v[100:103]
	v_mfma_f32_16x16x32_bf16 v[96:99], v[140:143], v[188:191], v[96:99]
	v_mfma_f32_16x16x32_bf16 v[92:95], v[144:147], v[160:163], v[92:95]
	v_mfma_f32_16x16x32_bf16 v[88:91], v[152:155], v[160:163], v[88:91]
	v_mfma_f32_16x16x32_bf16 v[84:87], v[144:147], v[168:171], v[84:87]
	v_mfma_f32_16x16x32_bf16 v[80:83], v[152:155], v[168:171], v[80:83]
	v_mfma_f32_16x16x32_bf16 v[76:79], v[144:147], v[176:179], v[76:79]
	v_mfma_f32_16x16x32_bf16 v[72:75], v[152:155], v[176:179], v[72:75]
	v_mfma_f32_16x16x32_bf16 v[68:71], v[144:147], v[184:187], v[68:71]
	v_mfma_f32_16x16x32_bf16 v[64:67], v[152:155], v[184:187], v[64:67]
	v_mfma_f32_16x16x32_bf16 v[92:95], v[148:151], v[164:167], v[92:95]
	v_mfma_f32_16x16x32_bf16 v[88:91], v[156:159], v[164:167], v[88:91]
	v_mfma_f32_16x16x32_bf16 v[84:87], v[148:151], v[172:175], v[84:87]
	v_mfma_f32_16x16x32_bf16 v[80:83], v[156:159], v[172:175], v[80:83]
	v_mfma_f32_16x16x32_bf16 v[76:79], v[148:151], v[180:183], v[76:79]
	v_mfma_f32_16x16x32_bf16 v[72:75], v[156:159], v[180:183], v[72:75]
	v_mfma_f32_16x16x32_bf16 v[68:71], v[148:151], v[188:191], v[68:71]
	v_mfma_f32_16x16x32_bf16 v[64:67], v[156:159], v[188:191], v[64:67]
	s_setprio 0
	s_barrier
	s_mov_b32 m0, s43
	ds_read_b128 v[160:163], v239 offset:16384
	ds_read_b128 v[164:167], v239 offset:17408
	ds_read_b128 v[168:171], v239 offset:18432
	ds_read_b128 v[172:175], v239 offset:19456
	ds_read_b128 v[176:179], v239 offset:20480
	ds_read_b128 v[180:183], v239 offset:21504
	ds_read_b128 v[184:187], v239 offset:22528
	ds_read_b128 v[188:191], v239 offset:23552
	buffer_load_dwordx4 v222, s[20:23], s54 offen lds
	s_mov_b32 m0, s46
	s_add_i32 s69, s54, s41
	buffer_load_dwordx4 v235, s[20:23], s54 offen lds
	s_mov_b32 m0, s47
	s_nop 0
	buffer_load_dwordx4 v222, s[20:23], s69 offen lds
	s_mov_b32 m0, s48
	s_nop 0
	buffer_load_dwordx4 v235, s[20:23], s69 offen lds
	s_mov_b32 m0, s42
	s_nop 0
	buffer_load_dwordx4 v192, s[16:19], s68 offen lds
	s_mov_b32 m0, s56
	s_nop 0
	buffer_load_dwordx4 v223, s[16:19], s68 offen lds
	s_waitcnt vmcnt(8)
	s_waitcnt lgkmcnt(0)
	s_barrier
; #define PG8_STAGE(bufoff, rs_, soff_, voff) do { _Pragma("unroll") for (int _i = 0; _i < 2; ++_i) \
;         __builtin_amdgcn_raw_ptr_buffer_load_lds(rs_, (LAS void*)(lds + (bufoff) + ldsw + _i * 8192), 16, (int)(voff)[_i], (int)(soff_), 0, 0); } while (0)
; #define PG8_LDA(dst, b, h) do { _Pragma("unroll") for (int m = 0; m < 4; ++m) dst[m] = PG8_LD2(lds + PG8_SA(b, h) + aoff + m * 2048); } while (0)
; #define PG8_LDB(dst, b, h) do { _Pragma("unroll") for (int n = 0; n < 2; ++n) dst[n] = PG8_LD2(lds + PG8_SB(b, h) + boff + n * 2048); } while (0)
; #define PG8_WAIT_V(n) asm volatile("s_waitcnt vmcnt(" #n ")" ::: "memory")
; #define PG8_WAIT_L(n) asm volatile("s_waitcnt lgkmcnt(" #n ")" ::: "memory")
; #define PG8_BAR __builtin_amdgcn_s_barrier()
; #define PG8_SCHED __builtin_amdgcn_sched_barrier(0)
; template <class Epi, class Sched, bool ALIGN_EPI = false, bool SP2 = false, bool FP8 = false>
; __device__ __forceinline__ void gemm_phase(LAS unsigned char* lds, const Gemm g, const Sched& S, const Epi& E, int wbase) {
;     ...
;             PG8_WAIT_V(8); PG8_WAIT_L(0); PG8_BAR; PG8_MMA(1, 0, At, B0); PG8_MMA(1, 1, At, B1); PG8_BAR; PG8_SCHED;
;             PG8_LDB(B0, 1, 0); PG8_LDB(B1, 1, 1); PG8_SCHED; PG8_LDA(At, 1, 0); PG8_STAGE(PG8_SA(0, 1), rA2, a2 + hstep, voffA);
;             PG8_WAIT_V(8); PG8_WAIT_L(0); PG8_BAR; PG8_MMA(0, 0, At, B0); PG8_MMA(0, 1, At, B1); PG8_BAR; PG8_SCHED;
	s_setprio 1
	v_mfma_f32_16x16x32_bf16 v[60:63], v[128:131], v[160:163], v[60:63]
	v_mfma_f32_16x16x32_bf16 v[56:59], v[136:139], v[160:163], v[56:59]
	v_mfma_f32_16x16x32_bf16 v[52:55], v[128:131], v[168:171], v[52:55]
	v_mfma_f32_16x16x32_bf16 v[48:51], v[136:139], v[168:171], v[48:51]
	v_mfma_f32_16x16x32_bf16 v[44:47], v[128:131], v[176:179], v[44:47]
	v_mfma_f32_16x16x32_bf16 v[40:43], v[136:139], v[176:179], v[40:43]
	v_mfma_f32_16x16x32_bf16 v[36:39], v[128:131], v[184:187], v[36:39]
	v_mfma_f32_16x16x32_bf16 v[32:35], v[136:139], v[184:187], v[32:35]
	v_mfma_f32_16x16x32_bf16 v[60:63], v[132:135], v[164:167], v[60:63]
	v_mfma_f32_16x16x32_bf16 v[56:59], v[140:143], v[164:167], v[56:59]
	v_mfma_f32_16x16x32_bf16 v[52:55], v[132:135], v[172:175], v[52:55]
	v_mfma_f32_16x16x32_bf16 v[48:51], v[140:143], v[172:175], v[48:51]
	v_mfma_f32_16x16x32_bf16 v[44:47], v[132:135], v[180:183], v[44:47]
	v_mfma_f32_16x16x32_bf16 v[40:43], v[140:143], v[180:183], v[40:43]
	v_mfma_f32_16x16x32_bf16 v[36:39], v[132:135], v[188:191], v[36:39]
	v_mfma_f32_16x16x32_bf16 v[32:35], v[140:143], v[188:191], v[32:35]
	v_mfma_f32_16x16x32_bf16 v[28:31], v[144:147], v[160:163], v[28:31]
	v_mfma_f32_16x16x32_bf16 v[24:27], v[152:155], v[160:163], v[24:27]
	v_mfma_f32_16x16x32_bf16 v[20:23], v[144:147], v[168:171], v[20:23]
	v_mfma_f32_16x16x32_bf16 v[16:19], v[152:155], v[168:171], v[16:19]
	v_mfma_f32_16x16x32_bf16 v[12:15], v[144:147], v[176:179], v[12:15]
	v_mfma_f32_16x16x32_bf16 v[8:11], v[152:155], v[176:179], v[8:11]
	v_mfma_f32_16x16x32_bf16 v[4:7], v[144:147], v[184:187], v[4:7]
	v_mfma_f32_16x16x32_bf16 v[0:3], v[152:155], v[184:187], v[0:3]
	v_mfma_f32_16x16x32_bf16 v[28:31], v[148:151], v[164:167], v[28:31]
	v_mfma_f32_16x16x32_bf16 v[24:27], v[156:159], v[164:167], v[24:27]
	v_mfma_f32_16x16x32_bf16 v[20:23], v[148:151], v[172:175], v[20:23]
	v_mfma_f32_16x16x32_bf16 v[16:19], v[156:159], v[172:175], v[16:19]
	v_mfma_f32_16x16x32_bf16 v[12:15], v[148:151], v[180:183], v[12:15]
	v_mfma_f32_16x16x32_bf16 v[8:11], v[156:159], v[180:183], v[8:11]
	v_mfma_f32_16x16x32_bf16 v[4:7], v[148:151], v[188:191], v[4:7]
	v_mfma_f32_16x16x32_bf16 v[0:3], v[156:159], v[188:191], v[0:3]
	s_setprio 0
	s_barrier
	v_add_u32_e32 v140, 0x18000, v238
	v_add_u32_e32 v156, 0x1c000, v238
	ds_read_b128 v[128:131], v140
	ds_read_b128 v[132:135], v140 offset:1024
	ds_read_b128 v[136:139], v140 offset:2048
	ds_read_b128 v[140:143], v140 offset:3072
	ds_read_b128 v[144:147], v156
	ds_read_b128 v[148:151], v156 offset:1024
	ds_read_b128 v[152:155], v156 offset:2048
	ds_read_b128 v[156:159], v156 offset:3072
	s_add_i32 s68, s68, s41
	s_mov_b32 m0, s57
	ds_read_b128 v[160:163], v239 offset:32768
	ds_read_b128 v[164:167], v239 offset:33792
	ds_read_b128 v[168:171], v239 offset:34816
	ds_read_b128 v[172:175], v239 offset:35840
	ds_read_b128 v[176:179], v239 offset:36864
	ds_read_b128 v[180:183], v239 offset:37888
	ds_read_b128 v[184:187], v239 offset:38912
	ds_read_b128 v[188:191], v239 offset:39936
	buffer_load_dwordx4 v192, s[16:19], s68 offen lds
	s_mov_b32 m0, s60
	s_nop 0
	buffer_load_dwordx4 v223, s[16:19], s68 offen lds
	s_waitcnt vmcnt(8)
	s_waitcnt lgkmcnt(0)
	s_barrier
	s_setprio 1
	v_mfma_f32_16x16x32_bf16 v[124:127], v[128:131], v[160:163], v[124:127]
	v_mfma_f32_16x16x32_bf16 v[120:123], v[136:139], v[160:163], v[120:123]
	v_mfma_f32_16x16x32_bf16 v[116:119], v[128:131], v[168:171], v[116:119]
	v_mfma_f32_16x16x32_bf16 v[112:115], v[136:139], v[168:171], v[112:115]
	v_mfma_f32_16x16x32_bf16 v[108:111], v[128:131], v[176:179], v[108:111]
	v_mfma_f32_16x16x32_bf16 v[104:107], v[136:139], v[176:179], v[104:107]
	v_mfma_f32_16x16x32_bf16 v[100:103], v[128:131], v[184:187], v[100:103]
	v_mfma_f32_16x16x32_bf16 v[96:99], v[136:139], v[184:187], v[96:99]
	v_mfma_f32_16x16x32_bf16 v[124:127], v[132:135], v[164:167], v[124:127]
	v_mfma_f32_16x16x32_bf16 v[120:123], v[140:143], v[164:167], v[120:123]
	v_mfma_f32_16x16x32_bf16 v[116:119], v[132:135], v[172:175], v[116:119]
	v_mfma_f32_16x16x32_bf16 v[112:115], v[140:143], v[172:175], v[112:115]
	v_mfma_f32_16x16x32_bf16 v[108:111], v[132:135], v[180:183], v[108:111]
	v_mfma_f32_16x16x32_bf16 v[104:107], v[140:143], v[180:183], v[104:107]
	v_mfma_f32_16x16x32_bf16 v[100:103], v[132:135], v[188:191], v[100:103]
	v_mfma_f32_16x16x32_bf16 v[96:99], v[140:143], v[188:191], v[96:99]
	v_mfma_f32_16x16x32_bf16 v[92:95], v[144:147], v[160:163], v[92:95]
	v_mfma_f32_16x16x32_bf16 v[88:91], v[152:155], v[160:163], v[88:91]
	v_mfma_f32_16x16x32_bf16 v[84:87], v[144:147], v[168:171], v[84:87]
	v_mfma_f32_16x16x32_bf16 v[80:83], v[152:155], v[168:171], v[80:83]
	v_mfma_f32_16x16x32_bf16 v[76:79], v[144:147], v[176:179], v[76:79]
	v_mfma_f32_16x16x32_bf16 v[72:75], v[152:155], v[176:179], v[72:75]
	v_mfma_f32_16x16x32_bf16 v[68:71], v[144:147], v[184:187], v[68:71]
	v_mfma_f32_16x16x32_bf16 v[64:67], v[152:155], v[184:187], v[64:67]
	v_mfma_f32_16x16x32_bf16 v[92:95], v[148:151], v[164:167], v[92:95]
	v_mfma_f32_16x16x32_bf16 v[88:91], v[156:159], v[164:167], v[88:91]
	v_mfma_f32_16x16x32_bf16 v[84:87], v[148:151], v[172:175], v[84:87]
	v_mfma_f32_16x16x32_bf16 v[80:83], v[156:159], v[172:175], v[80:83]
	v_mfma_f32_16x16x32_bf16 v[76:79], v[148:151], v[180:183], v[76:79]
	v_mfma_f32_16x16x32_bf16 v[72:75], v[156:159], v[180:183], v[72:75]
	v_mfma_f32_16x16x32_bf16 v[68:71], v[148:151], v[188:191], v[68:71]
	v_mfma_f32_16x16x32_bf16 v[64:67], v[156:159], v[188:191], v[64:67]
	s_setprio 0
	s_barrier
; #define PG8_STAGE(bufoff, rs_, soff_, voff) do { _Pragma("unroll") for (int _i = 0; _i < 2; ++_i) \
;         __builtin_amdgcn_raw_ptr_buffer_load_lds(rs_, (LAS void*)(lds + (bufoff) + ldsw + _i * 8192), 16, (int)(voff)[_i], (int)(soff_), 0, 0); } while (0)
; #define PG8_LDA(dst, b, h) do { _Pragma("unroll") for (int m = 0; m < 4; ++m) dst[m] = PG8_LD2(lds + PG8_SA(b, h) + aoff + m * 2048); } while (0)
; #define PG8_WAIT_V(n) asm volatile("s_waitcnt vmcnt(" #n ")" ::: "memory")
; #define PG8_WAIT_L(n) asm volatile("s_waitcnt lgkmcnt(" #n ")" ::: "memory")
; #define PG8_BAR __builtin_amdgcn_s_barrier()
; #define PG8_SCHED __builtin_amdgcn_sched_barrier(0)
; template <class Epi, class Sched, bool ALIGN_EPI = false, bool SP2 = false, bool FP8 = false>
; __device__ __forceinline__ void gemm_phase(LAS unsigned char* lds, const Gemm g, const Sched& S, const Epi& E, int wbase) {
;     ...
;             PG8_LDA(At, 1, 1); PG8_STAGE(PG8_SB(1, 0), rB2, b3, voffB); PG8_STAGE(PG8_SB(1, 1), rB2, b3 + hstep, voffB); PG8_STAGE(PG8_SA(1, 0), rA2, a3, voffA);
;             PG8_WAIT_V(8); PG8_WAIT_L(0); PG8_BAR; PG8_MMA(1, 0, At, B0); PG8_MMA(1, 1, At, B1); PG8_BAR; PG8_SCHED;
	s_mov_b32 m0, s63
	s_bitset1_b32 s54, 7
	ds_read_b128 v[160:163], v239 offset:49152
	ds_read_b128 v[164:167], v239 offset:50176
	ds_read_b128 v[168:171], v239 offset:51200
	ds_read_b128 v[172:175], v239 offset:52224
	ds_read_b128 v[176:179], v239 offset:53248
	ds_read_b128 v[180:183], v239 offset:54272
	ds_read_b128 v[184:187], v239 offset:55296
	ds_read_b128 v[188:191], v239 offset:56320
	buffer_load_dwordx4 v222, s[20:23], s54 offen lds
	s_mov_b32 m0, s65
	s_nop 0
	buffer_load_dwordx4 v235, s[20:23], s54 offen lds
	s_add_i32 s54, s54, s41
	s_mov_b32 m0, s79
	s_nop 0
	buffer_load_dwordx4 v222, s[20:23], s54 offen lds
	s_mov_b32 m0, s80
	s_nop 0
	buffer_load_dwordx4 v235, s[20:23], s54 offen lds
	s_mov_b32 m0, s76
	s_nop 0
	buffer_load_dwordx4 v192, s[16:19], s55 offen lds
	s_mov_b32 m0, s77
	s_nop 0
	buffer_load_dwordx4 v223, s[16:19], s55 offen lds
	s_waitcnt vmcnt(8)
	s_waitcnt lgkmcnt(0)
	s_barrier
	s_setprio 1
	v_mfma_f32_16x16x32_bf16 v[60:63], v[128:131], v[160:163], v[60:63]
	v_mfma_f32_16x16x32_bf16 v[56:59], v[136:139], v[160:163], v[56:59]
	v_mfma_f32_16x16x32_bf16 v[52:55], v[128:131], v[168:171], v[52:55]
	v_mfma_f32_16x16x32_bf16 v[48:51], v[136:139], v[168:171], v[48:51]
	v_mfma_f32_16x16x32_bf16 v[44:47], v[128:131], v[176:179], v[44:47]
	v_mfma_f32_16x16x32_bf16 v[40:43], v[136:139], v[176:179], v[40:43]
	v_mfma_f32_16x16x32_bf16 v[36:39], v[128:131], v[184:187], v[36:39]
	v_mfma_f32_16x16x32_bf16 v[32:35], v[136:139], v[184:187], v[32:35]
	v_mfma_f32_16x16x32_bf16 v[60:63], v[132:135], v[164:167], v[60:63]
	v_mfma_f32_16x16x32_bf16 v[56:59], v[140:143], v[164:167], v[56:59]
	v_mfma_f32_16x16x32_bf16 v[52:55], v[132:135], v[172:175], v[52:55]
	v_mfma_f32_16x16x32_bf16 v[48:51], v[140:143], v[172:175], v[48:51]
	v_mfma_f32_16x16x32_bf16 v[44:47], v[132:135], v[180:183], v[44:47]
	v_mfma_f32_16x16x32_bf16 v[40:43], v[140:143], v[180:183], v[40:43]
	v_mfma_f32_16x16x32_bf16 v[36:39], v[132:135], v[188:191], v[36:39]
	v_mfma_f32_16x16x32_bf16 v[32:35], v[140:143], v[188:191], v[32:35]
	v_mfma_f32_16x16x32_bf16 v[28:31], v[144:147], v[160:163], v[28:31]
	v_mfma_f32_16x16x32_bf16 v[24:27], v[152:155], v[160:163], v[24:27]
	v_mfma_f32_16x16x32_bf16 v[20:23], v[144:147], v[168:171], v[20:23]
	v_mfma_f32_16x16x32_bf16 v[16:19], v[152:155], v[168:171], v[16:19]
	v_mfma_f32_16x16x32_bf16 v[12:15], v[144:147], v[176:179], v[12:15]
	v_mfma_f32_16x16x32_bf16 v[8:11], v[152:155], v[176:179], v[8:11]
	v_mfma_f32_16x16x32_bf16 v[4:7], v[144:147], v[184:187], v[4:7]
	v_mfma_f32_16x16x32_bf16 v[0:3], v[152:155], v[184:187], v[0:3]
	v_mfma_f32_16x16x32_bf16 v[28:31], v[148:151], v[164:167], v[28:31]
	v_mfma_f32_16x16x32_bf16 v[24:27], v[156:159], v[164:167], v[24:27]
	v_mfma_f32_16x16x32_bf16 v[20:23], v[148:151], v[172:175], v[20:23]
	v_mfma_f32_16x16x32_bf16 v[16:19], v[156:159], v[172:175], v[16:19]
	v_mfma_f32_16x16x32_bf16 v[12:15], v[148:151], v[180:183], v[12:15]
	v_mfma_f32_16x16x32_bf16 v[8:11], v[156:159], v[180:183], v[8:11]
	v_mfma_f32_16x16x32_bf16 v[4:7], v[148:151], v[188:191], v[4:7]
	v_mfma_f32_16x16x32_bf16 v[0:3], v[156:159], v[188:191], v[0:3]
	s_setprio 0
	s_barrier
	s_add_i32 s85, s85, 2
	s_addk_i32 vcc_lo, 0x100
	s_addk_i32 vcc_hi, 0x100
	s_cmp_ge_i32 s85, s81
	s_cbranch_scc0 .LBB0_847
	v_readlane_b32 s68, v255, 22
	v_readlane_b32 s54, v255, 25
	v_readlane_b32 s69, v255, 23
	v_readlane_b32 s55, v255, 26

; #define PG8_STAGE(bufoff, rs_, soff_, voff) do { _Pragma("unroll") for (int _i = 0; _i < 2; ++_i) \
;         __builtin_amdgcn_raw_ptr_buffer_load_lds(rs_, (LAS void*)(lds + (bufoff) + ldsw + _i * 8192), 16, (int)(voff)[_i], (int)(soff_), 0, 0); } while (0)
; #define PG8_LDA(dst, b, h) do { _Pragma("unroll") for (int m = 0; m < 4; ++m) dst[m] = PG8_LD2(lds + PG8_SA(b, h) + aoff + m * 2048); } while (0)
; #define PG8_LDB(dst, b, h) do { _Pragma("unroll") for (int n = 0; n < 2; ++n) dst[n] = PG8_LD2(lds + PG8_SB(b, h) + boff + n * 2048); } while (0)
; #define PG8_WAIT_V(n) asm volatile("s_waitcnt vmcnt(" #n ")" ::: "memory")
; #define PG8_WAIT_L(n) asm volatile("s_waitcnt lgkmcnt(" #n ")" ::: "memory")
; #define PG8_BAR __builtin_amdgcn_s_barrier()
; #define PG8_SCHED __builtin_amdgcn_sched_barrier(0)
; template <class Epi, class Sched, bool ALIGN_EPI = false, bool SP2 = false, bool FP8 = false>
; __device__ __forceinline__ void gemm_phase(LAS unsigned char* lds, const Gemm g, const Sched& S, const Epi& E, int wbase) {
;     ...
;             PG8_LDB(B0, 0, 0); PG8_LDB(B1, 0, 1); PG8_SCHED; PG8_LDA(At, 0, 0); PG8_STAGE(PG8_SA(1, 1), rAc, a1 + hstep, voffA);
;             PG8_WAIT_V(8); PG8_WAIT_L(0); PG8_BAR; PG8_MMA(0, 0, At, B0); PG8_MMA(0, 1, At, B1); PG8_BAR; PG8_SCHED;
;             PG8_LDA(At, 0, 1); PG8_STAGE(PG8_SB(0, 0), rB2, b2, voffB); PG8_STAGE(PG8_SB(0, 1), rB2, b2 + hstep, voffB); PG8_STAGE(PG8_SA(0, 0), rA2, a2, voffA);
;             PG8_WAIT_V(8); PG8_WAIT_L(0); PG8_BAR; PG8_MMA(1, 0, At, B0); PG8_MMA(1, 1, At, B1); PG8_BAR; PG8_SCHED;
.LBB0_926:
	v_add_u32_e32 v120, 0x10000, v160
	ds_read_b128 v[132:135], v120
	ds_read_b128 v[136:139], v120 offset:1024
	ds_read_b128 v[140:143], v120 offset:2048
	ds_read_b128 v[144:147], v120 offset:3072
	v_add_u32_e32 v120, 0x14000, v160
	ds_read_b128 v[162:165], v120
	ds_read_b128 v[166:169], v120 offset:1024
	ds_read_b128 v[170:173], v120 offset:2048
	ds_read_b128 v[174:177], v120 offset:3072
	s_add_i32 s14, s4, 0x80
	s_cmp_eq_u32 s60, s11
	s_cselect_b32 s66, s2, s14
	s_cselect_b32 s55, s3, s5
	s_or_b32 s54, s66, 0x80
	s_add_i32 s14, s30, s4
	s_mov_b32 m0, s61
	ds_read_b128 v[178:181], v161
	ds_read_b128 v[182:185], v161 offset:1024
	ds_read_b128 v[194:197], v161 offset:2048
	ds_read_b128 v[198:201], v161 offset:3072
	ds_read_b128 v[202:205], v161 offset:4096
	ds_read_b128 v[206:209], v161 offset:5120
	ds_read_b128 v[210:213], v161 offset:6144
	ds_read_b128 v[214:217], v161 offset:7168
	buffer_load_dwordx4 v222, s[36:39], s14 offen lds
	s_mov_b32 m0, s62
	s_nop 0
	buffer_load_dwordx4 v156, s[36:39], s14 offen lds
	s_waitcnt vmcnt(8)
	s_waitcnt lgkmcnt(0)
	s_barrier
	s_setprio 1
	v_mfma_f32_16x16x128_f8f6f4 v[124:127], v[140:147], v[178:185], v[124:127]
	v_mfma_f32_16x16x128_f8f6f4 v[108:111], v[132:139], v[194:201], v[108:111]
	v_mfma_f32_16x16x128_f8f6f4 v[104:107], v[140:147], v[194:201], v[104:107]
	v_mfma_f32_16x16x128_f8f6f4 v[120:123], v[132:139], v[178:185], v[128:131]
	v_mfma_f32_16x16x128_f8f6f4 v[148:151], v[132:139], v[202:209], v[92:95]
	v_mfma_f32_16x16x128_f8f6f4 v[186:189], v[140:147], v[202:209], v[88:91]
	v_mfma_f32_16x16x128_f8f6f4 v[218:221], v[132:139], v[210:217], v[76:79]
	v_mfma_f32_16x16x128_f8f6f4 v[226:229], v[140:147], v[210:217], v[72:75]
	v_mfma_f32_16x16x128_f8f6f4 v[116:119], v[162:169], v[178:185], v[116:119]
	v_mfma_f32_16x16x128_f8f6f4 v[112:115], v[170:177], v[178:185], v[112:115]
	v_mfma_f32_16x16x128_f8f6f4 v[100:103], v[162:169], v[194:201], v[100:103]
	v_mfma_f32_16x16x128_f8f6f4 v[96:99], v[170:177], v[194:201], v[96:99]
	v_mfma_f32_16x16x128_f8f6f4 v[178:181], v[162:169], v[202:209], v[84:87]
	v_mfma_f32_16x16x128_f8f6f4 v[182:185], v[170:177], v[202:209], v[80:83]
	v_mfma_f32_16x16x128_f8f6f4 v[194:197], v[162:169], v[210:217], v[68:71]
	v_mfma_f32_16x16x128_f8f6f4 v[198:201], v[170:177], v[210:217], v[64:67]
	s_setprio 0
	s_barrier
	s_mov_b32 m0, s33
	s_mov_b32 s14, s38
	s_mov_b32 s15, s39
	s_nop 1
	ds_read_b128 v[64:67], v161 offset:16384
	ds_read_b128 v[68:71], v161 offset:17408
	ds_read_b128 v[72:75], v161 offset:18432
	ds_read_b128 v[76:79], v161 offset:19456
	ds_read_b128 v[80:83], v161 offset:20480
	ds_read_b128 v[84:87], v161 offset:21504
	ds_read_b128 v[88:91], v161 offset:22528
	ds_read_b128 v[92:95], v161 offset:23552
	buffer_load_dwordx4 v223, s[12:15], s55 offen lds
	s_mov_b32 m0, s34
	s_add_i32 s67, s55, s30
	buffer_load_dwordx4 v157, s[12:15], s55 offen lds
	s_mov_b32 m0, s35
	s_nop 0
	buffer_load_dwordx4 v223, s[12:15], s67 offen lds
	s_mov_b32 m0, s41
	s_nop 0
	buffer_load_dwordx4 v157, s[12:15], s67 offen lds
	s_mov_b32 m0, s31
	s_nop 0
	buffer_load_dwordx4 v222, s[36:39], s66 offen lds
	s_mov_b32 m0, s42
	s_nop 0
	buffer_load_dwordx4 v156, s[36:39], s66 offen lds
	s_waitcnt vmcnt(8)
	s_waitcnt lgkmcnt(0)
	s_barrier
	s_setprio 1
	v_mfma_f32_16x16x128_f8f6f4 v[60:63], v[132:139], v[64:71], v[60:63]
	v_mfma_f32_16x16x128_f8f6f4 v[56:59], v[140:147], v[64:71], v[56:59]
	v_mfma_f32_16x16x128_f8f6f4 v[202:205], v[132:139], v[72:79], v[44:47]
	v_mfma_f32_16x16x128_f8f6f4 v[206:209], v[140:147], v[72:79], v[40:43]
	v_mfma_f32_16x16x128_f8f6f4 v[210:213], v[132:139], v[80:87], v[28:31]
	v_mfma_f32_16x16x128_f8f6f4 v[214:217], v[140:147], v[80:87], v[24:27]
	v_mfma_f32_16x16x128_f8f6f4 v[230:233], v[132:139], v[88:95], v[12:15]
	v_mfma_f32_16x16x128_f8f6f4 v[234:237], v[140:147], v[88:95], v[8:11]
	v_mfma_f32_16x16x128_f8f6f4 v[52:55], v[162:169], v[64:71], v[52:55]
	v_mfma_f32_16x16x128_f8f6f4 v[48:51], v[170:177], v[64:71], v[48:51]
	v_mfma_f32_16x16x128_f8f6f4 v[238:241], v[162:169], v[72:79], v[36:39]
	v_mfma_f32_16x16x128_f8f6f4 v[242:245], v[170:177], v[72:79], v[32:35]
	v_mfma_f32_16x16x128_f8f6f4 v[246:249], v[162:169], v[80:87], v[20:23]
	v_mfma_f32_16x16x128_f8f6f4 v[250:253], v[170:177], v[80:87], v[16:19]
	v_mfma_f32_16x16x128_f8f6f4 v[190:193], v[162:169], v[88:95], v[4:7]
	v_mfma_f32_16x16x128_f8f6f4 v[152:155], v[170:177], v[88:95], v[0:3]
	s_setprio 0
	s_barrier
; #define PG8_STAGE(bufoff, rs_, soff_, voff) do { _Pragma("unroll") for (int _i = 0; _i < 2; ++_i) \
;         __builtin_amdgcn_raw_ptr_buffer_load_lds(rs_, (LAS void*)(lds + (bufoff) + ldsw + _i * 8192), 16, (int)(voff)[_i], (int)(soff_), 0, 0); } while (0)
; #define PG8_LDA(dst, b, h) do { _Pragma("unroll") for (int m = 0; m < 4; ++m) dst[m] = PG8_LD2(lds + PG8_SA(b, h) + aoff + m * 2048); } while (0)
; #define PG8_LDB(dst, b, h) do { _Pragma("unroll") for (int n = 0; n < 2; ++n) dst[n] = PG8_LD2(lds + PG8_SB(b, h) + boff + n * 2048); } while (0)
; #define PG8_WAIT_V(n) asm volatile("s_waitcnt vmcnt(" #n ")" ::: "memory")
; #define PG8_WAIT_L(n) asm volatile("s_waitcnt lgkmcnt(" #n ")" ::: "memory")
; #define PG8_BAR __builtin_amdgcn_s_barrier()
; #define PG8_SCHED __builtin_amdgcn_sched_barrier(0)
; template <class Epi, class Sched, bool ALIGN_EPI = false, bool SP2 = false, bool FP8 = false>
; __device__ __forceinline__ void gemm_phase(LAS unsigned char* lds, const Gemm g, const Sched& S, const Epi& E, int wbase) {
;     ...
;             PG8_LDB(B0, 1, 0); PG8_LDB(B1, 1, 1); PG8_SCHED; PG8_LDA(At, 1, 0); PG8_STAGE(PG8_SA(0, 1), rA2, a2 + hstep, voffA);
;             PG8_WAIT_V(8); PG8_WAIT_L(0); PG8_BAR; PG8_MMA(0, 0, At, B0); PG8_MMA(0, 1, At, B1); PG8_BAR; PG8_SCHED;
;             PG8_LDA(At, 1, 1); PG8_STAGE(PG8_SB(1, 0), rB2, b3, voffB); PG8_STAGE(PG8_SB(1, 1), rB2, b3 + hstep, voffB); PG8_STAGE(PG8_SA(1, 0), rA2, a3, voffA);
;             PG8_WAIT_V(8); PG8_WAIT_L(0); PG8_BAR; PG8_MMA(1, 0, At, B0); PG8_MMA(1, 1, At, B1); PG8_BAR; PG8_SCHED;
	v_add_u32_e32 v8, 0x18000, v160
	s_nop 3
	ds_read_b128 v[0:3], v8
	ds_read_b128 v[4:7], v8 offset:1024
	ds_read_b128 v[16:19], v8 offset:2048
	ds_read_b128 v[20:23], v8 offset:3072
	v_add_u32_e32 v8, 0x1c000, v160
	ds_read_b128 v[132:135], v8
	ds_read_b128 v[136:139], v8 offset:1024
	ds_read_b128 v[140:143], v8 offset:2048
	ds_read_b128 v[144:147], v8 offset:3072
	s_add_i32 s66, s66, s30
	s_mov_b32 m0, s43
	ds_read_b128 v[8:11], v161 offset:32768
	ds_read_b128 v[12:15], v161 offset:33792
	ds_read_b128 v[24:27], v161 offset:34816
	ds_read_b128 v[28:31], v161 offset:35840
	ds_read_b128 v[32:35], v161 offset:36864
	ds_read_b128 v[36:39], v161 offset:37888
	ds_read_b128 v[40:43], v161 offset:38912
	ds_read_b128 v[44:47], v161 offset:39936
	buffer_load_dwordx4 v222, s[36:39], s66 offen lds
	s_mov_b32 m0, s44
	s_nop 0
	buffer_load_dwordx4 v156, s[36:39], s66 offen lds
	s_waitcnt vmcnt(8)
	s_waitcnt lgkmcnt(0)
	s_barrier
	s_setprio 1
	v_mfma_f32_16x16x128_f8f6f4 v[128:131], v[0:7], v[8:15], v[120:123]
	v_mfma_f32_16x16x128_f8f6f4 v[124:127], v[16:23], v[8:15], v[124:127]
	v_mfma_f32_16x16x128_f8f6f4 v[108:111], v[0:7], v[24:31], v[108:111]
	v_mfma_f32_16x16x128_f8f6f4 v[104:107], v[16:23], v[24:31], v[104:107]
	v_mfma_f32_16x16x128_f8f6f4 v[92:95], v[0:7], v[32:39], v[148:151]
	v_mfma_f32_16x16x128_f8f6f4 v[88:91], v[16:23], v[32:39], v[186:189]
	v_mfma_f32_16x16x128_f8f6f4 v[76:79], v[0:7], v[40:47], v[218:221]
	v_mfma_f32_16x16x128_f8f6f4 v[72:75], v[16:23], v[40:47], v[226:229]
	v_mfma_f32_16x16x128_f8f6f4 v[116:119], v[132:139], v[8:15], v[116:119]
	v_mfma_f32_16x16x128_f8f6f4 v[112:115], v[140:147], v[8:15], v[112:115]
	v_mfma_f32_16x16x128_f8f6f4 v[100:103], v[132:139], v[24:31], v[100:103]
	v_mfma_f32_16x16x128_f8f6f4 v[96:99], v[140:147], v[24:31], v[96:99]
	v_mfma_f32_16x16x128_f8f6f4 v[84:87], v[132:139], v[32:39], v[178:181]
	v_mfma_f32_16x16x128_f8f6f4 v[80:83], v[140:147], v[32:39], v[182:185]
	v_mfma_f32_16x16x128_f8f6f4 v[68:71], v[132:139], v[40:47], v[194:197]
	v_mfma_f32_16x16x128_f8f6f4 v[64:67], v[140:147], v[40:47], v[198:201]
	s_setprio 0
	s_barrier
	s_mov_b32 m0, s45
	s_bitset1_b32 s55, 7
	ds_read_b128 v[32:35], v161 offset:49152
	ds_read_b128 v[36:39], v161 offset:50176
	ds_read_b128 v[162:165], v161 offset:51200
	ds_read_b128 v[166:169], v161 offset:52224
	ds_read_b128 v[170:173], v161 offset:53248
	ds_read_b128 v[174:177], v161 offset:54272
	ds_read_b128 v[178:181], v161 offset:55296
	ds_read_b128 v[182:185], v161 offset:56320
	buffer_load_dwordx4 v223, s[12:15], s55 offen lds
	s_mov_b32 m0, s46
	s_nop 0
	buffer_load_dwordx4 v157, s[12:15], s55 offen lds
	s_add_i32 s55, s55, s30
	s_mov_b32 m0, s52
	s_nop 0
	buffer_load_dwordx4 v223, s[12:15], s55 offen lds
	s_mov_b32 m0, s53
	s_nop 0
	buffer_load_dwordx4 v157, s[12:15], s55 offen lds
	s_mov_b32 m0, s47
	s_nop 0
	buffer_load_dwordx4 v222, s[36:39], s54 offen lds
	s_mov_b32 m0, s48
	s_nop 0
	buffer_load_dwordx4 v156, s[36:39], s54 offen lds
	s_waitcnt vmcnt(8)
	s_waitcnt lgkmcnt(0)
	s_barrier
	s_setprio 1
	v_mfma_f32_16x16x128_f8f6f4 v[60:63], v[0:7], v[32:39], v[60:63]
	v_mfma_f32_16x16x128_f8f6f4 v[56:59], v[16:23], v[32:39], v[56:59]
	v_mfma_f32_16x16x128_f8f6f4 v[44:47], v[0:7], v[162:169], v[202:205]
	v_mfma_f32_16x16x128_f8f6f4 v[40:43], v[16:23], v[162:169], v[206:209]
	v_mfma_f32_16x16x128_f8f6f4 v[28:31], v[0:7], v[170:177], v[210:213]
	v_mfma_f32_16x16x128_f8f6f4 v[24:27], v[16:23], v[170:177], v[214:217]
	v_mfma_f32_16x16x128_f8f6f4 v[12:15], v[0:7], v[178:185], v[230:233]
	v_mfma_f32_16x16x128_f8f6f4 v[8:11], v[16:23], v[178:185], v[234:237]
	v_mfma_f32_16x16x128_f8f6f4 v[52:55], v[132:139], v[32:39], v[52:55]
	v_mfma_f32_16x16x128_f8f6f4 v[48:51], v[140:147], v[32:39], v[48:51]
	v_mfma_f32_16x16x128_f8f6f4 v[36:39], v[132:139], v[162:169], v[238:241]
	v_mfma_f32_16x16x128_f8f6f4 v[32:35], v[140:147], v[162:169], v[242:245]
	v_mfma_f32_16x16x128_f8f6f4 v[20:23], v[132:139], v[170:177], v[246:249]
	v_mfma_f32_16x16x128_f8f6f4 v[16:19], v[140:147], v[170:177], v[250:253]
	v_mfma_f32_16x16x128_f8f6f4 v[4:7], v[132:139], v[178:185], v[190:193]
	v_mfma_f32_16x16x128_f8f6f4 v[0:3], v[140:147], v[178:185], v[152:155]
	s_setprio 0
	s_barrier
	s_add_i32 s11, s11, 2
	s_addk_i32 s4, 0x100
	s_addk_i32 s5, 0x100
	s_cmp_ge_i32 s11, s58
	s_cbranch_scc0 .LBB0_926
	v_mov_b32_e32 v230, 0x358637bd
	v_mov_b32_e32 v233, v159
	v_mov_b32_e32 v231, 1
	v_mov_b32_e32 v234, 0xff61b1e6
	s_and_b64 vcc, exec, s[24:25]
	s_cbranch_vccnz .LBB0_929
	s_branch .LBB0_930

; #define PG8_STAGE(bufoff, rs_, soff_, voff) do { _Pragma("unroll") for (int _i = 0; _i < 2; ++_i) \
;         __builtin_amdgcn_raw_ptr_buffer_load_lds(rs_, (LAS void*)(lds + (bufoff) + ldsw + _i * 8192), 16, (int)(voff)[_i], (int)(soff_), 0, 0); } while (0)
; #define PG8_LDA(dst, b, h) do { _Pragma("unroll") for (int m = 0; m < 4; ++m) dst[m] = PG8_LD2(lds + PG8_SA(b, h) + aoff + m * 2048); } while (0)
; #define PG8_LDB(dst, b, h) do { _Pragma("unroll") for (int n = 0; n < 2; ++n) dst[n] = PG8_LD2(lds + PG8_SB(b, h) + boff + n * 2048); } while (0)
; #define PG8_WAIT_V(n) asm volatile("s_waitcnt vmcnt(" #n ")" ::: "memory")
; #define PG8_WAIT_L(n) asm volatile("s_waitcnt lgkmcnt(" #n ")" ::: "memory")
; #define PG8_BAR __builtin_amdgcn_s_barrier()
; #define PG8_SCHED __builtin_amdgcn_sched_barrier(0)
; template <class Epi, class Sched, bool ALIGN_EPI = false, bool SP2 = false, bool FP8 = false>
; __device__ __forceinline__ void gemm_phase(LAS unsigned char* lds, const Gemm g, const Sched& S, const Epi& E, int wbase) {
;     ...
;             PG8_LDB(B0, 0, 0); PG8_LDB(B1, 0, 1); PG8_SCHED; PG8_LDA(At, 0, 0); PG8_STAGE(PG8_SA(1, 1), rAc, a1 + hstep, voffA);
;             PG8_WAIT_V(8); PG8_WAIT_L(0); PG8_BAR; PG8_MMA(0, 0, At, B0); PG8_MMA(0, 1, At, B1); PG8_BAR; PG8_SCHED;
;             PG8_LDA(At, 0, 1); PG8_STAGE(PG8_SB(0, 0), rB2, b2, voffB); PG8_STAGE(PG8_SB(0, 1), rB2, b2 + hstep, voffB); PG8_STAGE(PG8_SA(0, 0), rA2, a2, voffA);
;             PG8_WAIT_V(8); PG8_WAIT_L(0); PG8_BAR; PG8_MMA(1, 0, At, B0); PG8_MMA(1, 1, At, B1); PG8_BAR; PG8_SCHED;
.LBB0_1004:
	v_add_u32_e32 v132, 0x10000, v180
	v_add_u32_e32 v156, 0x14000, v180
	ds_read_b128 v[96:99], v132
	ds_read_b128 v[108:111], v132 offset:1024
	ds_read_b128 v[120:123], v132 offset:2048
	ds_read_b128 v[132:135], v132 offset:3072
	ds_read_b128 v[136:139], v156
	ds_read_b128 v[144:147], v156 offset:1024
	ds_read_b128 v[152:155], v156 offset:2048
	ds_read_b128 v[156:159], v156 offset:3072
	s_add_i32 s14, s4, 0x80
	s_cmp_eq_u32 s62, s11
	s_cselect_b32 s66, s2, s14
	s_cselect_b32 s55, s3, s5
	s_or_b32 s54, s66, 0x80
	s_add_i32 s14, s33, s4
	s_mov_b32 m0, s63
	ds_read_b128 v[160:163], v181
	ds_read_b128 v[164:167], v181 offset:1024
	ds_read_b128 v[168:171], v181 offset:2048
	ds_read_b128 v[182:185], v181 offset:3072
	ds_read_b128 v[186:189], v181 offset:4096
	ds_read_b128 v[190:193], v181 offset:5120
	ds_read_b128 v[194:197], v181 offset:6144
	ds_read_b128 v[198:201], v181 offset:7168
	buffer_load_dwordx4 v174, s[36:39], s14 offen lds
	s_mov_b32 m0, s65
	s_nop 0
	buffer_load_dwordx4 v176, s[36:39], s14 offen lds
	s_waitcnt vmcnt(8)
	s_waitcnt lgkmcnt(0)
	s_barrier
	s_setprio 1
	v_mfma_f32_16x16x32_bf16 v[148:151], v[96:99], v[160:163], v[148:151]
	v_mfma_f32_16x16x32_bf16 v[140:143], v[120:123], v[160:163], v[140:143]
	v_mfma_f32_16x16x32_bf16 v[116:119], v[96:99], v[168:171], v[116:119]
	v_mfma_f32_16x16x32_bf16 v[112:115], v[120:123], v[168:171], v[112:115]
	v_mfma_f32_16x16x32_bf16 v[92:95], v[96:99], v[186:189], v[92:95]
	v_mfma_f32_16x16x32_bf16 v[88:91], v[120:123], v[186:189], v[88:91]
	v_mfma_f32_16x16x32_bf16 v[76:79], v[96:99], v[194:197], v[76:79]
	v_mfma_f32_16x16x32_bf16 v[72:75], v[120:123], v[194:197], v[72:75]
	v_mfma_f32_16x16x32_bf16 v[148:151], v[108:111], v[164:167], v[148:151]
	v_mfma_f32_16x16x32_bf16 v[140:143], v[132:135], v[164:167], v[140:143]
	v_mfma_f32_16x16x32_bf16 v[116:119], v[108:111], v[182:185], v[116:119]
	v_mfma_f32_16x16x32_bf16 v[112:115], v[132:135], v[182:185], v[112:115]
	v_mfma_f32_16x16x32_bf16 v[92:95], v[108:111], v[190:193], v[92:95]
	v_mfma_f32_16x16x32_bf16 v[88:91], v[132:135], v[190:193], v[88:91]
	v_mfma_f32_16x16x32_bf16 v[76:79], v[108:111], v[198:201], v[76:79]
	v_mfma_f32_16x16x32_bf16 v[72:75], v[132:135], v[198:201], v[72:75]
	v_mfma_f32_16x16x32_bf16 v[128:131], v[136:139], v[160:163], v[128:131]
	v_mfma_f32_16x16x32_bf16 v[124:127], v[152:155], v[160:163], v[124:127]
	v_mfma_f32_16x16x32_bf16 v[104:107], v[136:139], v[168:171], v[104:107]
	v_mfma_f32_16x16x32_bf16 v[100:103], v[152:155], v[168:171], v[100:103]
	v_mfma_f32_16x16x32_bf16 v[84:87], v[136:139], v[186:189], v[84:87]
	v_mfma_f32_16x16x32_bf16 v[80:83], v[152:155], v[186:189], v[80:83]
	v_mfma_f32_16x16x32_bf16 v[68:71], v[136:139], v[194:197], v[68:71]
	v_mfma_f32_16x16x32_bf16 v[64:67], v[152:155], v[194:197], v[64:67]
	v_mfma_f32_16x16x32_bf16 v[128:131], v[144:147], v[164:167], v[128:131]
	v_mfma_f32_16x16x32_bf16 v[124:127], v[156:159], v[164:167], v[124:127]
	v_mfma_f32_16x16x32_bf16 v[104:107], v[144:147], v[182:185], v[104:107]
	v_mfma_f32_16x16x32_bf16 v[100:103], v[156:159], v[182:185], v[100:103]
	v_mfma_f32_16x16x32_bf16 v[84:87], v[144:147], v[190:193], v[84:87]
	v_mfma_f32_16x16x32_bf16 v[80:83], v[156:159], v[190:193], v[80:83]
	v_mfma_f32_16x16x32_bf16 v[68:71], v[144:147], v[198:201], v[68:71]
	v_mfma_f32_16x16x32_bf16 v[64:67], v[156:159], v[198:201], v[64:67]
	s_setprio 0
	s_barrier
	s_mov_b32 m0, s35
	s_mov_b32 s14, s38
	s_mov_b32 s15, s39
	ds_read_b128 v[160:163], v181 offset:16384
	ds_read_b128 v[164:167], v181 offset:17408
	ds_read_b128 v[168:171], v181 offset:18432
	ds_read_b128 v[182:185], v181 offset:19456
	ds_read_b128 v[186:189], v181 offset:20480
	ds_read_b128 v[190:193], v181 offset:21504
	ds_read_b128 v[194:197], v181 offset:22528
	ds_read_b128 v[198:201], v181 offset:23552
	buffer_load_dwordx4 v175, s[12:15], s55 offen lds
	s_mov_b32 m0, s41
	s_add_i32 s67, s55, s33
	buffer_load_dwordx4 v177, s[12:15], s55 offen lds
	s_mov_b32 m0, s42
	s_nop 0
	buffer_load_dwordx4 v175, s[12:15], s67 offen lds
	s_mov_b32 m0, s43
	s_nop 0
	buffer_load_dwordx4 v177, s[12:15], s67 offen lds
	s_mov_b32 m0, s34
	s_nop 0
	buffer_load_dwordx4 v174, s[36:39], s66 offen lds
	s_mov_b32 m0, s44
	s_nop 0
	buffer_load_dwordx4 v176, s[36:39], s66 offen lds
	s_waitcnt vmcnt(8)
	s_waitcnt lgkmcnt(0)
	s_barrier
	s_setprio 1
	v_mfma_f32_16x16x32_bf16 v[60:63], v[96:99], v[160:163], v[60:63]
	v_mfma_f32_16x16x32_bf16 v[56:59], v[120:123], v[160:163], v[56:59]
	v_mfma_f32_16x16x32_bf16 v[44:47], v[96:99], v[168:171], v[44:47]
	v_mfma_f32_16x16x32_bf16 v[40:43], v[120:123], v[168:171], v[40:43]
	v_mfma_f32_16x16x32_bf16 v[28:31], v[96:99], v[186:189], v[28:31]
	v_mfma_f32_16x16x32_bf16 v[24:27], v[120:123], v[186:189], v[24:27]
	v_mfma_f32_16x16x32_bf16 v[12:15], v[96:99], v[194:197], v[12:15]
	v_mfma_f32_16x16x32_bf16 v[8:11], v[120:123], v[194:197], v[8:11]
	v_mfma_f32_16x16x32_bf16 v[60:63], v[108:111], v[164:167], v[60:63]
	v_mfma_f32_16x16x32_bf16 v[56:59], v[132:135], v[164:167], v[56:59]
	v_mfma_f32_16x16x32_bf16 v[44:47], v[108:111], v[182:185], v[44:47]
	v_mfma_f32_16x16x32_bf16 v[40:43], v[132:135], v[182:185], v[40:43]
	v_mfma_f32_16x16x32_bf16 v[28:31], v[108:111], v[190:193], v[28:31]
	v_mfma_f32_16x16x32_bf16 v[24:27], v[132:135], v[190:193], v[24:27]
	v_mfma_f32_16x16x32_bf16 v[12:15], v[108:111], v[198:201], v[12:15]
	v_mfma_f32_16x16x32_bf16 v[8:11], v[132:135], v[198:201], v[8:11]
	v_mfma_f32_16x16x32_bf16 v[52:55], v[136:139], v[160:163], v[52:55]
	v_mfma_f32_16x16x32_bf16 v[48:51], v[152:155], v[160:163], v[48:51]
	v_mfma_f32_16x16x32_bf16 v[36:39], v[136:139], v[168:171], v[36:39]
	v_mfma_f32_16x16x32_bf16 v[32:35], v[152:155], v[168:171], v[32:35]
	v_mfma_f32_16x16x32_bf16 v[20:23], v[136:139], v[186:189], v[20:23]
	v_mfma_f32_16x16x32_bf16 v[16:19], v[152:155], v[186:189], v[16:19]
	v_mfma_f32_16x16x32_bf16 v[4:7], v[136:139], v[194:197], v[4:7]
	v_mfma_f32_16x16x32_bf16 v[0:3], v[152:155], v[194:197], v[0:3]
	v_mfma_f32_16x16x32_bf16 v[52:55], v[144:147], v[164:167], v[52:55]
	v_mfma_f32_16x16x32_bf16 v[48:51], v[156:159], v[164:167], v[48:51]
	v_mfma_f32_16x16x32_bf16 v[36:39], v[144:147], v[182:185], v[36:39]
	v_mfma_f32_16x16x32_bf16 v[32:35], v[156:159], v[182:185], v[32:35]
	v_mfma_f32_16x16x32_bf16 v[20:23], v[144:147], v[190:193], v[20:23]
	v_mfma_f32_16x16x32_bf16 v[16:19], v[156:159], v[190:193], v[16:19]
	v_mfma_f32_16x16x32_bf16 v[4:7], v[144:147], v[198:201], v[4:7]
	v_mfma_f32_16x16x32_bf16 v[0:3], v[156:159], v[198:201], v[0:3]
	s_setprio 0
	s_barrier
; #define PG8_STAGE(bufoff, rs_, soff_, voff) do { _Pragma("unroll") for (int _i = 0; _i < 2; ++_i) \
;         __builtin_amdgcn_raw_ptr_buffer_load_lds(rs_, (LAS void*)(lds + (bufoff) + ldsw + _i * 8192), 16, (int)(voff)[_i], (int)(soff_), 0, 0); } while (0)
; #define PG8_LDA(dst, b, h) do { _Pragma("unroll") for (int m = 0; m < 4; ++m) dst[m] = PG8_LD2(lds + PG8_SA(b, h) + aoff + m * 2048); } while (0)
; #define PG8_LDB(dst, b, h) do { _Pragma("unroll") for (int n = 0; n < 2; ++n) dst[n] = PG8_LD2(lds + PG8_SB(b, h) + boff + n * 2048); } while (0)
; #define PG8_WAIT_V(n) asm volatile("s_waitcnt vmcnt(" #n ")" ::: "memory")
; #define PG8_WAIT_L(n) asm volatile("s_waitcnt lgkmcnt(" #n ")" ::: "memory")
; #define PG8_BAR __builtin_amdgcn_s_barrier()
; #define PG8_SCHED __builtin_amdgcn_sched_barrier(0)
; template <class Epi, class Sched, bool ALIGN_EPI = false, bool SP2 = false, bool FP8 = false>
; __device__ __forceinline__ void gemm_phase(LAS unsigned char* lds, const Gemm g, const Sched& S, const Epi& E, int wbase) {
;     ...
;             PG8_LDB(B0, 1, 0); PG8_LDB(B1, 1, 1); PG8_SCHED; PG8_LDA(At, 1, 0); PG8_STAGE(PG8_SA(0, 1), rA2, a2 + hstep, voffA);
;             PG8_WAIT_V(8); PG8_WAIT_L(0); PG8_BAR; PG8_MMA(0, 0, At, B0); PG8_MMA(0, 1, At, B1); PG8_BAR; PG8_SCHED;
;             PG8_LDA(At, 1, 1); PG8_STAGE(PG8_SB(1, 0), rB2, b3, voffB); PG8_STAGE(PG8_SB(1, 1), rB2, b3 + hstep, voffB); PG8_STAGE(PG8_SA(1, 0), rA2, a3, voffA);
;             PG8_WAIT_V(8); PG8_WAIT_L(0); PG8_BAR; PG8_MMA(1, 0, At, B0); PG8_MMA(1, 1, At, B1); PG8_BAR; PG8_SCHED;
	v_add_u32_e32 v132, 0x18000, v180
	v_add_u32_e32 v156, 0x1c000, v180
	ds_read_b128 v[96:99], v132
	ds_read_b128 v[108:111], v132 offset:1024
	ds_read_b128 v[120:123], v132 offset:2048
	ds_read_b128 v[132:135], v132 offset:3072
	ds_read_b128 v[136:139], v156
	ds_read_b128 v[144:147], v156 offset:1024
	ds_read_b128 v[152:155], v156 offset:2048
	ds_read_b128 v[156:159], v156 offset:3072
	s_add_i32 s66, s66, s33
	s_mov_b32 m0, s45
	ds_read_b128 v[160:163], v181 offset:32768
	ds_read_b128 v[164:167], v181 offset:33792
	ds_read_b128 v[168:171], v181 offset:34816
	ds_read_b128 v[182:185], v181 offset:35840
	ds_read_b128 v[186:189], v181 offset:36864
	ds_read_b128 v[190:193], v181 offset:37888
	ds_read_b128 v[194:197], v181 offset:38912
	ds_read_b128 v[198:201], v181 offset:39936
	buffer_load_dwordx4 v174, s[36:39], s66 offen lds
	s_mov_b32 m0, s46
	s_nop 0
	buffer_load_dwordx4 v176, s[36:39], s66 offen lds
	s_waitcnt vmcnt(8)
	s_waitcnt lgkmcnt(0)
	s_barrier
	s_setprio 1
	v_mfma_f32_16x16x32_bf16 v[148:151], v[96:99], v[160:163], v[148:151]
	v_mfma_f32_16x16x32_bf16 v[140:143], v[120:123], v[160:163], v[140:143]
	v_mfma_f32_16x16x32_bf16 v[116:119], v[96:99], v[168:171], v[116:119]
	v_mfma_f32_16x16x32_bf16 v[112:115], v[120:123], v[168:171], v[112:115]
	v_mfma_f32_16x16x32_bf16 v[92:95], v[96:99], v[186:189], v[92:95]
	v_mfma_f32_16x16x32_bf16 v[88:91], v[120:123], v[186:189], v[88:91]
	v_mfma_f32_16x16x32_bf16 v[76:79], v[96:99], v[194:197], v[76:79]
	v_mfma_f32_16x16x32_bf16 v[72:75], v[120:123], v[194:197], v[72:75]
	v_mfma_f32_16x16x32_bf16 v[148:151], v[108:111], v[164:167], v[148:151]
	v_mfma_f32_16x16x32_bf16 v[140:143], v[132:135], v[164:167], v[140:143]
	v_mfma_f32_16x16x32_bf16 v[116:119], v[108:111], v[182:185], v[116:119]
	v_mfma_f32_16x16x32_bf16 v[112:115], v[132:135], v[182:185], v[112:115]
	v_mfma_f32_16x16x32_bf16 v[92:95], v[108:111], v[190:193], v[92:95]
	v_mfma_f32_16x16x32_bf16 v[88:91], v[132:135], v[190:193], v[88:91]
	v_mfma_f32_16x16x32_bf16 v[76:79], v[108:111], v[198:201], v[76:79]
	v_mfma_f32_16x16x32_bf16 v[72:75], v[132:135], v[198:201], v[72:75]
	v_mfma_f32_16x16x32_bf16 v[128:131], v[136:139], v[160:163], v[128:131]
	v_mfma_f32_16x16x32_bf16 v[124:127], v[152:155], v[160:163], v[124:127]
	v_mfma_f32_16x16x32_bf16 v[104:107], v[136:139], v[168:171], v[104:107]
	v_mfma_f32_16x16x32_bf16 v[100:103], v[152:155], v[168:171], v[100:103]
	v_mfma_f32_16x16x32_bf16 v[84:87], v[136:139], v[186:189], v[84:87]
	v_mfma_f32_16x16x32_bf16 v[80:83], v[152:155], v[186:189], v[80:83]
	v_mfma_f32_16x16x32_bf16 v[68:71], v[136:139], v[194:197], v[68:71]
	v_mfma_f32_16x16x32_bf16 v[64:67], v[152:155], v[194:197], v[64:67]
	v_mfma_f32_16x16x32_bf16 v[128:131], v[144:147], v[164:167], v[128:131]
	v_mfma_f32_16x16x32_bf16 v[124:127], v[156:159], v[164:167], v[124:127]
	v_mfma_f32_16x16x32_bf16 v[104:107], v[144:147], v[182:185], v[104:107]
	v_mfma_f32_16x16x32_bf16 v[100:103], v[156:159], v[182:185], v[100:103]
	v_mfma_f32_16x16x32_bf16 v[84:87], v[144:147], v[190:193], v[84:87]
	v_mfma_f32_16x16x32_bf16 v[80:83], v[156:159], v[190:193], v[80:83]
	v_mfma_f32_16x16x32_bf16 v[68:71], v[144:147], v[198:201], v[68:71]
	v_mfma_f32_16x16x32_bf16 v[64:67], v[156:159], v[198:201], v[64:67]
	s_setprio 0
	s_barrier
	s_mov_b32 m0, s47
	s_bitset1_b32 s55, 7
	ds_read_b128 v[160:163], v181 offset:49152
	ds_read_b128 v[164:167], v181 offset:50176
	ds_read_b128 v[168:171], v181 offset:51200
	ds_read_b128 v[182:185], v181 offset:52224
	ds_read_b128 v[186:189], v181 offset:53248
	ds_read_b128 v[190:193], v181 offset:54272
	ds_read_b128 v[194:197], v181 offset:55296
	ds_read_b128 v[198:201], v181 offset:56320
	buffer_load_dwordx4 v175, s[12:15], s55 offen lds
	s_mov_b32 m0, s48
	s_nop 0
	buffer_load_dwordx4 v177, s[12:15], s55 offen lds
	s_add_i32 s55, s55, s33
	s_mov_b32 m0, s56
	s_nop 0
	buffer_load_dwordx4 v175, s[12:15], s55 offen lds
	s_mov_b32 m0, s57
	s_nop 0
	buffer_load_dwordx4 v177, s[12:15], s55 offen lds
	s_mov_b32 m0, s52
	s_nop 0
	buffer_load_dwordx4 v174, s[36:39], s54 offen lds
	s_mov_b32 m0, s53
	s_nop 0
	buffer_load_dwordx4 v176, s[36:39], s54 offen lds
	s_waitcnt vmcnt(8)
	s_waitcnt lgkmcnt(0)
	s_barrier
	s_setprio 1
	v_mfma_f32_16x16x32_bf16 v[60:63], v[96:99], v[160:163], v[60:63]
	v_mfma_f32_16x16x32_bf16 v[56:59], v[120:123], v[160:163], v[56:59]
	v_mfma_f32_16x16x32_bf16 v[44:47], v[96:99], v[168:171], v[44:47]
	v_mfma_f32_16x16x32_bf16 v[40:43], v[120:123], v[168:171], v[40:43]
	v_mfma_f32_16x16x32_bf16 v[28:31], v[96:99], v[186:189], v[28:31]
	v_mfma_f32_16x16x32_bf16 v[24:27], v[120:123], v[186:189], v[24:27]
	v_mfma_f32_16x16x32_bf16 v[12:15], v[96:99], v[194:197], v[12:15]
	v_mfma_f32_16x16x32_bf16 v[8:11], v[120:123], v[194:197], v[8:11]
	v_mfma_f32_16x16x32_bf16 v[60:63], v[108:111], v[164:167], v[60:63]
	v_mfma_f32_16x16x32_bf16 v[56:59], v[132:135], v[164:167], v[56:59]
	v_mfma_f32_16x16x32_bf16 v[44:47], v[108:111], v[182:185], v[44:47]
	v_mfma_f32_16x16x32_bf16 v[40:43], v[132:135], v[182:185], v[40:43]
	v_mfma_f32_16x16x32_bf16 v[28:31], v[108:111], v[190:193], v[28:31]
	v_mfma_f32_16x16x32_bf16 v[24:27], v[132:135], v[190:193], v[24:27]
	v_mfma_f32_16x16x32_bf16 v[12:15], v[108:111], v[198:201], v[12:15]
	v_mfma_f32_16x16x32_bf16 v[8:11], v[132:135], v[198:201], v[8:11]
	v_mfma_f32_16x16x32_bf16 v[52:55], v[136:139], v[160:163], v[52:55]
	v_mfma_f32_16x16x32_bf16 v[48:51], v[152:155], v[160:163], v[48:51]
	v_mfma_f32_16x16x32_bf16 v[36:39], v[136:139], v[168:171], v[36:39]
	v_mfma_f32_16x16x32_bf16 v[32:35], v[152:155], v[168:171], v[32:35]
	v_mfma_f32_16x16x32_bf16 v[20:23], v[136:139], v[186:189], v[20:23]
	v_mfma_f32_16x16x32_bf16 v[16:19], v[152:155], v[186:189], v[16:19]
	v_mfma_f32_16x16x32_bf16 v[4:7], v[136:139], v[194:197], v[4:7]
	v_mfma_f32_16x16x32_bf16 v[0:3], v[152:155], v[194:197], v[0:3]
	v_mfma_f32_16x16x32_bf16 v[52:55], v[144:147], v[164:167], v[52:55]
	v_mfma_f32_16x16x32_bf16 v[48:51], v[156:159], v[164:167], v[48:51]
	v_mfma_f32_16x16x32_bf16 v[36:39], v[144:147], v[182:185], v[36:39]
	v_mfma_f32_16x16x32_bf16 v[32:35], v[156:159], v[182:185], v[32:35]
	v_mfma_f32_16x16x32_bf16 v[20:23], v[144:147], v[190:193], v[20:23]
	v_mfma_f32_16x16x32_bf16 v[16:19], v[156:159], v[190:193], v[16:19]
	v_mfma_f32_16x16x32_bf16 v[4:7], v[144:147], v[198:201], v[4:7]
	v_mfma_f32_16x16x32_bf16 v[0:3], v[156:159], v[198:201], v[0:3]
	s_setprio 0
	s_barrier
	s_add_i32 s11, s11, 2
	s_addk_i32 s4, 0x100
	s_addk_i32 s5, 0x100
	s_cmp_ge_i32 s11, s60
	s_cbranch_scc0 .LBB0_1004
	s_and_b64 vcc, exec, s[26:27]
	s_cbranch_vccz .LBB0_1007

; #define PG8_STAGE(bufoff, rs_, soff_, voff) do { _Pragma("unroll") for (int _i = 0; _i < 2; ++_i) \
;         __builtin_amdgcn_raw_ptr_buffer_load_lds(rs_, (LAS void*)(lds + (bufoff) + ldsw + _i * 8192), 16, (int)(voff)[_i], (int)(soff_), 0, 0); } while (0)
; #define PG8_LDA(dst, b, h) do { _Pragma("unroll") for (int m = 0; m < 4; ++m) dst[m] = PG8_LD2(lds + PG8_SA(b, h) + aoff + m * 2048); } while (0)
; #define PG8_LDB(dst, b, h) do { _Pragma("unroll") for (int n = 0; n < 2; ++n) dst[n] = PG8_LD2(lds + PG8_SB(b, h) + boff + n * 2048); } while (0)
; #define PG8_WAIT_V(n) asm volatile("s_waitcnt vmcnt(" #n ")" ::: "memory")
; #define PG8_WAIT_L(n) asm volatile("s_waitcnt lgkmcnt(" #n ")" ::: "memory")
; #define PG8_BAR __builtin_amdgcn_s_barrier()
; #define PG8_SCHED __builtin_amdgcn_sched_barrier(0)
; template <class Epi, class Sched, bool ALIGN_EPI = false, bool SP2 = false, bool FP8 = false>
; __device__ __forceinline__ void gemm_phase(LAS unsigned char* lds, const Gemm g, const Sched& S, const Epi& E, int wbase) {
;     ...
;             PG8_LDB(B0, 0, 0); PG8_LDB(B1, 0, 1); PG8_SCHED; PG8_LDA(At, 0, 0); PG8_STAGE(PG8_SA(1, 1), rAc, a1 + hstep, voffA);
;             PG8_WAIT_V(8); PG8_WAIT_L(0); PG8_BAR; PG8_MMA(0, 0, At, B0); PG8_MMA(0, 1, At, B1); PG8_BAR; PG8_SCHED;
;             PG8_LDA(At, 0, 1); PG8_STAGE(PG8_SB(0, 0), rB2, b2, voffB); PG8_STAGE(PG8_SB(0, 1), rB2, b2 + hstep, voffB); PG8_STAGE(PG8_SA(0, 0), rA2, a2, voffA);
.LBB0_1348:
	v_add_u32_e32 v12, 0x10000, v199
	v_add_u32_e32 v28, 0x14000, v199
	ds_read_b128 v[0:3], v12
	ds_read_b128 v[4:7], v12 offset:1024
	ds_read_b128 v[8:11], v12 offset:2048
	ds_read_b128 v[12:15], v12 offset:3072
	ds_read_b128 v[16:19], v28
	ds_read_b128 v[20:23], v28 offset:1024
	ds_read_b128 v[24:27], v28 offset:2048
	ds_read_b128 v[28:31], v28 offset:3072
	s_add_i32 s6, s67, 0x80
	s_cmp_eq_u32 s65, s85
	s_cselect_b32 s54, s66, s6
	s_cselect_b64 vcc, -1, 0
	v_cndmask_b32_e32 v211, v210, v201, vcc
	s_or_b32 s78, s54, 0x80
	s_add_i32 s6, s41, s67
	s_mov_b32 m0, s76
	ds_read_b128 v[32:35], v200
	ds_read_b128 v[36:39], v200 offset:1024
	ds_read_b128 v[40:43], v200 offset:2048
	ds_read_b128 v[44:47], v200 offset:3072
	ds_read_b128 v[48:51], v200 offset:4096
	ds_read_b128 v[52:55], v200 offset:5120
	ds_read_b128 v[56:59], v200 offset:6144
	ds_read_b128 v[60:63], v200 offset:7168
	buffer_load_dwordx4 v192, s[36:39], s6 offen lds
	s_mov_b32 m0, s77
	s_nop 0
	buffer_load_dwordx4 v195, s[36:39], s6 offen lds
	s_waitcnt vmcnt(8)
	s_waitcnt lgkmcnt(0)
	s_barrier
	s_setprio 1
	v_mfma_f32_16x16x128_f8f6f4 v[184:187], v[0:7], v[32:39], v[184:187]
	v_mfma_f32_16x16x128_f8f6f4 v[188:191], v[8:15], v[32:39], v[188:191]
	v_mfma_f32_16x16x128_f8f6f4 v[168:171], v[0:7], v[40:47], v[168:171]
	v_mfma_f32_16x16x128_f8f6f4 v[172:175], v[8:15], v[40:47], v[172:175]
	v_mfma_f32_16x16x128_f8f6f4 v[152:155], v[0:7], v[48:55], v[152:155]
	v_mfma_f32_16x16x128_f8f6f4 v[156:159], v[8:15], v[48:55], v[156:159]
	v_mfma_f32_16x16x128_f8f6f4 v[136:139], v[0:7], v[56:63], v[136:139]
	v_mfma_f32_16x16x128_f8f6f4 v[140:143], v[8:15], v[56:63], v[140:143]
	v_mfma_f32_16x16x128_f8f6f4 v[176:179], v[16:23], v[32:39], v[176:179]
	v_mfma_f32_16x16x128_f8f6f4 v[180:183], v[24:31], v[32:39], v[180:183]
	v_mfma_f32_16x16x128_f8f6f4 v[160:163], v[16:23], v[40:47], v[160:163]
	v_mfma_f32_16x16x128_f8f6f4 v[164:167], v[24:31], v[40:47], v[164:167]
	v_mfma_f32_16x16x128_f8f6f4 v[144:147], v[16:23], v[48:55], v[144:147]
	v_mfma_f32_16x16x128_f8f6f4 v[148:151], v[24:31], v[48:55], v[148:151]
	v_mfma_f32_16x16x128_f8f6f4 v[128:131], v[16:23], v[56:63], v[128:131]
	v_mfma_f32_16x16x128_f8f6f4 v[132:135], v[24:31], v[56:63], v[132:135]
	s_setprio 0
	s_barrier
	ds_read_b128 v[32:35], v200 offset:16384
	ds_read_b128 v[36:39], v200 offset:17408
	ds_read_b128 v[40:43], v200 offset:18432
	ds_read_b128 v[44:47], v200 offset:19456
	ds_read_b128 v[48:51], v200 offset:20480
	ds_read_b128 v[52:55], v200 offset:21504
	ds_read_b128 v[56:59], v200 offset:22528
	ds_read_b128 v[60:63], v200 offset:23552
	s_mov_b32 s6, s38
	s_mov_b32 s7, s39
	s_mov_b64 s[20:21], exec
	s_mov_b32 m0, s43

; #define PG8_STAGE(bufoff, rs_, soff_, voff) do { _Pragma("unroll") for (int _i = 0; _i < 2; ++_i) \
;         __builtin_amdgcn_raw_ptr_buffer_load_lds(rs_, (LAS void*)(lds + (bufoff) + ldsw + _i * 8192), 16, (int)(voff)[_i], (int)(soff_), 0, 0); } while (0)
; #define PG8_LDA(dst, b, h) do { _Pragma("unroll") for (int m = 0; m < 4; ++m) dst[m] = PG8_LD2(lds + PG8_SA(b, h) + aoff + m * 2048); } while (0)
; #define PG8_LDB(dst, b, h) do { _Pragma("unroll") for (int n = 0; n < 2; ++n) dst[n] = PG8_LD2(lds + PG8_SB(b, h) + boff + n * 2048); } while (0)
; #define PG8_WAIT_V(n) asm volatile("s_waitcnt vmcnt(" #n ")" ::: "memory")
; #define PG8_WAIT_L(n) asm volatile("s_waitcnt lgkmcnt(" #n ")" ::: "memory")
; #define PG8_BAR __builtin_amdgcn_s_barrier()
; #define PG8_SCHED __builtin_amdgcn_sched_barrier(0)
; template <class Epi, class Sched, bool ALIGN_EPI = false, bool SP2 = false, bool FP8 = false>
; __device__ __forceinline__ void gemm_phase(LAS unsigned char* lds, const Gemm g, const Sched& S, const Epi& E, int wbase) {
;     ...
;             PG8_LDA(At, 0, 1); PG8_STAGE(PG8_SB(0, 0), rB2, b2, voffB); PG8_STAGE(PG8_SB(0, 1), rB2, b2 + hstep, voffB); PG8_STAGE(PG8_SA(0, 0), rA2, a2, voffA);
;             PG8_WAIT_V(8); PG8_WAIT_L(0); PG8_BAR; PG8_MMA(1, 0, At, B0); PG8_MMA(1, 1, At, B1); PG8_BAR; PG8_SCHED;
;             PG8_LDB(B0, 1, 0); PG8_LDB(B1, 1, 1); PG8_SCHED; PG8_LDA(At, 1, 0); PG8_STAGE(PG8_SA(0, 1), rA2, a2 + hstep, voffA);
;             PG8_WAIT_V(8); PG8_WAIT_L(0); PG8_BAR; PG8_MMA(0, 0, At, B0); PG8_MMA(0, 1, At, B1); PG8_BAR; PG8_SCHED;
;             PG8_LDA(At, 1, 1); PG8_STAGE(PG8_SB(1, 0), rB2, b3, voffB); PG8_STAGE(PG8_SB(1, 1), rB2, b3 + hstep, voffB); PG8_STAGE(PG8_SA(1, 0), rA2, a3, voffA);
.LBB0_1355:
	v_readfirstlane_b32 s55, v212
	s_nop 1
	v_cmp_eq_u32_e32 vcc, s55, v212
	s_and_saveexec_b64 vcc, vcc
	s_nop 0
	buffer_load_dwordx4 v196, s[4:7], s55 offen lds
	s_xor_b64 exec, exec, vcc
	s_cbranch_execnz .LBB0_1355
	s_mov_b64 exec, s[20:21]
	s_mov_b32 m0, s42
	s_nop 0
	buffer_load_dwordx4 v192, s[36:39], s54 offen lds
	s_mov_b32 m0, s47
	s_nop 0
	buffer_load_dwordx4 v195, s[36:39], s54 offen lds
	s_waitcnt vmcnt(8)
	s_waitcnt lgkmcnt(0)
	s_barrier
	s_setprio 1
	v_mfma_f32_16x16x128_f8f6f4 v[120:123], v[0:7], v[32:39], v[120:123]
	v_mfma_f32_16x16x128_f8f6f4 v[124:127], v[8:15], v[32:39], v[124:127]
	v_mfma_f32_16x16x128_f8f6f4 v[104:107], v[0:7], v[40:47], v[104:107]
	v_mfma_f32_16x16x128_f8f6f4 v[108:111], v[8:15], v[40:47], v[108:111]
	v_mfma_f32_16x16x128_f8f6f4 v[88:91], v[0:7], v[48:55], v[88:91]
	v_mfma_f32_16x16x128_f8f6f4 v[92:95], v[8:15], v[48:55], v[92:95]
	v_mfma_f32_16x16x128_f8f6f4 v[72:75], v[0:7], v[56:63], v[72:75]
	v_mfma_f32_16x16x128_f8f6f4 v[76:79], v[8:15], v[56:63], v[76:79]
	v_mfma_f32_16x16x128_f8f6f4 v[112:115], v[16:23], v[32:39], v[112:115]
	v_mfma_f32_16x16x128_f8f6f4 v[116:119], v[24:31], v[32:39], v[116:119]
	v_mfma_f32_16x16x128_f8f6f4 v[96:99], v[16:23], v[40:47], v[96:99]
	v_mfma_f32_16x16x128_f8f6f4 v[100:103], v[24:31], v[40:47], v[100:103]
	v_mfma_f32_16x16x128_f8f6f4 v[80:83], v[16:23], v[48:55], v[80:83]
	v_mfma_f32_16x16x128_f8f6f4 v[84:87], v[24:31], v[48:55], v[84:87]
	v_mfma_f32_16x16x128_f8f6f4 v[68:71], v[16:23], v[56:63], v[68:71]
	v_mfma_f32_16x16x128_f8f6f4 v[64:67], v[24:31], v[56:63], v[64:67]
	s_setprio 0
	s_barrier
	v_add_u32_e32 v12, 0x18000, v199
	v_add_u32_e32 v28, 0x1c000, v199
	ds_read_b128 v[0:3], v12
	ds_read_b128 v[4:7], v12 offset:1024
	ds_read_b128 v[8:11], v12 offset:2048
	ds_read_b128 v[12:15], v12 offset:3072
	ds_read_b128 v[16:19], v28
	ds_read_b128 v[20:23], v28 offset:1024
	ds_read_b128 v[24:27], v28 offset:2048
	ds_read_b128 v[28:31], v28 offset:3072
	s_add_i32 s54, s54, s41
	s_mov_b32 m0, s48
	ds_read_b128 v[32:35], v200 offset:32768
	ds_read_b128 v[36:39], v200 offset:33792
	ds_read_b128 v[40:43], v200 offset:34816
	ds_read_b128 v[44:47], v200 offset:35840
	ds_read_b128 v[48:51], v200 offset:36864
	ds_read_b128 v[52:55], v200 offset:37888
	ds_read_b128 v[56:59], v200 offset:38912
	ds_read_b128 v[60:63], v200 offset:39936
	buffer_load_dwordx4 v192, s[36:39], s54 offen lds
	s_mov_b32 m0, s52
	s_nop 0
	buffer_load_dwordx4 v195, s[36:39], s54 offen lds
	s_waitcnt vmcnt(8)
	s_waitcnt lgkmcnt(0)
	s_barrier
	s_setprio 1
	v_mfma_f32_16x16x128_f8f6f4 v[184:187], v[0:7], v[32:39], v[184:187]
	v_mfma_f32_16x16x128_f8f6f4 v[188:191], v[8:15], v[32:39], v[188:191]
	v_mfma_f32_16x16x128_f8f6f4 v[168:171], v[0:7], v[40:47], v[168:171]
	v_mfma_f32_16x16x128_f8f6f4 v[172:175], v[8:15], v[40:47], v[172:175]
	v_mfma_f32_16x16x128_f8f6f4 v[152:155], v[0:7], v[48:55], v[152:155]
	v_mfma_f32_16x16x128_f8f6f4 v[156:159], v[8:15], v[48:55], v[156:159]
	v_mfma_f32_16x16x128_f8f6f4 v[136:139], v[0:7], v[56:63], v[136:139]
	v_mfma_f32_16x16x128_f8f6f4 v[140:143], v[8:15], v[56:63], v[140:143]
	v_mfma_f32_16x16x128_f8f6f4 v[176:179], v[16:23], v[32:39], v[176:179]
	v_mfma_f32_16x16x128_f8f6f4 v[180:183], v[24:31], v[32:39], v[180:183]
	v_mfma_f32_16x16x128_f8f6f4 v[160:163], v[16:23], v[40:47], v[160:163]
	v_mfma_f32_16x16x128_f8f6f4 v[164:167], v[24:31], v[40:47], v[164:167]
	v_mfma_f32_16x16x128_f8f6f4 v[144:147], v[16:23], v[48:55], v[144:147]
	v_mfma_f32_16x16x128_f8f6f4 v[148:151], v[24:31], v[48:55], v[148:151]
	v_mfma_f32_16x16x128_f8f6f4 v[128:131], v[16:23], v[56:63], v[128:131]
	v_mfma_f32_16x16x128_f8f6f4 v[132:135], v[24:31], v[56:63], v[132:135]
	s_setprio 0
	s_barrier
	ds_read_b128 v[32:35], v200 offset:49152
	ds_read_b128 v[36:39], v200 offset:50176
	ds_read_b128 v[40:43], v200 offset:51200
	ds_read_b128 v[44:47], v200 offset:52224
	ds_read_b128 v[48:51], v200 offset:53248
	ds_read_b128 v[52:55], v200 offset:54272
	ds_read_b128 v[56:59], v200 offset:55296
	ds_read_b128 v[60:63], v200 offset:56320
	v_add_u32_e32 v211, 0x80, v211
	s_mov_b64 s[20:21], exec
	s_mov_b32 m0, s57

; #define PG8_STAGE(bufoff, rs_, soff_, voff) do { _Pragma("unroll") for (int _i = 0; _i < 2; ++_i) \
;         __builtin_amdgcn_raw_ptr_buffer_load_lds(rs_, (LAS void*)(lds + (bufoff) + ldsw + _i * 8192), 16, (int)(voff)[_i], (int)(soff_), 0, 0); } while (0)
; #define PG8_LDA(dst, b, h) do { _Pragma("unroll") for (int m = 0; m < 4; ++m) dst[m] = PG8_LD2(lds + PG8_SA(b, h) + aoff + m * 2048); } while (0)
; #define PG8_WAIT_V(n) asm volatile("s_waitcnt vmcnt(" #n ")" ::: "memory")
; #define PG8_WAIT_L(n) asm volatile("s_waitcnt lgkmcnt(" #n ")" ::: "memory")
; #define PG8_BAR __builtin_amdgcn_s_barrier()
; #define PG8_SCHED __builtin_amdgcn_sched_barrier(0)
; template <class Epi, class Sched, bool ALIGN_EPI = false, bool SP2 = false, bool FP8 = false>
; __device__ __forceinline__ void gemm_phase(LAS unsigned char* lds, const Gemm g, const Sched& S, const Epi& E, int wbase) {
;     ...
;             PG8_LDA(At, 1, 1); PG8_STAGE(PG8_SB(1, 0), rB2, b3, voffB); PG8_STAGE(PG8_SB(1, 1), rB2, b3 + hstep, voffB); PG8_STAGE(PG8_SA(1, 0), rA2, a3, voffA);
;             PG8_WAIT_V(8); PG8_WAIT_L(0); PG8_BAR; PG8_MMA(1, 0, At, B0); PG8_MMA(1, 1, At, B1); PG8_BAR; PG8_SCHED;
.LBB0_1363:
	v_readfirstlane_b32 s54, v211
	s_nop 1
	v_cmp_eq_u32_e32 vcc, s54, v211
	s_and_saveexec_b64 vcc, vcc
	s_nop 0
	buffer_load_dwordx4 v196, s[4:7], s54 offen lds
	s_xor_b64 exec, exec, vcc
	s_cbranch_execnz .LBB0_1363
	s_mov_b64 exec, s[20:21]
	s_mov_b32 m0, s59
	s_nop 0
	buffer_load_dwordx4 v192, s[36:39], s78 offen lds
	s_mov_b32 m0, s60
	s_nop 0
	buffer_load_dwordx4 v195, s[36:39], s78 offen lds
	s_waitcnt vmcnt(8)
	s_waitcnt lgkmcnt(0)
	s_barrier
	s_setprio 1
	v_mfma_f32_16x16x128_f8f6f4 v[120:123], v[0:7], v[32:39], v[120:123]
	v_mfma_f32_16x16x128_f8f6f4 v[124:127], v[8:15], v[32:39], v[124:127]
	v_mfma_f32_16x16x128_f8f6f4 v[104:107], v[0:7], v[40:47], v[104:107]
	v_mfma_f32_16x16x128_f8f6f4 v[108:111], v[8:15], v[40:47], v[108:111]
	v_mfma_f32_16x16x128_f8f6f4 v[88:91], v[0:7], v[48:55], v[88:91]
	v_mfma_f32_16x16x128_f8f6f4 v[92:95], v[8:15], v[48:55], v[92:95]
	v_mfma_f32_16x16x128_f8f6f4 v[72:75], v[0:7], v[56:63], v[72:75]
	v_mfma_f32_16x16x128_f8f6f4 v[76:79], v[8:15], v[56:63], v[76:79]
	v_mfma_f32_16x16x128_f8f6f4 v[112:115], v[16:23], v[32:39], v[112:115]
	v_mfma_f32_16x16x128_f8f6f4 v[116:119], v[24:31], v[32:39], v[116:119]
	v_mfma_f32_16x16x128_f8f6f4 v[96:99], v[16:23], v[40:47], v[96:99]
	v_mfma_f32_16x16x128_f8f6f4 v[100:103], v[24:31], v[40:47], v[100:103]
	v_mfma_f32_16x16x128_f8f6f4 v[80:83], v[16:23], v[48:55], v[80:83]
	v_mfma_f32_16x16x128_f8f6f4 v[84:87], v[24:31], v[48:55], v[84:87]
	v_mfma_f32_16x16x128_f8f6f4 v[68:71], v[16:23], v[56:63], v[68:71]
	v_mfma_f32_16x16x128_f8f6f4 v[64:67], v[24:31], v[56:63], v[64:67]
	s_setprio 0
	s_barrier
	s_add_i32 s85, s85, 2
	s_addk_i32 s67, 0x100
	s_cmp_ge_i32 s85, s53
	v_add_u32_e32 v210, 0x100, v210
	s_cbranch_scc0 .LBB0_1348
	v_readlane_b32 s54, v255, 25
	v_readlane_b32 s55, v255, 26
	s_and_b64 vcc, exec, s[18:19]
	s_cbranch_vccnz .LBB0_1367
	s_branch .LBB0_1368

; #define PG8_STAGE(bufoff, rs_, soff_, voff) do { _Pragma("unroll") for (int _i = 0; _i < 2; ++_i) \
;         __builtin_amdgcn_raw_ptr_buffer_load_lds(rs_, (LAS void*)(lds + (bufoff) + ldsw + _i * 8192), 16, (int)(voff)[_i], (int)(soff_), 0, 0); } while (0)
; #define PG8_LDA(dst, b, h) do { _Pragma("unroll") for (int m = 0; m < 4; ++m) dst[m] = PG8_LD2(lds + PG8_SA(b, h) + aoff + m * 2048); } while (0)
; #define PG8_LDB(dst, b, h) do { _Pragma("unroll") for (int n = 0; n < 2; ++n) dst[n] = PG8_LD2(lds + PG8_SB(b, h) + boff + n * 2048); } while (0)
; #define PG8_WAIT_V(n) asm volatile("s_waitcnt vmcnt(" #n ")" ::: "memory")
; #define PG8_WAIT_L(n) asm volatile("s_waitcnt lgkmcnt(" #n ")" ::: "memory")
; #define PG8_BAR __builtin_amdgcn_s_barrier()
; #define PG8_SCHED __builtin_amdgcn_sched_barrier(0)
; template <class Epi, class Sched, bool ALIGN_EPI = false, bool SP2 = false, bool FP8 = false>
; __device__ __forceinline__ void gemm_phase(LAS unsigned char* lds, const Gemm g, const Sched& S, const Epi& E, int wbase) {
;     ...
;             PG8_LDB(B0, 0, 0); PG8_LDB(B1, 0, 1); PG8_SCHED; PG8_LDA(At, 0, 0); PG8_STAGE(PG8_SA(1, 1), rAc, a1 + hstep, voffA);
;             PG8_WAIT_V(8); PG8_WAIT_L(0); PG8_BAR; PG8_MMA(0, 0, At, B0); PG8_MMA(0, 1, At, B1); PG8_BAR; PG8_SCHED;
;             PG8_LDA(At, 0, 1); PG8_STAGE(PG8_SB(0, 0), rB2, b2, voffB); PG8_STAGE(PG8_SB(0, 1), rB2, b2 + hstep, voffB); PG8_STAGE(PG8_SA(0, 0), rA2, a2, voffA);
.LBB0_1453:
	v_add_u32_e32 v12, 0x10000, v199
	v_add_u32_e32 v28, 0x14000, v199
	ds_read_b128 v[0:3], v12
	ds_read_b128 v[4:7], v12 offset:1024
	ds_read_b128 v[8:11], v12 offset:2048
	ds_read_b128 v[12:15], v12 offset:3072
	ds_read_b128 v[16:19], v28
	ds_read_b128 v[20:23], v28 offset:1024
	ds_read_b128 v[24:27], v28 offset:2048
	ds_read_b128 v[28:31], v28 offset:3072
	s_add_i32 s6, s67, 0x80
	s_cmp_eq_u32 s61, s81
	s_cselect_b32 s54, s66, s6
	s_cselect_b64 vcc, -1, 0
	v_cndmask_b32_e32 v203, v202, v201, vcc
	s_or_b32 s78, s54, 0x80
	s_add_i32 s6, s34, s67
	s_mov_b32 m0, s62
	ds_read_b128 v[32:35], v200
	ds_read_b128 v[36:39], v200 offset:1024
	ds_read_b128 v[40:43], v200 offset:2048
	ds_read_b128 v[44:47], v200 offset:3072
	ds_read_b128 v[48:51], v200 offset:4096
	ds_read_b128 v[52:55], v200 offset:5120
	ds_read_b128 v[56:59], v200 offset:6144
	ds_read_b128 v[60:63], v200 offset:7168
	buffer_load_dwordx4 v192, s[36:39], s6 offen lds
	s_mov_b32 m0, s63
	s_nop 0
	buffer_load_dwordx4 v195, s[36:39], s6 offen lds
	s_waitcnt vmcnt(8)
	s_waitcnt lgkmcnt(0)
	s_barrier
	s_setprio 1
	v_mfma_f32_16x16x128_f8f6f4 v[188:191], v[0:7], v[32:39], v[188:191]
	v_mfma_f32_16x16x128_f8f6f4 v[184:187], v[8:15], v[32:39], v[184:187]
	v_mfma_f32_16x16x128_f8f6f4 v[172:175], v[0:7], v[40:47], v[172:175]
	v_mfma_f32_16x16x128_f8f6f4 v[168:171], v[8:15], v[40:47], v[168:171]
	v_mfma_f32_16x16x128_f8f6f4 v[156:159], v[0:7], v[48:55], v[156:159]
	v_mfma_f32_16x16x128_f8f6f4 v[152:155], v[8:15], v[48:55], v[152:155]
	v_mfma_f32_16x16x128_f8f6f4 v[140:143], v[0:7], v[56:63], v[140:143]
	v_mfma_f32_16x16x128_f8f6f4 v[136:139], v[8:15], v[56:63], v[136:139]
	v_mfma_f32_16x16x128_f8f6f4 v[180:183], v[16:23], v[32:39], v[180:183]
	v_mfma_f32_16x16x128_f8f6f4 v[176:179], v[24:31], v[32:39], v[176:179]
	v_mfma_f32_16x16x128_f8f6f4 v[164:167], v[16:23], v[40:47], v[164:167]
	v_mfma_f32_16x16x128_f8f6f4 v[160:163], v[24:31], v[40:47], v[160:163]
	v_mfma_f32_16x16x128_f8f6f4 v[148:151], v[16:23], v[48:55], v[148:151]
	v_mfma_f32_16x16x128_f8f6f4 v[144:147], v[24:31], v[48:55], v[144:147]
	v_mfma_f32_16x16x128_f8f6f4 v[132:135], v[16:23], v[56:63], v[132:135]
	v_mfma_f32_16x16x128_f8f6f4 v[128:131], v[24:31], v[56:63], v[128:131]
	s_setprio 0
	s_barrier
	ds_read_b128 v[32:35], v200 offset:16384
	ds_read_b128 v[36:39], v200 offset:17408
	ds_read_b128 v[40:43], v200 offset:18432
	ds_read_b128 v[44:47], v200 offset:19456
	ds_read_b128 v[48:51], v200 offset:20480
	ds_read_b128 v[52:55], v200 offset:21504
	ds_read_b128 v[56:59], v200 offset:22528
	ds_read_b128 v[60:63], v200 offset:23552
	s_mov_b32 s6, s38
	s_mov_b32 s7, s39
	s_mov_b64 s[18:19], exec
	s_mov_b32 m0, s41

; #define PG8_STAGE(bufoff, rs_, soff_, voff) do { _Pragma("unroll") for (int _i = 0; _i < 2; ++_i) \
;         __builtin_amdgcn_raw_ptr_buffer_load_lds(rs_, (LAS void*)(lds + (bufoff) + ldsw + _i * 8192), 16, (int)(voff)[_i], (int)(soff_), 0, 0); } while (0)
; #define PG8_LDA(dst, b, h) do { _Pragma("unroll") for (int m = 0; m < 4; ++m) dst[m] = PG8_LD2(lds + PG8_SA(b, h) + aoff + m * 2048); } while (0)
; #define PG8_LDB(dst, b, h) do { _Pragma("unroll") for (int n = 0; n < 2; ++n) dst[n] = PG8_LD2(lds + PG8_SB(b, h) + boff + n * 2048); } while (0)
; #define PG8_WAIT_V(n) asm volatile("s_waitcnt vmcnt(" #n ")" ::: "memory")
; #define PG8_WAIT_L(n) asm volatile("s_waitcnt lgkmcnt(" #n ")" ::: "memory")
; #define PG8_BAR __builtin_amdgcn_s_barrier()
; #define PG8_SCHED __builtin_amdgcn_sched_barrier(0)
; template <class Epi, class Sched, bool ALIGN_EPI = false, bool SP2 = false, bool FP8 = false>
; __device__ __forceinline__ void gemm_phase(LAS unsigned char* lds, const Gemm g, const Sched& S, const Epi& E, int wbase) {
;     ...
;             PG8_LDA(At, 0, 1); PG8_STAGE(PG8_SB(0, 0), rB2, b2, voffB); PG8_STAGE(PG8_SB(0, 1), rB2, b2 + hstep, voffB); PG8_STAGE(PG8_SA(0, 0), rA2, a2, voffA);
;             PG8_WAIT_V(8); PG8_WAIT_L(0); PG8_BAR; PG8_MMA(1, 0, At, B0); PG8_MMA(1, 1, At, B1); PG8_BAR; PG8_SCHED;
;             PG8_LDB(B0, 1, 0); PG8_LDB(B1, 1, 1); PG8_SCHED; PG8_LDA(At, 1, 0); PG8_STAGE(PG8_SA(0, 1), rA2, a2 + hstep, voffA);
;             PG8_WAIT_V(8); PG8_WAIT_L(0); PG8_BAR; PG8_MMA(0, 0, At, B0); PG8_MMA(0, 1, At, B1); PG8_BAR; PG8_SCHED;
;             PG8_LDA(At, 1, 1); PG8_STAGE(PG8_SB(1, 0), rB2, b3, voffB); PG8_STAGE(PG8_SB(1, 1), rB2, b3 + hstep, voffB); PG8_STAGE(PG8_SA(1, 0), rA2, a3, voffA);
.LBB0_1460:
	v_readfirstlane_b32 s55, v204
	s_nop 1
	v_cmp_eq_u32_e32 vcc, s55, v204
	s_and_saveexec_b64 vcc, vcc
	s_nop 0
	buffer_load_dwordx4 v196, s[4:7], s55 offen lds
	s_xor_b64 exec, exec, vcc
	s_cbranch_execnz .LBB0_1460
	s_mov_b64 exec, s[18:19]
	s_mov_b32 m0, s35
	s_nop 0
	buffer_load_dwordx4 v192, s[36:39], s54 offen lds
	s_mov_b32 m0, s45
	s_nop 0
	buffer_load_dwordx4 v195, s[36:39], s54 offen lds
	s_waitcnt vmcnt(8)
	s_waitcnt lgkmcnt(0)
	s_barrier
	s_setprio 1
	v_mfma_f32_16x16x128_f8f6f4 v[124:127], v[0:7], v[32:39], v[124:127]
	v_mfma_f32_16x16x128_f8f6f4 v[120:123], v[8:15], v[32:39], v[120:123]
	v_mfma_f32_16x16x128_f8f6f4 v[108:111], v[0:7], v[40:47], v[108:111]
	v_mfma_f32_16x16x128_f8f6f4 v[104:107], v[8:15], v[40:47], v[104:107]
	v_mfma_f32_16x16x128_f8f6f4 v[92:95], v[0:7], v[48:55], v[92:95]
	v_mfma_f32_16x16x128_f8f6f4 v[88:91], v[8:15], v[48:55], v[88:91]
	v_mfma_f32_16x16x128_f8f6f4 v[76:79], v[0:7], v[56:63], v[76:79]
	v_mfma_f32_16x16x128_f8f6f4 v[72:75], v[8:15], v[56:63], v[72:75]
	v_mfma_f32_16x16x128_f8f6f4 v[116:119], v[16:23], v[32:39], v[116:119]
	v_mfma_f32_16x16x128_f8f6f4 v[112:115], v[24:31], v[32:39], v[112:115]
	v_mfma_f32_16x16x128_f8f6f4 v[100:103], v[16:23], v[40:47], v[100:103]
	v_mfma_f32_16x16x128_f8f6f4 v[96:99], v[24:31], v[40:47], v[96:99]
	v_mfma_f32_16x16x128_f8f6f4 v[84:87], v[16:23], v[48:55], v[84:87]
	v_mfma_f32_16x16x128_f8f6f4 v[80:83], v[24:31], v[48:55], v[80:83]
	v_mfma_f32_16x16x128_f8f6f4 v[68:71], v[16:23], v[56:63], v[68:71]
	v_mfma_f32_16x16x128_f8f6f4 v[64:67], v[24:31], v[56:63], v[64:67]
	s_setprio 0
	s_barrier
	v_add_u32_e32 v12, 0x18000, v199
	v_add_u32_e32 v28, 0x1c000, v199
	ds_read_b128 v[0:3], v12
	ds_read_b128 v[4:7], v12 offset:1024
	ds_read_b128 v[8:11], v12 offset:2048
	ds_read_b128 v[12:15], v12 offset:3072
	ds_read_b128 v[16:19], v28
	ds_read_b128 v[20:23], v28 offset:1024
	ds_read_b128 v[24:27], v28 offset:2048
	ds_read_b128 v[28:31], v28 offset:3072
	s_add_i32 s54, s54, s34
	s_mov_b32 m0, s46
	ds_read_b128 v[32:35], v200 offset:32768
	ds_read_b128 v[36:39], v200 offset:33792
	ds_read_b128 v[40:43], v200 offset:34816
	ds_read_b128 v[44:47], v200 offset:35840
	ds_read_b128 v[48:51], v200 offset:36864
	ds_read_b128 v[52:55], v200 offset:37888
	ds_read_b128 v[56:59], v200 offset:38912
	ds_read_b128 v[60:63], v200 offset:39936
	buffer_load_dwordx4 v192, s[36:39], s54 offen lds
	s_mov_b32 m0, s47
	s_nop 0
	buffer_load_dwordx4 v195, s[36:39], s54 offen lds
	s_waitcnt vmcnt(8)
	s_waitcnt lgkmcnt(0)
	s_barrier
	s_setprio 1
	v_mfma_f32_16x16x128_f8f6f4 v[188:191], v[0:7], v[32:39], v[188:191]
	v_mfma_f32_16x16x128_f8f6f4 v[184:187], v[8:15], v[32:39], v[184:187]
	v_mfma_f32_16x16x128_f8f6f4 v[172:175], v[0:7], v[40:47], v[172:175]
	v_mfma_f32_16x16x128_f8f6f4 v[168:171], v[8:15], v[40:47], v[168:171]
	v_mfma_f32_16x16x128_f8f6f4 v[156:159], v[0:7], v[48:55], v[156:159]
	v_mfma_f32_16x16x128_f8f6f4 v[152:155], v[8:15], v[48:55], v[152:155]
	v_mfma_f32_16x16x128_f8f6f4 v[140:143], v[0:7], v[56:63], v[140:143]
	v_mfma_f32_16x16x128_f8f6f4 v[136:139], v[8:15], v[56:63], v[136:139]
	v_mfma_f32_16x16x128_f8f6f4 v[180:183], v[16:23], v[32:39], v[180:183]
	v_mfma_f32_16x16x128_f8f6f4 v[176:179], v[24:31], v[32:39], v[176:179]
	v_mfma_f32_16x16x128_f8f6f4 v[164:167], v[16:23], v[40:47], v[164:167]
	v_mfma_f32_16x16x128_f8f6f4 v[160:163], v[24:31], v[40:47], v[160:163]
	v_mfma_f32_16x16x128_f8f6f4 v[148:151], v[16:23], v[48:55], v[148:151]
	v_mfma_f32_16x16x128_f8f6f4 v[144:147], v[24:31], v[48:55], v[144:147]
	v_mfma_f32_16x16x128_f8f6f4 v[132:135], v[16:23], v[56:63], v[132:135]
	v_mfma_f32_16x16x128_f8f6f4 v[128:131], v[24:31], v[56:63], v[128:131]
	s_setprio 0
	s_barrier
	ds_read_b128 v[32:35], v200 offset:49152
	ds_read_b128 v[36:39], v200 offset:50176
	ds_read_b128 v[40:43], v200 offset:51200
	ds_read_b128 v[44:47], v200 offset:52224
	ds_read_b128 v[48:51], v200 offset:53248
	ds_read_b128 v[52:55], v200 offset:54272
	ds_read_b128 v[56:59], v200 offset:55296
	ds_read_b128 v[60:63], v200 offset:56320
	v_add_u32_e32 v203, 0x80, v203
	s_mov_b64 s[18:19], exec
	s_mov_b32 m0, s53

; #define PG8_STAGE(bufoff, rs_, soff_, voff) do { _Pragma("unroll") for (int _i = 0; _i < 2; ++_i) \
;         __builtin_amdgcn_raw_ptr_buffer_load_lds(rs_, (LAS void*)(lds + (bufoff) + ldsw + _i * 8192), 16, (int)(voff)[_i], (int)(soff_), 0, 0); } while (0)
; #define PG8_LDA(dst, b, h) do { _Pragma("unroll") for (int m = 0; m < 4; ++m) dst[m] = PG8_LD2(lds + PG8_SA(b, h) + aoff + m * 2048); } while (0)
; #define PG8_WAIT_V(n) asm volatile("s_waitcnt vmcnt(" #n ")" ::: "memory")
; #define PG8_WAIT_L(n) asm volatile("s_waitcnt lgkmcnt(" #n ")" ::: "memory")
; #define PG8_BAR __builtin_amdgcn_s_barrier()
; #define PG8_SCHED __builtin_amdgcn_sched_barrier(0)
; template <class Epi, class Sched, bool ALIGN_EPI = false, bool SP2 = false, bool FP8 = false>
; __device__ __forceinline__ void gemm_phase(LAS unsigned char* lds, const Gemm g, const Sched& S, const Epi& E, int wbase) {
;     ...
;             PG8_LDA(At, 1, 1); PG8_STAGE(PG8_SB(1, 0), rB2, b3, voffB); PG8_STAGE(PG8_SB(1, 1), rB2, b3 + hstep, voffB); PG8_STAGE(PG8_SA(1, 0), rA2, a3, voffA);
;             PG8_WAIT_V(8); PG8_WAIT_L(0); PG8_BAR; PG8_MMA(1, 0, At, B0); PG8_MMA(1, 1, At, B1); PG8_BAR; PG8_SCHED;
.LBB0_1468:
	v_readfirstlane_b32 s54, v203
	s_nop 1
	v_cmp_eq_u32_e32 vcc, s54, v203
	s_and_saveexec_b64 vcc, vcc
	s_nop 0
	buffer_load_dwordx4 v196, s[4:7], s54 offen lds
	s_xor_b64 exec, exec, vcc
	s_cbranch_execnz .LBB0_1468
	s_mov_b64 exec, s[18:19]
	s_mov_b32 m0, s57
	s_nop 0
	buffer_load_dwordx4 v192, s[36:39], s78 offen lds
	s_mov_b32 m0, s58
	s_nop 0
	buffer_load_dwordx4 v195, s[36:39], s78 offen lds
	s_waitcnt vmcnt(8)
	s_waitcnt lgkmcnt(0)
	s_barrier
	s_setprio 1
	v_mfma_f32_16x16x128_f8f6f4 v[124:127], v[0:7], v[32:39], v[124:127]
	v_mfma_f32_16x16x128_f8f6f4 v[120:123], v[8:15], v[32:39], v[120:123]
	v_mfma_f32_16x16x128_f8f6f4 v[108:111], v[0:7], v[40:47], v[108:111]
	v_mfma_f32_16x16x128_f8f6f4 v[104:107], v[8:15], v[40:47], v[104:107]
	v_mfma_f32_16x16x128_f8f6f4 v[92:95], v[0:7], v[48:55], v[92:95]
	v_mfma_f32_16x16x128_f8f6f4 v[88:91], v[8:15], v[48:55], v[88:91]
	v_mfma_f32_16x16x128_f8f6f4 v[76:79], v[0:7], v[56:63], v[76:79]
	v_mfma_f32_16x16x128_f8f6f4 v[72:75], v[8:15], v[56:63], v[72:75]
	v_mfma_f32_16x16x128_f8f6f4 v[116:119], v[16:23], v[32:39], v[116:119]
	v_mfma_f32_16x16x128_f8f6f4 v[112:115], v[24:31], v[32:39], v[112:115]
	v_mfma_f32_16x16x128_f8f6f4 v[100:103], v[16:23], v[40:47], v[100:103]
	v_mfma_f32_16x16x128_f8f6f4 v[96:99], v[24:31], v[40:47], v[96:99]
	v_mfma_f32_16x16x128_f8f6f4 v[84:87], v[16:23], v[48:55], v[84:87]
	v_mfma_f32_16x16x128_f8f6f4 v[80:83], v[24:31], v[48:55], v[80:83]
	v_mfma_f32_16x16x128_f8f6f4 v[68:71], v[16:23], v[56:63], v[68:71]
	v_mfma_f32_16x16x128_f8f6f4 v[64:67], v[24:31], v[56:63], v[64:67]
	s_setprio 0
	s_barrier
	s_add_i32 s81, s81, 2
	s_addk_i32 s67, 0x100
	s_cmp_ge_i32 s81, s48
	v_add_u32_e32 v202, 0x100, v202
	s_cbranch_scc0 .LBB0_1453
	v_readlane_b32 s54, v255, 25
	v_readlane_b32 s55, v255, 26
	s_and_b64 vcc, exec, s[14:15]
	s_cbranch_vccnz .LBB0_1472
	s_branch .LBB0_1473

; #define PG8_STAGE(bufoff, rs_, soff_, voff) do { _Pragma("unroll") for (int _i = 0; _i < 2; ++_i) \
;         __builtin_amdgcn_raw_ptr_buffer_load_lds(rs_, (LAS void*)(lds + (bufoff) + ldsw + _i * 8192), 16, (int)(voff)[_i], (int)(soff_), 0, 0); } while (0)
; #define PG8_LDA(dst, b, h) do { _Pragma("unroll") for (int m = 0; m < 4; ++m) dst[m] = PG8_LD2(lds + PG8_SA(b, h) + aoff + m * 2048); } while (0)
; #define PG8_LDB(dst, b, h) do { _Pragma("unroll") for (int n = 0; n < 2; ++n) dst[n] = PG8_LD2(lds + PG8_SB(b, h) + boff + n * 2048); } while (0)
; #define PG8_WAIT_V(n) asm volatile("s_waitcnt vmcnt(" #n ")" ::: "memory")
; #define PG8_WAIT_L(n) asm volatile("s_waitcnt lgkmcnt(" #n ")" ::: "memory")
; #define PG8_BAR __builtin_amdgcn_s_barrier()
; #define PG8_SCHED __builtin_amdgcn_sched_barrier(0)
; template <class Epi, class Sched, bool ALIGN_EPI = false, bool SP2 = false, bool FP8 = false>
; __device__ __forceinline__ void gemm_phase(LAS unsigned char* lds, const Gemm g, const Sched& S, const Epi& E, int wbase) {
;     ...
;             PG8_LDB(B0, 0, 0); PG8_LDB(B1, 0, 1); PG8_SCHED; PG8_LDA(At, 0, 0); PG8_STAGE(PG8_SA(1, 1), rAc, a1 + hstep, voffA);
;             PG8_WAIT_V(8); PG8_WAIT_L(0); PG8_BAR; PG8_MMA(0, 0, At, B0); PG8_MMA(0, 1, At, B1); PG8_BAR; PG8_SCHED;
;             PG8_LDA(At, 0, 1); PG8_STAGE(PG8_SB(0, 0), rB2, b2, voffB); PG8_STAGE(PG8_SB(0, 1), rB2, b2 + hstep, voffB); PG8_STAGE(PG8_SA(0, 0), rA2, a2, voffA);
;             PG8_WAIT_V(8); PG8_WAIT_L(0); PG8_BAR; PG8_MMA(1, 0, At, B0); PG8_MMA(1, 1, At, B1); PG8_BAR; PG8_SCHED;
.LBB0_1628:
	v_add_u32_e32 v136, 0x10000, v161
	ds_read_b128 v[128:131], v136
	ds_read_b128 v[132:135], v136 offset:1024
	ds_read_b128 v[164:167], v136 offset:2048
	ds_read_b128 v[168:171], v136 offset:3072
	v_add_u32_e32 v136, 0x14000, v161
	ds_read_b128 v[172:175], v136
	ds_read_b128 v[176:179], v136 offset:1024
	ds_read_b128 v[180:183], v136 offset:2048
	ds_read_b128 v[184:187], v136 offset:3072
	s_add_i32 s6, s61, 0x80
	s_cmp_eq_u32 s46, s63
	s_cselect_b32 s65, s59, s6
	s_cselect_b32 s55, s60, s62
	s_or_b32 s54, s65, 0x80
	s_add_i32 s6, s22, s61
	s_mov_b32 m0, s47
	ds_read_b128 v[188:191], v162
	ds_read_b128 v[192:195], v162 offset:1024
	ds_read_b128 v[196:199], v162 offset:2048
	ds_read_b128 v[200:203], v162 offset:3072
	ds_read_b128 v[204:207], v162 offset:4096
	ds_read_b128 v[208:211], v162 offset:5120
	ds_read_b128 v[212:215], v162 offset:6144
	ds_read_b128 v[216:219], v162 offset:7168
	buffer_load_dwordx4 v137, s[36:39], s6 offen lds
	s_mov_b32 m0, s48
	s_nop 0
	buffer_load_dwordx4 v145, s[36:39], s6 offen lds
	s_waitcnt vmcnt(8)
	s_waitcnt lgkmcnt(0)
	s_barrier
	s_setprio 1
	v_mfma_f32_16x16x32_bf16 v[120:123], v[128:131], v[188:191], v[120:123]
	v_mfma_f32_16x16x32_bf16 v[124:127], v[164:167], v[188:191], v[124:127]
	v_mfma_f32_16x16x32_bf16 v[104:107], v[128:131], v[196:199], v[104:107]
	v_mfma_f32_16x16x32_bf16 v[108:111], v[164:167], v[196:199], v[108:111]
	v_mfma_f32_16x16x32_bf16 v[88:91], v[128:131], v[204:207], v[88:91]
	v_mfma_f32_16x16x32_bf16 v[92:95], v[164:167], v[204:207], v[92:95]
	v_mfma_f32_16x16x32_bf16 v[72:75], v[128:131], v[212:215], v[72:75]
	v_mfma_f32_16x16x32_bf16 v[76:79], v[164:167], v[212:215], v[76:79]
	v_mfma_f32_16x16x32_bf16 v[120:123], v[132:135], v[192:195], v[120:123]
	v_mfma_f32_16x16x32_bf16 v[124:127], v[168:171], v[192:195], v[124:127]
	v_mfma_f32_16x16x32_bf16 v[104:107], v[132:135], v[200:203], v[104:107]
	v_mfma_f32_16x16x32_bf16 v[108:111], v[168:171], v[200:203], v[108:111]
	v_mfma_f32_16x16x32_bf16 v[88:91], v[132:135], v[208:211], v[88:91]
	v_mfma_f32_16x16x32_bf16 v[92:95], v[168:171], v[208:211], v[92:95]
	v_mfma_f32_16x16x32_bf16 v[72:75], v[132:135], v[216:219], v[72:75]
	v_mfma_f32_16x16x32_bf16 v[76:79], v[168:171], v[216:219], v[76:79]
	v_mfma_f32_16x16x32_bf16 v[112:115], v[172:175], v[188:191], v[112:115]
	v_mfma_f32_16x16x32_bf16 v[116:119], v[180:183], v[188:191], v[116:119]
	v_mfma_f32_16x16x32_bf16 v[96:99], v[172:175], v[196:199], v[96:99]
	v_mfma_f32_16x16x32_bf16 v[100:103], v[180:183], v[196:199], v[100:103]
	v_mfma_f32_16x16x32_bf16 v[80:83], v[172:175], v[204:207], v[80:83]
	v_mfma_f32_16x16x32_bf16 v[84:87], v[180:183], v[204:207], v[84:87]
	v_mfma_f32_16x16x32_bf16 v[64:67], v[172:175], v[212:215], v[64:67]
	v_mfma_f32_16x16x32_bf16 v[68:71], v[180:183], v[212:215], v[68:71]
	v_mfma_f32_16x16x32_bf16 v[112:115], v[176:179], v[192:195], v[112:115]
	v_mfma_f32_16x16x32_bf16 v[116:119], v[184:187], v[192:195], v[116:119]
	v_mfma_f32_16x16x32_bf16 v[96:99], v[176:179], v[200:203], v[96:99]
	v_mfma_f32_16x16x32_bf16 v[100:103], v[184:187], v[200:203], v[100:103]
	v_mfma_f32_16x16x32_bf16 v[80:83], v[176:179], v[208:211], v[80:83]
	v_mfma_f32_16x16x32_bf16 v[84:87], v[184:187], v[208:211], v[84:87]
	v_mfma_f32_16x16x32_bf16 v[64:67], v[176:179], v[216:219], v[64:67]
	v_mfma_f32_16x16x32_bf16 v[68:71], v[184:187], v[216:219], v[68:71]
	s_setprio 0
	s_barrier
	s_mov_b32 m0, s24
	s_mov_b32 s6, s38
	s_mov_b32 s7, s39
	ds_read_b128 v[188:191], v162 offset:16384
	ds_read_b128 v[192:195], v162 offset:17408
	ds_read_b128 v[196:199], v162 offset:18432
	ds_read_b128 v[200:203], v162 offset:19456
	ds_read_b128 v[204:207], v162 offset:20480
	ds_read_b128 v[208:211], v162 offset:21504
	ds_read_b128 v[212:215], v162 offset:22528
	ds_read_b128 v[216:219], v162 offset:23552
	buffer_load_dwordx4 v141, s[4:7], s55 offen lds
	s_mov_b32 m0, s25
	s_add_i32 s66, s55, s22
	buffer_load_dwordx4 v149, s[4:7], s55 offen lds
	s_mov_b32 m0, s26
	s_nop 0
	buffer_load_dwordx4 v141, s[4:7], s66 offen lds
	s_mov_b32 m0, s27
	s_nop 0
	buffer_load_dwordx4 v149, s[4:7], s66 offen lds
	s_mov_b32 m0, s23
	s_nop 0
	buffer_load_dwordx4 v137, s[36:39], s65 offen lds
	s_mov_b32 m0, s28
	s_nop 0
	buffer_load_dwordx4 v145, s[36:39], s65 offen lds
	s_waitcnt vmcnt(8)
	s_waitcnt lgkmcnt(0)
	s_barrier
	s_setprio 1
	v_mfma_f32_16x16x32_bf16 v[56:59], v[128:131], v[188:191], v[56:59]
	v_mfma_f32_16x16x32_bf16 v[60:63], v[164:167], v[188:191], v[60:63]
	v_mfma_f32_16x16x32_bf16 v[40:43], v[128:131], v[196:199], v[40:43]
	v_mfma_f32_16x16x32_bf16 v[44:47], v[164:167], v[196:199], v[44:47]
	v_mfma_f32_16x16x32_bf16 v[24:27], v[128:131], v[204:207], v[24:27]
	v_mfma_f32_16x16x32_bf16 v[28:31], v[164:167], v[204:207], v[28:31]
	v_mfma_f32_16x16x32_bf16 v[8:11], v[128:131], v[212:215], v[8:11]
	v_mfma_f32_16x16x32_bf16 v[12:15], v[164:167], v[212:215], v[12:15]
	v_mfma_f32_16x16x32_bf16 v[56:59], v[132:135], v[192:195], v[56:59]
	v_mfma_f32_16x16x32_bf16 v[60:63], v[168:171], v[192:195], v[60:63]
	v_mfma_f32_16x16x32_bf16 v[40:43], v[132:135], v[200:203], v[40:43]
	v_mfma_f32_16x16x32_bf16 v[44:47], v[168:171], v[200:203], v[44:47]
	v_mfma_f32_16x16x32_bf16 v[24:27], v[132:135], v[208:211], v[24:27]
	v_mfma_f32_16x16x32_bf16 v[28:31], v[168:171], v[208:211], v[28:31]
	v_mfma_f32_16x16x32_bf16 v[8:11], v[132:135], v[216:219], v[8:11]
	v_mfma_f32_16x16x32_bf16 v[12:15], v[168:171], v[216:219], v[12:15]
	v_mfma_f32_16x16x32_bf16 v[48:51], v[172:175], v[188:191], v[48:51]
	v_mfma_f32_16x16x32_bf16 v[52:55], v[180:183], v[188:191], v[52:55]
	v_mfma_f32_16x16x32_bf16 v[32:35], v[172:175], v[196:199], v[32:35]
	v_mfma_f32_16x16x32_bf16 v[36:39], v[180:183], v[196:199], v[36:39]
	v_mfma_f32_16x16x32_bf16 v[16:19], v[172:175], v[204:207], v[16:19]
	v_mfma_f32_16x16x32_bf16 v[20:23], v[180:183], v[204:207], v[20:23]
	v_mfma_f32_16x16x32_bf16 v[4:7], v[172:175], v[212:215], v[4:7]
	v_mfma_f32_16x16x32_bf16 v[0:3], v[180:183], v[212:215], v[0:3]
	v_mfma_f32_16x16x32_bf16 v[48:51], v[176:179], v[192:195], v[48:51]
	v_mfma_f32_16x16x32_bf16 v[52:55], v[184:187], v[192:195], v[52:55]
	v_mfma_f32_16x16x32_bf16 v[32:35], v[176:179], v[200:203], v[32:35]
	v_mfma_f32_16x16x32_bf16 v[36:39], v[184:187], v[200:203], v[36:39]
	v_mfma_f32_16x16x32_bf16 v[16:19], v[176:179], v[208:211], v[16:19]
	v_mfma_f32_16x16x32_bf16 v[20:23], v[184:187], v[208:211], v[20:23]
	v_mfma_f32_16x16x32_bf16 v[4:7], v[176:179], v[216:219], v[4:7]
	v_mfma_f32_16x16x32_bf16 v[0:3], v[184:187], v[216:219], v[0:3]
	s_setprio 0
	s_barrier
; #define PG8_STAGE(bufoff, rs_, soff_, voff) do { _Pragma("unroll") for (int _i = 0; _i < 2; ++_i) \
;         __builtin_amdgcn_raw_ptr_buffer_load_lds(rs_, (LAS void*)(lds + (bufoff) + ldsw + _i * 8192), 16, (int)(voff)[_i], (int)(soff_), 0, 0); } while (0)
; #define PG8_LDA(dst, b, h) do { _Pragma("unroll") for (int m = 0; m < 4; ++m) dst[m] = PG8_LD2(lds + PG8_SA(b, h) + aoff + m * 2048); } while (0)
; #define PG8_LDB(dst, b, h) do { _Pragma("unroll") for (int n = 0; n < 2; ++n) dst[n] = PG8_LD2(lds + PG8_SB(b, h) + boff + n * 2048); } while (0)
; #define PG8_WAIT_V(n) asm volatile("s_waitcnt vmcnt(" #n ")" ::: "memory")
; #define PG8_WAIT_L(n) asm volatile("s_waitcnt lgkmcnt(" #n ")" ::: "memory")
; #define PG8_BAR __builtin_amdgcn_s_barrier()
; #define PG8_SCHED __builtin_amdgcn_sched_barrier(0)
; template <class Epi, class Sched, bool ALIGN_EPI = false, bool SP2 = false, bool FP8 = false>
; __device__ __forceinline__ void gemm_phase(LAS unsigned char* lds, const Gemm g, const Sched& S, const Epi& E, int wbase) {
;     ...
;             PG8_LDB(B0, 1, 0); PG8_LDB(B1, 1, 1); PG8_SCHED; PG8_LDA(At, 1, 0); PG8_STAGE(PG8_SA(0, 1), rA2, a2 + hstep, voffA);
;             PG8_WAIT_V(8); PG8_WAIT_L(0); PG8_BAR; PG8_MMA(0, 0, At, B0); PG8_MMA(0, 1, At, B1); PG8_BAR; PG8_SCHED;
;             PG8_LDA(At, 1, 1); PG8_STAGE(PG8_SB(1, 0), rB2, b3, voffB); PG8_STAGE(PG8_SB(1, 1), rB2, b3 + hstep, voffB); PG8_STAGE(PG8_SA(1, 0), rA2, a3, voffA);
;             PG8_WAIT_V(8); PG8_WAIT_L(0); PG8_BAR; PG8_MMA(1, 0, At, B0); PG8_MMA(1, 1, At, B1); PG8_BAR; PG8_SCHED;
	v_add_u32_e32 v136, 0x18000, v161
	ds_read_b128 v[128:131], v136
	ds_read_b128 v[132:135], v136 offset:1024
	ds_read_b128 v[164:167], v136 offset:2048
	ds_read_b128 v[168:171], v136 offset:3072
	v_add_u32_e32 v136, 0x1c000, v161
	ds_read_b128 v[172:175], v136
	ds_read_b128 v[176:179], v136 offset:1024
	ds_read_b128 v[180:183], v136 offset:2048
	ds_read_b128 v[184:187], v136 offset:3072
	s_add_i32 s65, s65, s22
	s_mov_b32 m0, s29
	ds_read_b128 v[188:191], v162 offset:32768
	ds_read_b128 v[192:195], v162 offset:33792
	ds_read_b128 v[196:199], v162 offset:34816
	ds_read_b128 v[200:203], v162 offset:35840
	ds_read_b128 v[204:207], v162 offset:36864
	ds_read_b128 v[208:211], v162 offset:37888
	ds_read_b128 v[212:215], v162 offset:38912
	ds_read_b128 v[216:219], v162 offset:39936
	buffer_load_dwordx4 v137, s[36:39], s65 offen lds
	s_mov_b32 m0, s30
	s_nop 0
	buffer_load_dwordx4 v145, s[36:39], s65 offen lds
	s_waitcnt vmcnt(8)
	s_waitcnt lgkmcnt(0)
	s_barrier
	s_setprio 1
	v_mfma_f32_16x16x32_bf16 v[120:123], v[128:131], v[188:191], v[120:123]
	v_mfma_f32_16x16x32_bf16 v[124:127], v[164:167], v[188:191], v[124:127]
	v_mfma_f32_16x16x32_bf16 v[104:107], v[128:131], v[196:199], v[104:107]
	v_mfma_f32_16x16x32_bf16 v[108:111], v[164:167], v[196:199], v[108:111]
	v_mfma_f32_16x16x32_bf16 v[88:91], v[128:131], v[204:207], v[88:91]
	v_mfma_f32_16x16x32_bf16 v[92:95], v[164:167], v[204:207], v[92:95]
	v_mfma_f32_16x16x32_bf16 v[72:75], v[128:131], v[212:215], v[72:75]
	v_mfma_f32_16x16x32_bf16 v[76:79], v[164:167], v[212:215], v[76:79]
	v_mfma_f32_16x16x32_bf16 v[120:123], v[132:135], v[192:195], v[120:123]
	v_mfma_f32_16x16x32_bf16 v[124:127], v[168:171], v[192:195], v[124:127]
	v_mfma_f32_16x16x32_bf16 v[104:107], v[132:135], v[200:203], v[104:107]
	v_mfma_f32_16x16x32_bf16 v[108:111], v[168:171], v[200:203], v[108:111]
	v_mfma_f32_16x16x32_bf16 v[88:91], v[132:135], v[208:211], v[88:91]
	v_mfma_f32_16x16x32_bf16 v[92:95], v[168:171], v[208:211], v[92:95]
	v_mfma_f32_16x16x32_bf16 v[72:75], v[132:135], v[216:219], v[72:75]
	v_mfma_f32_16x16x32_bf16 v[76:79], v[168:171], v[216:219], v[76:79]
	v_mfma_f32_16x16x32_bf16 v[112:115], v[172:175], v[188:191], v[112:115]
	v_mfma_f32_16x16x32_bf16 v[116:119], v[180:183], v[188:191], v[116:119]
	v_mfma_f32_16x16x32_bf16 v[96:99], v[172:175], v[196:199], v[96:99]
	v_mfma_f32_16x16x32_bf16 v[100:103], v[180:183], v[196:199], v[100:103]
	v_mfma_f32_16x16x32_bf16 v[80:83], v[172:175], v[204:207], v[80:83]
	v_mfma_f32_16x16x32_bf16 v[84:87], v[180:183], v[204:207], v[84:87]
	v_mfma_f32_16x16x32_bf16 v[64:67], v[172:175], v[212:215], v[64:67]
	v_mfma_f32_16x16x32_bf16 v[68:71], v[180:183], v[212:215], v[68:71]
	v_mfma_f32_16x16x32_bf16 v[112:115], v[176:179], v[192:195], v[112:115]
	v_mfma_f32_16x16x32_bf16 v[116:119], v[184:187], v[192:195], v[116:119]
	v_mfma_f32_16x16x32_bf16 v[96:99], v[176:179], v[200:203], v[96:99]
	v_mfma_f32_16x16x32_bf16 v[100:103], v[184:187], v[200:203], v[100:103]
	v_mfma_f32_16x16x32_bf16 v[80:83], v[176:179], v[208:211], v[80:83]
	v_mfma_f32_16x16x32_bf16 v[84:87], v[184:187], v[208:211], v[84:87]
	v_mfma_f32_16x16x32_bf16 v[64:67], v[176:179], v[216:219], v[64:67]
	v_mfma_f32_16x16x32_bf16 v[68:71], v[184:187], v[216:219], v[68:71]
	s_setprio 0
	s_barrier
	s_mov_b32 m0, s31
	s_bitset1_b32 s55, 7
	ds_read_b128 v[188:191], v162 offset:49152
	ds_read_b128 v[192:195], v162 offset:50176
	ds_read_b128 v[196:199], v162 offset:51200
	ds_read_b128 v[200:203], v162 offset:52224
	ds_read_b128 v[204:207], v162 offset:53248
	ds_read_b128 v[208:211], v162 offset:54272
	ds_read_b128 v[212:215], v162 offset:55296
	ds_read_b128 v[216:219], v162 offset:56320
	buffer_load_dwordx4 v141, s[4:7], s55 offen lds
	s_mov_b32 m0, s33
	s_nop 0
	buffer_load_dwordx4 v149, s[4:7], s55 offen lds
	s_add_i32 s55, s55, s22
	s_mov_b32 m0, s41
	s_nop 0
	buffer_load_dwordx4 v141, s[4:7], s55 offen lds
	s_mov_b32 m0, s42
	s_nop 0
	buffer_load_dwordx4 v149, s[4:7], s55 offen lds
	s_mov_b32 m0, s34
	s_nop 0
	buffer_load_dwordx4 v137, s[36:39], s54 offen lds
	s_mov_b32 m0, s35
	s_nop 0
	buffer_load_dwordx4 v145, s[36:39], s54 offen lds
	s_waitcnt vmcnt(8)
	s_waitcnt lgkmcnt(0)
	s_barrier
	s_setprio 1
	v_mfma_f32_16x16x32_bf16 v[56:59], v[128:131], v[188:191], v[56:59]
	v_mfma_f32_16x16x32_bf16 v[60:63], v[164:167], v[188:191], v[60:63]
	v_mfma_f32_16x16x32_bf16 v[40:43], v[128:131], v[196:199], v[40:43]
	v_mfma_f32_16x16x32_bf16 v[44:47], v[164:167], v[196:199], v[44:47]
	v_mfma_f32_16x16x32_bf16 v[24:27], v[128:131], v[204:207], v[24:27]
	v_mfma_f32_16x16x32_bf16 v[28:31], v[164:167], v[204:207], v[28:31]
	v_mfma_f32_16x16x32_bf16 v[8:11], v[128:131], v[212:215], v[8:11]
	v_mfma_f32_16x16x32_bf16 v[12:15], v[164:167], v[212:215], v[12:15]
	v_mfma_f32_16x16x32_bf16 v[56:59], v[132:135], v[192:195], v[56:59]
	v_mfma_f32_16x16x32_bf16 v[60:63], v[168:171], v[192:195], v[60:63]
	v_mfma_f32_16x16x32_bf16 v[40:43], v[132:135], v[200:203], v[40:43]
	v_mfma_f32_16x16x32_bf16 v[44:47], v[168:171], v[200:203], v[44:47]
	v_mfma_f32_16x16x32_bf16 v[24:27], v[132:135], v[208:211], v[24:27]
	v_mfma_f32_16x16x32_bf16 v[28:31], v[168:171], v[208:211], v[28:31]
	v_mfma_f32_16x16x32_bf16 v[8:11], v[132:135], v[216:219], v[8:11]
	v_mfma_f32_16x16x32_bf16 v[12:15], v[168:171], v[216:219], v[12:15]
	v_mfma_f32_16x16x32_bf16 v[48:51], v[172:175], v[188:191], v[48:51]
	v_mfma_f32_16x16x32_bf16 v[52:55], v[180:183], v[188:191], v[52:55]
	v_mfma_f32_16x16x32_bf16 v[32:35], v[172:175], v[196:199], v[32:35]
	v_mfma_f32_16x16x32_bf16 v[36:39], v[180:183], v[196:199], v[36:39]
	v_mfma_f32_16x16x32_bf16 v[16:19], v[172:175], v[204:207], v[16:19]
	v_mfma_f32_16x16x32_bf16 v[20:23], v[180:183], v[204:207], v[20:23]
	v_mfma_f32_16x16x32_bf16 v[4:7], v[172:175], v[212:215], v[4:7]
	v_mfma_f32_16x16x32_bf16 v[0:3], v[180:183], v[212:215], v[0:3]
	v_mfma_f32_16x16x32_bf16 v[48:51], v[176:179], v[192:195], v[48:51]
	v_mfma_f32_16x16x32_bf16 v[52:55], v[184:187], v[192:195], v[52:55]
	v_mfma_f32_16x16x32_bf16 v[32:35], v[176:179], v[200:203], v[32:35]
	v_mfma_f32_16x16x32_bf16 v[36:39], v[184:187], v[200:203], v[36:39]
	v_mfma_f32_16x16x32_bf16 v[16:19], v[176:179], v[208:211], v[16:19]
	v_mfma_f32_16x16x32_bf16 v[20:23], v[184:187], v[208:211], v[20:23]
	v_mfma_f32_16x16x32_bf16 v[4:7], v[176:179], v[216:219], v[4:7]
	v_mfma_f32_16x16x32_bf16 v[0:3], v[184:187], v[216:219], v[0:3]
	s_setprio 0
	s_barrier
	s_add_i32 s63, s63, 2
	s_addk_i32 s61, 0x100
	s_addk_i32 s62, 0x100
	s_cmp_ge_i32 s63, s44
	s_cbranch_scc0 .LBB0_1628
	s_and_b64 vcc, exec, s[14:15]
	s_cbranch_vccz .LBB0_1631

; #define PG8_STAGE(bufoff, rs_, soff_, voff) do { _Pragma("unroll") for (int _i = 0; _i < 2; ++_i) \
;         __builtin_amdgcn_raw_ptr_buffer_load_lds(rs_, (LAS void*)(lds + (bufoff) + ldsw + _i * 8192), 16, (int)(voff)[_i], (int)(soff_), 0, 0); } while (0)
; #define PG8_LDA(dst, b, h) do { _Pragma("unroll") for (int m = 0; m < 4; ++m) dst[m] = PG8_LD2(lds + PG8_SA(b, h) + aoff + m * 2048); } while (0)
; #define PG8_LDB(dst, b, h) do { _Pragma("unroll") for (int n = 0; n < 2; ++n) dst[n] = PG8_LD2(lds + PG8_SB(b, h) + boff + n * 2048); } while (0)
; #define PG8_WAIT_V(n) asm volatile("s_waitcnt vmcnt(" #n ")" ::: "memory")
; #define PG8_WAIT_L(n) asm volatile("s_waitcnt lgkmcnt(" #n ")" ::: "memory")
; #define PG8_BAR __builtin_amdgcn_s_barrier()
; #define PG8_SCHED __builtin_amdgcn_sched_barrier(0)
; template <class Epi, class Sched, bool ALIGN_EPI = false, bool SP2 = false, bool FP8 = false>
; __device__ __forceinline__ void gemm_phase(LAS unsigned char* lds, const Gemm g, const Sched& S, const Epi& E, int wbase) {
;     ...
;             PG8_LDB(B0, 0, 0); PG8_LDB(B1, 0, 1); PG8_SCHED; PG8_LDA(At, 0, 0); PG8_STAGE(PG8_SA(1, 1), rAc, a1 + hstep, voffA);
;             PG8_WAIT_V(8); PG8_WAIT_L(0); PG8_BAR; PG8_MMA(0, 0, At, B0); PG8_MMA(0, 1, At, B1); PG8_BAR; PG8_SCHED;
;             PG8_LDA(At, 0, 1); PG8_STAGE(PG8_SB(0, 0), rB2, b2, voffB); PG8_STAGE(PG8_SB(0, 1), rB2, b2 + hstep, voffB); PG8_STAGE(PG8_SA(0, 0), rA2, a2, voffA);
;             PG8_WAIT_V(8); PG8_WAIT_L(0); PG8_BAR; PG8_MMA(1, 0, At, B0); PG8_MMA(1, 1, At, B1); PG8_BAR; PG8_SCHED;
.LBB0_1701:
	v_add_u32_e32 v140, 0x10000, v176
	v_add_u32_e32 v156, 0x14000, v176
	ds_read_b128 v[112:115], v140
	ds_read_b128 v[124:127], v140 offset:1024
	ds_read_b128 v[136:139], v140 offset:2048
	ds_read_b128 v[140:143], v140 offset:3072
	ds_read_b128 v[144:147], v156
	ds_read_b128 v[148:151], v156 offset:1024
	ds_read_b128 v[152:155], v156 offset:2048
	ds_read_b128 v[156:159], v156 offset:3072
	s_add_i32 s6, s65, 0x80
	s_cmp_eq_u32 s52, s67
	s_cselect_b32 s68, s21, s6
	s_cselect_b32 s55, s63, s66
	s_or_b32 s54, s68, 0x80
	s_add_i32 s6, s25, s65
	s_mov_b32 m0, s53
	ds_read_b128 v[160:163], v177
	ds_read_b128 v[164:167], v177 offset:1024
	ds_read_b128 v[178:181], v177 offset:2048
	ds_read_b128 v[182:185], v177 offset:3072
	ds_read_b128 v[186:189], v177 offset:4096
	ds_read_b128 v[190:193], v177 offset:5120
	ds_read_b128 v[194:197], v177 offset:6144
	ds_read_b128 v[198:201], v177 offset:7168
	buffer_load_dwordx4 v170, s[36:39], s6 offen lds
	s_mov_b32 m0, s56
	s_nop 0
	buffer_load_dwordx4 v172, s[36:39], s6 offen lds
	s_waitcnt vmcnt(8)
	s_waitcnt lgkmcnt(0)
	s_barrier
	s_setprio 1
	v_mfma_f32_16x16x32_bf16 v[132:135], v[112:115], v[160:163], v[132:135]
	v_mfma_f32_16x16x32_bf16 v[128:131], v[136:139], v[160:163], v[128:131]
	v_mfma_f32_16x16x32_bf16 v[108:111], v[112:115], v[178:181], v[108:111]
	v_mfma_f32_16x16x32_bf16 v[104:107], v[136:139], v[178:181], v[104:107]
	v_mfma_f32_16x16x32_bf16 v[92:95], v[112:115], v[186:189], v[92:95]
	v_mfma_f32_16x16x32_bf16 v[88:91], v[136:139], v[186:189], v[88:91]
	v_mfma_f32_16x16x32_bf16 v[76:79], v[112:115], v[194:197], v[76:79]
	v_mfma_f32_16x16x32_bf16 v[72:75], v[136:139], v[194:197], v[72:75]
	v_mfma_f32_16x16x32_bf16 v[132:135], v[124:127], v[164:167], v[132:135]
	v_mfma_f32_16x16x32_bf16 v[128:131], v[140:143], v[164:167], v[128:131]
	v_mfma_f32_16x16x32_bf16 v[108:111], v[124:127], v[182:185], v[108:111]
	v_mfma_f32_16x16x32_bf16 v[104:107], v[140:143], v[182:185], v[104:107]
	v_mfma_f32_16x16x32_bf16 v[92:95], v[124:127], v[190:193], v[92:95]
	v_mfma_f32_16x16x32_bf16 v[88:91], v[140:143], v[190:193], v[88:91]
	v_mfma_f32_16x16x32_bf16 v[76:79], v[124:127], v[198:201], v[76:79]
	v_mfma_f32_16x16x32_bf16 v[72:75], v[140:143], v[198:201], v[72:75]
	v_mfma_f32_16x16x32_bf16 v[120:123], v[144:147], v[160:163], v[120:123]
	v_mfma_f32_16x16x32_bf16 v[116:119], v[152:155], v[160:163], v[116:119]
	v_mfma_f32_16x16x32_bf16 v[100:103], v[144:147], v[178:181], v[100:103]
	v_mfma_f32_16x16x32_bf16 v[96:99], v[152:155], v[178:181], v[96:99]
	v_mfma_f32_16x16x32_bf16 v[84:87], v[144:147], v[186:189], v[84:87]
	v_mfma_f32_16x16x32_bf16 v[80:83], v[152:155], v[186:189], v[80:83]
	v_mfma_f32_16x16x32_bf16 v[68:71], v[144:147], v[194:197], v[68:71]
	v_mfma_f32_16x16x32_bf16 v[64:67], v[152:155], v[194:197], v[64:67]
	v_mfma_f32_16x16x32_bf16 v[120:123], v[148:151], v[164:167], v[120:123]
	v_mfma_f32_16x16x32_bf16 v[116:119], v[156:159], v[164:167], v[116:119]
	v_mfma_f32_16x16x32_bf16 v[100:103], v[148:151], v[182:185], v[100:103]
	v_mfma_f32_16x16x32_bf16 v[96:99], v[156:159], v[182:185], v[96:99]
	v_mfma_f32_16x16x32_bf16 v[84:87], v[148:151], v[190:193], v[84:87]
	v_mfma_f32_16x16x32_bf16 v[80:83], v[156:159], v[190:193], v[80:83]
	v_mfma_f32_16x16x32_bf16 v[68:71], v[148:151], v[198:201], v[68:71]
	v_mfma_f32_16x16x32_bf16 v[64:67], v[156:159], v[198:201], v[64:67]
	s_setprio 0
	s_barrier
	s_mov_b32 m0, s27
	s_mov_b32 s6, s38
	s_mov_b32 s7, s39
	ds_read_b128 v[160:163], v177 offset:16384
	ds_read_b128 v[164:167], v177 offset:17408
	ds_read_b128 v[178:181], v177 offset:18432
	ds_read_b128 v[182:185], v177 offset:19456
	ds_read_b128 v[186:189], v177 offset:20480
	ds_read_b128 v[190:193], v177 offset:21504
	ds_read_b128 v[194:197], v177 offset:22528
	ds_read_b128 v[198:201], v177 offset:23552
	buffer_load_dwordx4 v171, s[4:7], s55 offen lds
	s_mov_b32 m0, s28
	s_add_i32 s69, s55, s25
	buffer_load_dwordx4 v173, s[4:7], s55 offen lds
	s_mov_b32 m0, s29
	s_nop 0
	buffer_load_dwordx4 v171, s[4:7], s69 offen lds
	s_mov_b32 m0, s30
	s_nop 0
	buffer_load_dwordx4 v173, s[4:7], s69 offen lds
	s_mov_b32 m0, s26
	s_nop 0
	buffer_load_dwordx4 v170, s[36:39], s68 offen lds
	s_mov_b32 m0, s31
	s_nop 0
	buffer_load_dwordx4 v172, s[36:39], s68 offen lds
	s_waitcnt vmcnt(8)
	s_waitcnt lgkmcnt(0)
	s_barrier
	s_setprio 1
	v_mfma_f32_16x16x32_bf16 v[60:63], v[112:115], v[160:163], v[60:63]
	v_mfma_f32_16x16x32_bf16 v[56:59], v[136:139], v[160:163], v[56:59]
	v_mfma_f32_16x16x32_bf16 v[44:47], v[112:115], v[178:181], v[44:47]
	v_mfma_f32_16x16x32_bf16 v[40:43], v[136:139], v[178:181], v[40:43]
	v_mfma_f32_16x16x32_bf16 v[28:31], v[112:115], v[186:189], v[28:31]
	v_mfma_f32_16x16x32_bf16 v[24:27], v[136:139], v[186:189], v[24:27]
	v_mfma_f32_16x16x32_bf16 v[12:15], v[112:115], v[194:197], v[12:15]
	v_mfma_f32_16x16x32_bf16 v[8:11], v[136:139], v[194:197], v[8:11]
	v_mfma_f32_16x16x32_bf16 v[60:63], v[124:127], v[164:167], v[60:63]
	v_mfma_f32_16x16x32_bf16 v[56:59], v[140:143], v[164:167], v[56:59]
	v_mfma_f32_16x16x32_bf16 v[44:47], v[124:127], v[182:185], v[44:47]
	v_mfma_f32_16x16x32_bf16 v[40:43], v[140:143], v[182:185], v[40:43]
	v_mfma_f32_16x16x32_bf16 v[28:31], v[124:127], v[190:193], v[28:31]
	v_mfma_f32_16x16x32_bf16 v[24:27], v[140:143], v[190:193], v[24:27]
	v_mfma_f32_16x16x32_bf16 v[12:15], v[124:127], v[198:201], v[12:15]
	v_mfma_f32_16x16x32_bf16 v[8:11], v[140:143], v[198:201], v[8:11]
	v_mfma_f32_16x16x32_bf16 v[52:55], v[144:147], v[160:163], v[52:55]
	v_mfma_f32_16x16x32_bf16 v[48:51], v[152:155], v[160:163], v[48:51]
	v_mfma_f32_16x16x32_bf16 v[36:39], v[144:147], v[178:181], v[36:39]
	v_mfma_f32_16x16x32_bf16 v[32:35], v[152:155], v[178:181], v[32:35]
	v_mfma_f32_16x16x32_bf16 v[20:23], v[144:147], v[186:189], v[20:23]
	v_mfma_f32_16x16x32_bf16 v[16:19], v[152:155], v[186:189], v[16:19]
	v_mfma_f32_16x16x32_bf16 v[4:7], v[144:147], v[194:197], v[4:7]
	v_mfma_f32_16x16x32_bf16 v[0:3], v[152:155], v[194:197], v[0:3]
	v_mfma_f32_16x16x32_bf16 v[52:55], v[148:151], v[164:167], v[52:55]
	v_mfma_f32_16x16x32_bf16 v[48:51], v[156:159], v[164:167], v[48:51]
	v_mfma_f32_16x16x32_bf16 v[36:39], v[148:151], v[182:185], v[36:39]
	v_mfma_f32_16x16x32_bf16 v[32:35], v[156:159], v[182:185], v[32:35]
	v_mfma_f32_16x16x32_bf16 v[20:23], v[148:151], v[190:193], v[20:23]
	v_mfma_f32_16x16x32_bf16 v[16:19], v[156:159], v[190:193], v[16:19]
	v_mfma_f32_16x16x32_bf16 v[4:7], v[148:151], v[198:201], v[4:7]
	v_mfma_f32_16x16x32_bf16 v[0:3], v[156:159], v[198:201], v[0:3]
	s_setprio 0
	s_barrier
; #define PG8_STAGE(bufoff, rs_, soff_, voff) do { _Pragma("unroll") for (int _i = 0; _i < 2; ++_i) \
;         __builtin_amdgcn_raw_ptr_buffer_load_lds(rs_, (LAS void*)(lds + (bufoff) + ldsw + _i * 8192), 16, (int)(voff)[_i], (int)(soff_), 0, 0); } while (0)
; #define PG8_LDA(dst, b, h) do { _Pragma("unroll") for (int m = 0; m < 4; ++m) dst[m] = PG8_LD2(lds + PG8_SA(b, h) + aoff + m * 2048); } while (0)
; #define PG8_LDB(dst, b, h) do { _Pragma("unroll") for (int n = 0; n < 2; ++n) dst[n] = PG8_LD2(lds + PG8_SB(b, h) + boff + n * 2048); } while (0)
; #define PG8_WAIT_V(n) asm volatile("s_waitcnt vmcnt(" #n ")" ::: "memory")
; #define PG8_WAIT_L(n) asm volatile("s_waitcnt lgkmcnt(" #n ")" ::: "memory")
; #define PG8_BAR __builtin_amdgcn_s_barrier()
; #define PG8_SCHED __builtin_amdgcn_sched_barrier(0)
; template <class Epi, class Sched, bool ALIGN_EPI = false, bool SP2 = false, bool FP8 = false>
; __device__ __forceinline__ void gemm_phase(LAS unsigned char* lds, const Gemm g, const Sched& S, const Epi& E, int wbase) {
;     ...
;             PG8_LDB(B0, 1, 0); PG8_LDB(B1, 1, 1); PG8_SCHED; PG8_LDA(At, 1, 0); PG8_STAGE(PG8_SA(0, 1), rA2, a2 + hstep, voffA);
;             PG8_WAIT_V(8); PG8_WAIT_L(0); PG8_BAR; PG8_MMA(0, 0, At, B0); PG8_MMA(0, 1, At, B1); PG8_BAR; PG8_SCHED;
;             PG8_LDA(At, 1, 1); PG8_STAGE(PG8_SB(1, 0), rB2, b3, voffB); PG8_STAGE(PG8_SB(1, 1), rB2, b3 + hstep, voffB); PG8_STAGE(PG8_SA(1, 0), rA2, a3, voffA);
;             PG8_WAIT_V(8); PG8_WAIT_L(0); PG8_BAR; PG8_MMA(1, 0, At, B0); PG8_MMA(1, 1, At, B1); PG8_BAR; PG8_SCHED;
	v_add_u32_e32 v140, 0x18000, v176
	v_add_u32_e32 v156, 0x1c000, v176
	ds_read_b128 v[112:115], v140
	ds_read_b128 v[124:127], v140 offset:1024
	ds_read_b128 v[136:139], v140 offset:2048
	ds_read_b128 v[140:143], v140 offset:3072
	ds_read_b128 v[144:147], v156
	ds_read_b128 v[148:151], v156 offset:1024
	ds_read_b128 v[152:155], v156 offset:2048
	ds_read_b128 v[156:159], v156 offset:3072
	s_add_i32 s68, s68, s25
	s_mov_b32 m0, s33
	ds_read_b128 v[160:163], v177 offset:32768
	ds_read_b128 v[164:167], v177 offset:33792
	ds_read_b128 v[178:181], v177 offset:34816
	ds_read_b128 v[182:185], v177 offset:35840
	ds_read_b128 v[186:189], v177 offset:36864
	ds_read_b128 v[190:193], v177 offset:37888
	ds_read_b128 v[194:197], v177 offset:38912
	ds_read_b128 v[198:201], v177 offset:39936
	buffer_load_dwordx4 v170, s[36:39], s68 offen lds
	s_mov_b32 m0, s34
	s_nop 0
	buffer_load_dwordx4 v172, s[36:39], s68 offen lds
	s_waitcnt vmcnt(8)
	s_waitcnt lgkmcnt(0)
	s_barrier
	s_setprio 1
	v_mfma_f32_16x16x32_bf16 v[132:135], v[112:115], v[160:163], v[132:135]
	v_mfma_f32_16x16x32_bf16 v[128:131], v[136:139], v[160:163], v[128:131]
	v_mfma_f32_16x16x32_bf16 v[108:111], v[112:115], v[178:181], v[108:111]
	v_mfma_f32_16x16x32_bf16 v[104:107], v[136:139], v[178:181], v[104:107]
	v_mfma_f32_16x16x32_bf16 v[92:95], v[112:115], v[186:189], v[92:95]
	v_mfma_f32_16x16x32_bf16 v[88:91], v[136:139], v[186:189], v[88:91]
	v_mfma_f32_16x16x32_bf16 v[76:79], v[112:115], v[194:197], v[76:79]
	v_mfma_f32_16x16x32_bf16 v[72:75], v[136:139], v[194:197], v[72:75]
	v_mfma_f32_16x16x32_bf16 v[132:135], v[124:127], v[164:167], v[132:135]
	v_mfma_f32_16x16x32_bf16 v[128:131], v[140:143], v[164:167], v[128:131]
	v_mfma_f32_16x16x32_bf16 v[108:111], v[124:127], v[182:185], v[108:111]
	v_mfma_f32_16x16x32_bf16 v[104:107], v[140:143], v[182:185], v[104:107]
	v_mfma_f32_16x16x32_bf16 v[92:95], v[124:127], v[190:193], v[92:95]
	v_mfma_f32_16x16x32_bf16 v[88:91], v[140:143], v[190:193], v[88:91]
	v_mfma_f32_16x16x32_bf16 v[76:79], v[124:127], v[198:201], v[76:79]
	v_mfma_f32_16x16x32_bf16 v[72:75], v[140:143], v[198:201], v[72:75]
	v_mfma_f32_16x16x32_bf16 v[120:123], v[144:147], v[160:163], v[120:123]
	v_mfma_f32_16x16x32_bf16 v[116:119], v[152:155], v[160:163], v[116:119]
	v_mfma_f32_16x16x32_bf16 v[100:103], v[144:147], v[178:181], v[100:103]
	v_mfma_f32_16x16x32_bf16 v[96:99], v[152:155], v[178:181], v[96:99]
	v_mfma_f32_16x16x32_bf16 v[84:87], v[144:147], v[186:189], v[84:87]
	v_mfma_f32_16x16x32_bf16 v[80:83], v[152:155], v[186:189], v[80:83]
	v_mfma_f32_16x16x32_bf16 v[68:71], v[144:147], v[194:197], v[68:71]
	v_mfma_f32_16x16x32_bf16 v[64:67], v[152:155], v[194:197], v[64:67]
	v_mfma_f32_16x16x32_bf16 v[120:123], v[148:151], v[164:167], v[120:123]
	v_mfma_f32_16x16x32_bf16 v[116:119], v[156:159], v[164:167], v[116:119]
	v_mfma_f32_16x16x32_bf16 v[100:103], v[148:151], v[182:185], v[100:103]
	v_mfma_f32_16x16x32_bf16 v[96:99], v[156:159], v[182:185], v[96:99]
	v_mfma_f32_16x16x32_bf16 v[84:87], v[148:151], v[190:193], v[84:87]
	v_mfma_f32_16x16x32_bf16 v[80:83], v[156:159], v[190:193], v[80:83]
	v_mfma_f32_16x16x32_bf16 v[68:71], v[148:151], v[198:201], v[68:71]
	v_mfma_f32_16x16x32_bf16 v[64:67], v[156:159], v[198:201], v[64:67]
	s_setprio 0
	s_barrier
	s_mov_b32 m0, s1
	s_bitset1_b32 s55, 7
	ds_read_b128 v[160:163], v177 offset:49152
	ds_read_b128 v[164:167], v177 offset:50176
	ds_read_b128 v[178:181], v177 offset:51200
	ds_read_b128 v[182:185], v177 offset:52224
	ds_read_b128 v[186:189], v177 offset:53248
	ds_read_b128 v[190:193], v177 offset:54272
	ds_read_b128 v[194:197], v177 offset:55296
	ds_read_b128 v[198:201], v177 offset:56320
	buffer_load_dwordx4 v171, s[4:7], s55 offen lds
	s_mov_b32 m0, s35
	s_nop 0
	buffer_load_dwordx4 v173, s[4:7], s55 offen lds
	s_add_i32 s55, s55, s25
	s_mov_b32 m0, s43
	s_nop 0
	buffer_load_dwordx4 v171, s[4:7], s55 offen lds
	s_mov_b32 m0, s44
	s_nop 0
	buffer_load_dwordx4 v173, s[4:7], s55 offen lds
	s_mov_b32 m0, s41
	s_nop 0
	buffer_load_dwordx4 v170, s[36:39], s54 offen lds
	s_mov_b32 m0, s42
	s_nop 0
	buffer_load_dwordx4 v172, s[36:39], s54 offen lds
	s_waitcnt vmcnt(8)
	s_waitcnt lgkmcnt(0)
	s_barrier
	s_setprio 1
	v_mfma_f32_16x16x32_bf16 v[60:63], v[112:115], v[160:163], v[60:63]
	v_mfma_f32_16x16x32_bf16 v[56:59], v[136:139], v[160:163], v[56:59]
	v_mfma_f32_16x16x32_bf16 v[44:47], v[112:115], v[178:181], v[44:47]
	v_mfma_f32_16x16x32_bf16 v[40:43], v[136:139], v[178:181], v[40:43]
	v_mfma_f32_16x16x32_bf16 v[28:31], v[112:115], v[186:189], v[28:31]
	v_mfma_f32_16x16x32_bf16 v[24:27], v[136:139], v[186:189], v[24:27]
	v_mfma_f32_16x16x32_bf16 v[12:15], v[112:115], v[194:197], v[12:15]
	v_mfma_f32_16x16x32_bf16 v[8:11], v[136:139], v[194:197], v[8:11]
	v_mfma_f32_16x16x32_bf16 v[60:63], v[124:127], v[164:167], v[60:63]
	v_mfma_f32_16x16x32_bf16 v[56:59], v[140:143], v[164:167], v[56:59]
	v_mfma_f32_16x16x32_bf16 v[44:47], v[124:127], v[182:185], v[44:47]
	v_mfma_f32_16x16x32_bf16 v[40:43], v[140:143], v[182:185], v[40:43]
	v_mfma_f32_16x16x32_bf16 v[28:31], v[124:127], v[190:193], v[28:31]
	v_mfma_f32_16x16x32_bf16 v[24:27], v[140:143], v[190:193], v[24:27]
	v_mfma_f32_16x16x32_bf16 v[12:15], v[124:127], v[198:201], v[12:15]
	v_mfma_f32_16x16x32_bf16 v[8:11], v[140:143], v[198:201], v[8:11]
	v_mfma_f32_16x16x32_bf16 v[52:55], v[144:147], v[160:163], v[52:55]
	v_mfma_f32_16x16x32_bf16 v[48:51], v[152:155], v[160:163], v[48:51]
	v_mfma_f32_16x16x32_bf16 v[36:39], v[144:147], v[178:181], v[36:39]
	v_mfma_f32_16x16x32_bf16 v[32:35], v[152:155], v[178:181], v[32:35]
	v_mfma_f32_16x16x32_bf16 v[20:23], v[144:147], v[186:189], v[20:23]
	v_mfma_f32_16x16x32_bf16 v[16:19], v[152:155], v[186:189], v[16:19]
	v_mfma_f32_16x16x32_bf16 v[4:7], v[144:147], v[194:197], v[4:7]
	v_mfma_f32_16x16x32_bf16 v[0:3], v[152:155], v[194:197], v[0:3]
	v_mfma_f32_16x16x32_bf16 v[52:55], v[148:151], v[164:167], v[52:55]
	v_mfma_f32_16x16x32_bf16 v[48:51], v[156:159], v[164:167], v[48:51]
	v_mfma_f32_16x16x32_bf16 v[36:39], v[148:151], v[182:185], v[36:39]
	v_mfma_f32_16x16x32_bf16 v[32:35], v[156:159], v[182:185], v[32:35]
	v_mfma_f32_16x16x32_bf16 v[20:23], v[148:151], v[190:193], v[20:23]
	v_mfma_f32_16x16x32_bf16 v[16:19], v[156:159], v[190:193], v[16:19]
	v_mfma_f32_16x16x32_bf16 v[4:7], v[148:151], v[198:201], v[4:7]
	v_mfma_f32_16x16x32_bf16 v[0:3], v[156:159], v[198:201], v[0:3]
	s_setprio 0
	s_barrier
	s_add_i32 s67, s67, 2
	s_addk_i32 s65, 0x100
	s_addk_i32 s66, 0x100
	s_cmp_ge_i32 s67, s47
	s_cbranch_scc0 .LBB0_1701
	v_readlane_b32 s68, v255, 22
	v_readlane_b32 s69, v255, 23
	s_and_b64 vcc, exec, s[16:17]
	s_cbranch_vccnz .LBB0_1704
	s_branch .LBB0_1705

; #define PG8_STAGE(bufoff, rs_, soff_, voff) do { _Pragma("unroll") for (int _i = 0; _i < 2; ++_i) \
;         __builtin_amdgcn_raw_ptr_buffer_load_lds(rs_, (LAS void*)(lds + (bufoff) + ldsw + _i * 8192), 16, (int)(voff)[_i], (int)(soff_), 0, 0); } while (0)
; #define PG8_LDA(dst, b, h) do { _Pragma("unroll") for (int m = 0; m < 4; ++m) dst[m] = PG8_LD2(lds + PG8_SA(b, h) + aoff + m * 2048); } while (0)
; #define PG8_LDB(dst, b, h) do { _Pragma("unroll") for (int n = 0; n < 2; ++n) dst[n] = PG8_LD2(lds + PG8_SB(b, h) + boff + n * 2048); } while (0)
; #define PG8_WAIT_V(n) asm volatile("s_waitcnt vmcnt(" #n ")" ::: "memory")
; #define PG8_WAIT_L(n) asm volatile("s_waitcnt lgkmcnt(" #n ")" ::: "memory")
; #define PG8_BAR __builtin_amdgcn_s_barrier()
; #define PG8_SCHED __builtin_amdgcn_sched_barrier(0)
; template <class Epi, class Sched, bool ALIGN_EPI = false, bool SP2 = false, bool FP8 = false>
; __device__ __forceinline__ void gemm_phase(LAS unsigned char* lds, const Gemm g, const Sched& S, const Epi& E, int wbase) {
;     ...
;             PG8_LDB(B0, 0, 0); PG8_LDB(B1, 0, 1); PG8_SCHED; PG8_LDA(At, 0, 0); PG8_STAGE(PG8_SA(1, 1), rAc, a1 + hstep, voffA);
;             PG8_WAIT_V(8); PG8_WAIT_L(0); PG8_BAR; PG8_MMA(0, 0, At, B0); PG8_MMA(0, 1, At, B1); PG8_BAR; PG8_SCHED;
;             PG8_LDA(At, 0, 1); PG8_STAGE(PG8_SB(0, 0), rB2, b2, voffB); PG8_STAGE(PG8_SB(0, 1), rB2, b2 + hstep, voffB); PG8_STAGE(PG8_SA(0, 0), rA2, a2, voffA);
;             PG8_WAIT_V(8); PG8_WAIT_L(0); PG8_BAR; PG8_MMA(1, 0, At, B0); PG8_MMA(1, 1, At, B1); PG8_BAR; PG8_SCHED;
.LBB0_1781:
	v_add_u32_e32 v140, 0x10000, v154
	v_add_u32_e32 v144, 0x14000, v154
	ds_read_b128 v[128:131], v140
	ds_read_b128 v[132:135], v140 offset:1024
	ds_read_b128 v[136:139], v140 offset:2048
	ds_read_b128 v[140:143], v140 offset:3072
	ds_read_b128 v[156:159], v144
	ds_read_b128 v[160:163], v144 offset:1024
	ds_read_b128 v[164:167], v144 offset:2048
	ds_read_b128 v[168:171], v144 offset:3072
	s_add_i32 s6, s61, 0x80
	s_cmp_eq_u32 s45, s63
	s_cselect_b32 s65, s59, s6
	s_cselect_b32 s55, s60, s62
	s_or_b32 s54, s65, 0x80
	s_add_i32 s6, s21, s61
	s_mov_b32 m0, s46
	ds_read_b128 v[172:175], v155
	ds_read_b128 v[176:179], v155 offset:1024
	ds_read_b128 v[180:183], v155 offset:2048
	ds_read_b128 v[184:187], v155 offset:3072
	ds_read_b128 v[194:197], v155 offset:4096
	ds_read_b128 v[198:201], v155 offset:5120
	ds_read_b128 v[202:205], v155 offset:6144
	ds_read_b128 v[206:209], v155 offset:7168
	buffer_load_dwordx4 v148, s[36:39], s6 offen lds
	s_mov_b32 m0, s47
	s_nop 0
	buffer_load_dwordx4 v150, s[36:39], s6 offen lds
	s_waitcnt vmcnt(8)
	s_waitcnt lgkmcnt(0)
	s_barrier
	s_setprio 1
	v_mfma_f32_16x16x128_f8f6f4 v[120:123], v[128:135], v[172:179], v[120:123]
	v_mfma_f32_16x16x128_f8f6f4 v[124:127], v[136:143], v[172:179], v[124:127]
	v_mfma_f32_16x16x128_f8f6f4 v[104:107], v[128:135], v[180:187], v[104:107]
	v_mfma_f32_16x16x128_f8f6f4 v[108:111], v[136:143], v[180:187], v[108:111]
	v_mfma_f32_16x16x128_f8f6f4 v[144:147], v[128:135], v[194:201], v[88:91]
	v_mfma_f32_16x16x128_f8f6f4 v[188:191], v[136:143], v[194:201], v[92:95]
	v_mfma_f32_16x16x128_f8f6f4 v[210:213], v[128:135], v[202:209], v[72:75]
	v_mfma_f32_16x16x128_f8f6f4 v[214:217], v[136:143], v[202:209], v[76:79]
	v_mfma_f32_16x16x128_f8f6f4 v[112:115], v[156:163], v[172:179], v[112:115]
	v_mfma_f32_16x16x128_f8f6f4 v[116:119], v[164:171], v[172:179], v[116:119]
	v_mfma_f32_16x16x128_f8f6f4 v[96:99], v[156:163], v[180:187], v[96:99]
	v_mfma_f32_16x16x128_f8f6f4 v[100:103], v[164:171], v[180:187], v[100:103]
	v_mfma_f32_16x16x128_f8f6f4 v[172:175], v[156:163], v[194:201], v[80:83]
	v_mfma_f32_16x16x128_f8f6f4 v[176:179], v[164:171], v[194:201], v[84:87]
	v_mfma_f32_16x16x128_f8f6f4 v[180:183], v[156:163], v[202:209], v[64:67]
	v_mfma_f32_16x16x128_f8f6f4 v[184:187], v[164:171], v[202:209], v[68:71]
	s_setprio 0
	s_barrier
	s_mov_b32 m0, s23
	s_mov_b32 s6, s38
	s_mov_b32 s7, s39
	s_nop 0
	ds_read_b128 v[64:67], v155 offset:16384
	ds_read_b128 v[68:71], v155 offset:17408
	ds_read_b128 v[72:75], v155 offset:18432
	ds_read_b128 v[76:79], v155 offset:19456
	ds_read_b128 v[80:83], v155 offset:20480
	ds_read_b128 v[84:87], v155 offset:21504
	ds_read_b128 v[88:91], v155 offset:22528
	ds_read_b128 v[92:95], v155 offset:23552
	buffer_load_dwordx4 v149, s[4:7], s55 offen lds
	s_mov_b32 m0, s24
	s_add_i32 s66, s55, s21
	buffer_load_dwordx4 v151, s[4:7], s55 offen lds
	s_mov_b32 m0, s25
	s_nop 0
	buffer_load_dwordx4 v149, s[4:7], s66 offen lds
	s_mov_b32 m0, s26
	s_nop 0
	buffer_load_dwordx4 v151, s[4:7], s66 offen lds
	s_mov_b32 m0, s22
	s_nop 0
	buffer_load_dwordx4 v148, s[36:39], s65 offen lds
	s_mov_b32 m0, s27
	s_nop 0
	buffer_load_dwordx4 v150, s[36:39], s65 offen lds
	s_waitcnt vmcnt(8)
	s_waitcnt lgkmcnt(0)
	s_barrier
	s_setprio 1
	v_mfma_f32_16x16x128_f8f6f4 v[56:59], v[128:135], v[64:71], v[56:59]
	v_mfma_f32_16x16x128_f8f6f4 v[60:63], v[136:143], v[64:71], v[60:63]
	v_mfma_f32_16x16x128_f8f6f4 v[8:11], v[128:135], v[88:95], v[8:11]
	v_mfma_f32_16x16x128_f8f6f4 v[192:195], v[128:135], v[72:79], v[40:43]
	v_mfma_f32_16x16x128_f8f6f4 v[196:199], v[136:143], v[72:79], v[44:47]
	v_mfma_f32_16x16x128_f8f6f4 v[200:203], v[128:135], v[80:87], v[24:27]
	v_mfma_f32_16x16x128_f8f6f4 v[204:207], v[136:143], v[80:87], v[28:31]
	v_mfma_f32_16x16x128_f8f6f4 v[218:221], v[136:143], v[88:95], v[12:15]
	v_mfma_f32_16x16x128_f8f6f4 v[52:55], v[164:171], v[64:71], v[52:55]
	v_mfma_f32_16x16x128_f8f6f4 v[226:229], v[156:163], v[64:71], v[48:51]
	v_mfma_f32_16x16x128_f8f6f4 v[230:233], v[156:163], v[72:79], v[32:35]
	v_mfma_f32_16x16x128_f8f6f4 v[234:237], v[164:171], v[72:79], v[36:39]
	v_mfma_f32_16x16x128_f8f6f4 v[238:241], v[156:163], v[80:87], v[16:19]
	v_mfma_f32_16x16x128_f8f6f4 v[242:245], v[164:171], v[80:87], v[20:23]
	v_mfma_f32_16x16x128_f8f6f4 v[246:249], v[156:163], v[88:95], v[4:7]
	v_mfma_f32_16x16x128_f8f6f4 v[250:253], v[164:171], v[88:95], v[0:3]
	s_setprio 0
	s_barrier
; #define PG8_STAGE(bufoff, rs_, soff_, voff) do { _Pragma("unroll") for (int _i = 0; _i < 2; ++_i) \
;         __builtin_amdgcn_raw_ptr_buffer_load_lds(rs_, (LAS void*)(lds + (bufoff) + ldsw + _i * 8192), 16, (int)(voff)[_i], (int)(soff_), 0, 0); } while (0)
; #define PG8_LDA(dst, b, h) do { _Pragma("unroll") for (int m = 0; m < 4; ++m) dst[m] = PG8_LD2(lds + PG8_SA(b, h) + aoff + m * 2048); } while (0)
; #define PG8_LDB(dst, b, h) do { _Pragma("unroll") for (int n = 0; n < 2; ++n) dst[n] = PG8_LD2(lds + PG8_SB(b, h) + boff + n * 2048); } while (0)
; #define PG8_WAIT_V(n) asm volatile("s_waitcnt vmcnt(" #n ")" ::: "memory")
; #define PG8_WAIT_L(n) asm volatile("s_waitcnt lgkmcnt(" #n ")" ::: "memory")
; #define PG8_BAR __builtin_amdgcn_s_barrier()
; #define PG8_SCHED __builtin_amdgcn_sched_barrier(0)
; template <class Epi, class Sched, bool ALIGN_EPI = false, bool SP2 = false, bool FP8 = false>
; __device__ __forceinline__ void gemm_phase(LAS unsigned char* lds, const Gemm g, const Sched& S, const Epi& E, int wbase) {
;     ...
;             PG8_LDB(B0, 1, 0); PG8_LDB(B1, 1, 1); PG8_SCHED; PG8_LDA(At, 1, 0); PG8_STAGE(PG8_SA(0, 1), rA2, a2 + hstep, voffA);
;             PG8_WAIT_V(8); PG8_WAIT_L(0); PG8_BAR; PG8_MMA(0, 0, At, B0); PG8_MMA(0, 1, At, B1); PG8_BAR; PG8_SCHED;
;             PG8_LDA(At, 1, 1); PG8_STAGE(PG8_SB(1, 0), rB2, b3, voffB); PG8_STAGE(PG8_SB(1, 1), rB2, b3 + hstep, voffB); PG8_STAGE(PG8_SA(1, 0), rA2, a3, voffA);
;             PG8_WAIT_V(8); PG8_WAIT_L(0); PG8_BAR; PG8_MMA(1, 0, At, B0); PG8_MMA(1, 1, At, B1); PG8_BAR; PG8_SCHED;
	s_nop 1
	v_add_u32_e32 v16, 0x18000, v154
	v_add_u32_e32 v20, 0x1c000, v154
	s_nop 0
	ds_read_b128 v[0:3], v16
	ds_read_b128 v[4:7], v16 offset:1024
	ds_read_b128 v[12:15], v16 offset:2048
	ds_read_b128 v[16:19], v16 offset:3072
	ds_read_b128 v[128:131], v20
	ds_read_b128 v[132:135], v20 offset:1024
	ds_read_b128 v[136:139], v20 offset:2048
	ds_read_b128 v[140:143], v20 offset:3072
	s_add_i32 s65, s65, s21
	s_mov_b32 m0, s28
	ds_read_b128 v[20:23], v155 offset:32768
	ds_read_b128 v[24:27], v155 offset:33792
	ds_read_b128 v[28:31], v155 offset:34816
	ds_read_b128 v[32:35], v155 offset:35840
	ds_read_b128 v[36:39], v155 offset:36864
	ds_read_b128 v[40:43], v155 offset:37888
	ds_read_b128 v[44:47], v155 offset:38912
	ds_read_b128 v[48:51], v155 offset:39936
	buffer_load_dwordx4 v148, s[36:39], s65 offen lds
	s_mov_b32 m0, s29
	s_nop 0
	buffer_load_dwordx4 v150, s[36:39], s65 offen lds
	s_waitcnt vmcnt(8)
	s_waitcnt lgkmcnt(0)
	s_barrier
	s_setprio 1
	v_mfma_f32_16x16x128_f8f6f4 v[120:123], v[0:7], v[20:27], v[120:123]
	v_mfma_f32_16x16x128_f8f6f4 v[124:127], v[12:19], v[20:27], v[124:127]
	v_mfma_f32_16x16x128_f8f6f4 v[104:107], v[0:7], v[28:35], v[104:107]
	v_mfma_f32_16x16x128_f8f6f4 v[108:111], v[12:19], v[28:35], v[108:111]
	v_mfma_f32_16x16x128_f8f6f4 v[88:91], v[0:7], v[36:43], v[144:147]
	v_mfma_f32_16x16x128_f8f6f4 v[92:95], v[12:19], v[36:43], v[188:191]
	v_mfma_f32_16x16x128_f8f6f4 v[72:75], v[0:7], v[44:51], v[210:213]
	v_mfma_f32_16x16x128_f8f6f4 v[76:79], v[12:19], v[44:51], v[214:217]
	v_mfma_f32_16x16x128_f8f6f4 v[112:115], v[128:135], v[20:27], v[112:115]
	v_mfma_f32_16x16x128_f8f6f4 v[116:119], v[136:143], v[20:27], v[116:119]
	v_mfma_f32_16x16x128_f8f6f4 v[96:99], v[128:135], v[28:35], v[96:99]
	v_mfma_f32_16x16x128_f8f6f4 v[100:103], v[136:143], v[28:35], v[100:103]
	v_mfma_f32_16x16x128_f8f6f4 v[80:83], v[128:135], v[36:43], v[172:175]
	v_mfma_f32_16x16x128_f8f6f4 v[84:87], v[136:143], v[36:43], v[176:179]
	v_mfma_f32_16x16x128_f8f6f4 v[64:67], v[128:135], v[44:51], v[180:183]
	v_mfma_f32_16x16x128_f8f6f4 v[68:71], v[136:143], v[44:51], v[184:187]
	s_setprio 0
	s_barrier
	s_mov_b32 m0, s30
	s_bitset1_b32 s55, 7
	ds_read_b128 v[32:35], v155 offset:49152
	ds_read_b128 v[36:39], v155 offset:50176
	ds_read_b128 v[156:159], v155 offset:51200
	ds_read_b128 v[160:163], v155 offset:52224
	ds_read_b128 v[164:167], v155 offset:53248
	ds_read_b128 v[168:171], v155 offset:54272
	ds_read_b128 v[172:175], v155 offset:55296
	ds_read_b128 v[176:179], v155 offset:56320
	buffer_load_dwordx4 v149, s[4:7], s55 offen lds
	s_mov_b32 m0, s31
	s_nop 0
	buffer_load_dwordx4 v151, s[4:7], s55 offen lds
	s_add_i32 s55, s55, s21
	s_mov_b32 m0, s35
	s_nop 0
	buffer_load_dwordx4 v149, s[4:7], s55 offen lds
	s_mov_b32 m0, s41
	s_nop 0
	buffer_load_dwordx4 v151, s[4:7], s55 offen lds
	s_mov_b32 m0, s33
	s_nop 0
	buffer_load_dwordx4 v148, s[36:39], s54 offen lds
	s_mov_b32 m0, s34
	s_nop 0
	buffer_load_dwordx4 v150, s[36:39], s54 offen lds
	s_waitcnt vmcnt(8)
	s_waitcnt lgkmcnt(0)
	s_barrier
	s_setprio 1
	v_mfma_f32_16x16x128_f8f6f4 v[56:59], v[0:7], v[32:39], v[56:59]
	v_mfma_f32_16x16x128_f8f6f4 v[60:63], v[12:19], v[32:39], v[60:63]
	v_mfma_f32_16x16x128_f8f6f4 v[40:43], v[0:7], v[156:163], v[192:195]
	v_mfma_f32_16x16x128_f8f6f4 v[44:47], v[12:19], v[156:163], v[196:199]
	v_mfma_f32_16x16x128_f8f6f4 v[24:27], v[0:7], v[164:171], v[200:203]
	v_mfma_f32_16x16x128_f8f6f4 v[28:31], v[12:19], v[164:171], v[204:207]
	v_mfma_f32_16x16x128_f8f6f4 v[8:11], v[0:7], v[172:179], v[8:11]
	v_mfma_f32_16x16x128_f8f6f4 v[12:15], v[12:19], v[172:179], v[218:221]
	v_mfma_f32_16x16x128_f8f6f4 v[48:51], v[128:135], v[32:39], v[226:229]
	v_mfma_f32_16x16x128_f8f6f4 v[52:55], v[136:143], v[32:39], v[52:55]
	v_mfma_f32_16x16x128_f8f6f4 v[32:35], v[128:135], v[156:163], v[230:233]
	v_mfma_f32_16x16x128_f8f6f4 v[36:39], v[136:143], v[156:163], v[234:237]
	v_mfma_f32_16x16x128_f8f6f4 v[16:19], v[128:135], v[164:171], v[238:241]
	v_mfma_f32_16x16x128_f8f6f4 v[20:23], v[136:143], v[164:171], v[242:245]
	v_mfma_f32_16x16x128_f8f6f4 v[4:7], v[128:135], v[172:179], v[246:249]
	v_mfma_f32_16x16x128_f8f6f4 v[0:3], v[136:143], v[172:179], v[250:253]
	s_setprio 0
	s_barrier
	s_add_i32 s63, s63, 2
	s_addk_i32 s61, 0x100
	s_addk_i32 s62, 0x100
	s_cmp_ge_i32 s63, s43
	s_cbranch_scc0 .LBB0_1781
	v_mov_b32_e32 v230, v222
	v_mov_b32_e32 v233, v223
	v_mov_b32_e32 v231, v225
	v_mov_b32_e32 v234, 0xff61b1e6
	s_and_b64 vcc, exec, s[16:17]
	s_cbranch_vccnz .LBB0_1784
	s_branch .LBB0_1785

; #define PG8_STAGE(bufoff, rs_, soff_, voff) do { _Pragma("unroll") for (int _i = 0; _i < 2; ++_i) \
;         __builtin_amdgcn_raw_ptr_buffer_load_lds(rs_, (LAS void*)(lds + (bufoff) + ldsw + _i * 8192), 16, (int)(voff)[_i], (int)(soff_), 0, 0); } while (0)
; #define PG8_LDA(dst, b, h) do { _Pragma("unroll") for (int m = 0; m < 4; ++m) dst[m] = PG8_LD2(lds + PG8_SA(b, h) + aoff + m * 2048); } while (0)
; #define PG8_LDB(dst, b, h) do { _Pragma("unroll") for (int n = 0; n < 2; ++n) dst[n] = PG8_LD2(lds + PG8_SB(b, h) + boff + n * 2048); } while (0)
; #define PG8_WAIT_V(n) asm volatile("s_waitcnt vmcnt(" #n ")" ::: "memory")
; #define PG8_WAIT_L(n) asm volatile("s_waitcnt lgkmcnt(" #n ")" ::: "memory")
; #define PG8_BAR __builtin_amdgcn_s_barrier()
; #define PG8_SCHED __builtin_amdgcn_sched_barrier(0)
; template <class Epi, class Sched, bool ALIGN_EPI = false, bool SP2 = false, bool FP8 = false>
; __device__ __forceinline__ void gemm_phase(LAS unsigned char* lds, const Gemm g, const Sched& S, const Epi& E, int wbase) {
;     ...
;             PG8_LDB(B0, 0, 0); PG8_LDB(B1, 0, 1); PG8_SCHED; PG8_LDA(At, 0, 0); PG8_STAGE(PG8_SA(1, 1), rAc, a1 + hstep, voffA);
;             PG8_WAIT_V(8); PG8_WAIT_L(0); PG8_BAR; PG8_MMA(0, 0, At, B0); PG8_MMA(0, 1, At, B1); PG8_BAR; PG8_SCHED;
;             PG8_LDA(At, 0, 1); PG8_STAGE(PG8_SB(0, 0), rB2, b2, voffB); PG8_STAGE(PG8_SB(0, 1), rB2, b2 + hstep, voffB); PG8_STAGE(PG8_SA(0, 0), rA2, a2, voffA);
;             PG8_WAIT_V(8); PG8_WAIT_L(0); PG8_BAR; PG8_MMA(1, 0, At, B0); PG8_MMA(1, 1, At, B1); PG8_BAR; PG8_SCHED;
.LBB0_1854:
	v_add_u32_e32 v140, 0x10000, v176
	v_add_u32_e32 v156, 0x14000, v176
	ds_read_b128 v[128:131], v140
	ds_read_b128 v[132:135], v140 offset:1024
	ds_read_b128 v[136:139], v140 offset:2048
	ds_read_b128 v[140:143], v140 offset:3072
	ds_read_b128 v[144:147], v156
	ds_read_b128 v[148:151], v156 offset:1024
	ds_read_b128 v[152:155], v156 offset:2048
	ds_read_b128 v[156:159], v156 offset:3072
	s_add_i32 s6, s65, 0x80
	s_cmp_eq_u32 s52, s67
	s_cselect_b32 s68, s21, s6
	s_cselect_b32 s55, s63, s66
	s_or_b32 s54, s68, 0x80
	s_add_i32 s6, s24, s65
	s_mov_b32 m0, s53
	ds_read_b128 v[160:163], v177
	ds_read_b128 v[164:167], v177 offset:1024
	ds_read_b128 v[178:181], v177 offset:2048
	ds_read_b128 v[182:185], v177 offset:3072
	ds_read_b128 v[194:197], v177 offset:4096
	ds_read_b128 v[198:201], v177 offset:5120
	ds_read_b128 v[202:205], v177 offset:6144
	ds_read_b128 v[206:209], v177 offset:7168
	buffer_load_dwordx4 v170, s[36:39], s6 offen lds
	s_mov_b32 m0, s56
	s_nop 0
	buffer_load_dwordx4 v172, s[36:39], s6 offen lds
	s_waitcnt vmcnt(8)
	s_waitcnt lgkmcnt(0)
	s_barrier
	s_setprio 1
	v_mfma_f32_16x16x128_f8f6f4 v[124:127], v[128:135], v[160:167], v[124:127]
	v_mfma_f32_16x16x128_f8f6f4 v[120:123], v[136:143], v[160:167], v[120:123]
	v_mfma_f32_16x16x128_f8f6f4 v[108:111], v[128:135], v[178:185], v[108:111]
	v_mfma_f32_16x16x128_f8f6f4 v[104:107], v[136:143], v[178:185], v[104:107]
	v_mfma_f32_16x16x128_f8f6f4 v[186:189], v[128:135], v[194:201], v[92:95]
	v_mfma_f32_16x16x128_f8f6f4 v[190:193], v[136:143], v[194:201], v[88:91]
	v_mfma_f32_16x16x128_f8f6f4 v[210:213], v[128:135], v[202:209], v[76:79]
	v_mfma_f32_16x16x128_f8f6f4 v[214:217], v[136:143], v[202:209], v[72:75]
	v_mfma_f32_16x16x128_f8f6f4 v[116:119], v[144:151], v[160:167], v[116:119]
	v_mfma_f32_16x16x128_f8f6f4 v[112:115], v[152:159], v[160:167], v[112:115]
	v_mfma_f32_16x16x128_f8f6f4 v[100:103], v[144:151], v[178:185], v[100:103]
	v_mfma_f32_16x16x128_f8f6f4 v[96:99], v[152:159], v[178:185], v[96:99]
	v_mfma_f32_16x16x128_f8f6f4 v[160:163], v[144:151], v[194:201], v[84:87]
	v_mfma_f32_16x16x128_f8f6f4 v[164:167], v[152:159], v[194:201], v[80:83]
	v_mfma_f32_16x16x128_f8f6f4 v[178:181], v[144:151], v[202:209], v[68:71]
	v_mfma_f32_16x16x128_f8f6f4 v[182:185], v[152:159], v[202:209], v[64:67]
	s_setprio 0
	s_barrier
	s_mov_b32 m0, s26
	s_mov_b32 s6, s38
	s_mov_b32 s7, s39
	s_nop 1
	ds_read_b128 v[64:67], v177 offset:16384
	ds_read_b128 v[68:71], v177 offset:17408
	ds_read_b128 v[72:75], v177 offset:18432
	ds_read_b128 v[76:79], v177 offset:19456
	ds_read_b128 v[80:83], v177 offset:20480
	ds_read_b128 v[84:87], v177 offset:21504
	ds_read_b128 v[88:91], v177 offset:22528
	ds_read_b128 v[92:95], v177 offset:23552
	buffer_load_dwordx4 v171, s[4:7], s55 offen lds
	s_mov_b32 m0, s27
	s_add_i32 s69, s55, s24
	buffer_load_dwordx4 v173, s[4:7], s55 offen lds
	s_mov_b32 m0, s28
	s_nop 0
	buffer_load_dwordx4 v171, s[4:7], s69 offen lds
	s_mov_b32 m0, s29
	s_nop 0
	buffer_load_dwordx4 v173, s[4:7], s69 offen lds
	s_mov_b32 m0, s25
	s_nop 0
	buffer_load_dwordx4 v170, s[36:39], s68 offen lds
	s_mov_b32 m0, s30
	s_nop 0
	buffer_load_dwordx4 v172, s[36:39], s68 offen lds
	s_waitcnt vmcnt(8)
	s_waitcnt lgkmcnt(0)
	s_barrier
	s_setprio 1
	v_mfma_f32_16x16x128_f8f6f4 v[60:63], v[128:135], v[64:71], v[60:63]
	v_mfma_f32_16x16x128_f8f6f4 v[56:59], v[136:143], v[64:71], v[56:59]
	v_mfma_f32_16x16x128_f8f6f4 v[194:197], v[128:135], v[72:79], v[44:47]
	v_mfma_f32_16x16x128_f8f6f4 v[198:201], v[136:143], v[72:79], v[40:43]
	v_mfma_f32_16x16x128_f8f6f4 v[202:205], v[128:135], v[80:87], v[28:31]
	v_mfma_f32_16x16x128_f8f6f4 v[206:209], v[136:143], v[80:87], v[24:27]
	v_mfma_f32_16x16x128_f8f6f4 v[218:221], v[128:135], v[88:95], v[12:15]
	v_mfma_f32_16x16x128_f8f6f4 v[226:229], v[136:143], v[88:95], v[8:11]
	v_mfma_f32_16x16x128_f8f6f4 v[52:55], v[144:151], v[64:71], v[52:55]
	v_mfma_f32_16x16x128_f8f6f4 v[48:51], v[152:159], v[64:71], v[48:51]
	v_mfma_f32_16x16x128_f8f6f4 v[230:233], v[144:151], v[72:79], v[36:39]
	v_mfma_f32_16x16x128_f8f6f4 v[234:237], v[152:159], v[72:79], v[32:35]
	v_mfma_f32_16x16x128_f8f6f4 v[238:241], v[144:151], v[80:87], v[20:23]
	v_mfma_f32_16x16x128_f8f6f4 v[242:245], v[152:159], v[80:87], v[16:19]
	v_mfma_f32_16x16x128_f8f6f4 v[246:249], v[144:151], v[88:95], v[4:7]
	v_mfma_f32_16x16x128_f8f6f4 v[250:253], v[152:159], v[88:95], v[0:3]
	s_setprio 0
	s_barrier
; #define PG8_STAGE(bufoff, rs_, soff_, voff) do { _Pragma("unroll") for (int _i = 0; _i < 2; ++_i) \
;         __builtin_amdgcn_raw_ptr_buffer_load_lds(rs_, (LAS void*)(lds + (bufoff) + ldsw + _i * 8192), 16, (int)(voff)[_i], (int)(soff_), 0, 0); } while (0)
; #define PG8_LDA(dst, b, h) do { _Pragma("unroll") for (int m = 0; m < 4; ++m) dst[m] = PG8_LD2(lds + PG8_SA(b, h) + aoff + m * 2048); } while (0)
; #define PG8_LDB(dst, b, h) do { _Pragma("unroll") for (int n = 0; n < 2; ++n) dst[n] = PG8_LD2(lds + PG8_SB(b, h) + boff + n * 2048); } while (0)
; #define PG8_WAIT_V(n) asm volatile("s_waitcnt vmcnt(" #n ")" ::: "memory")
; #define PG8_WAIT_L(n) asm volatile("s_waitcnt lgkmcnt(" #n ")" ::: "memory")
; #define PG8_BAR __builtin_amdgcn_s_barrier()
; #define PG8_SCHED __builtin_amdgcn_sched_barrier(0)
; template <class Epi, class Sched, bool ALIGN_EPI = false, bool SP2 = false, bool FP8 = false>
; __device__ __forceinline__ void gemm_phase(LAS unsigned char* lds, const Gemm g, const Sched& S, const Epi& E, int wbase) {
;     ...
;             PG8_LDB(B0, 1, 0); PG8_LDB(B1, 1, 1); PG8_SCHED; PG8_LDA(At, 1, 0); PG8_STAGE(PG8_SA(0, 1), rA2, a2 + hstep, voffA);
;             PG8_WAIT_V(8); PG8_WAIT_L(0); PG8_BAR; PG8_MMA(0, 0, At, B0); PG8_MMA(0, 1, At, B1); PG8_BAR; PG8_SCHED;
;             PG8_LDA(At, 1, 1); PG8_STAGE(PG8_SB(1, 0), rB2, b3, voffB); PG8_STAGE(PG8_SB(1, 1), rB2, b3 + hstep, voffB); PG8_STAGE(PG8_SA(1, 0), rA2, a3, voffA);
;             PG8_WAIT_V(8); PG8_WAIT_L(0); PG8_BAR; PG8_MMA(1, 0, At, B0); PG8_MMA(1, 1, At, B1); PG8_BAR; PG8_SCHED;
	v_add_u32_e32 v8, 0x18000, v176
	s_nop 3
	ds_read_b128 v[0:3], v8
	ds_read_b128 v[4:7], v8 offset:1024
	ds_read_b128 v[16:19], v8 offset:2048
	ds_read_b128 v[20:23], v8 offset:3072
	v_add_u32_e32 v8, 0x1c000, v176
	ds_read_b128 v[128:131], v8
	ds_read_b128 v[132:135], v8 offset:1024
	ds_read_b128 v[136:139], v8 offset:2048
	ds_read_b128 v[140:143], v8 offset:3072
	s_add_i32 s68, s68, s24
	s_mov_b32 m0, s31
	ds_read_b128 v[8:11], v177 offset:32768
	ds_read_b128 v[12:15], v177 offset:33792
	ds_read_b128 v[24:27], v177 offset:34816
	ds_read_b128 v[28:31], v177 offset:35840
	ds_read_b128 v[32:35], v177 offset:36864
	ds_read_b128 v[36:39], v177 offset:37888
	ds_read_b128 v[40:43], v177 offset:38912
	ds_read_b128 v[44:47], v177 offset:39936
	buffer_load_dwordx4 v170, s[36:39], s68 offen lds
	s_mov_b32 m0, s33
	s_nop 0
	buffer_load_dwordx4 v172, s[36:39], s68 offen lds
	s_waitcnt vmcnt(8)
	s_waitcnt lgkmcnt(0)
	s_barrier
	s_setprio 1
	v_mfma_f32_16x16x128_f8f6f4 v[124:127], v[0:7], v[8:15], v[124:127]
	v_mfma_f32_16x16x128_f8f6f4 v[120:123], v[16:23], v[8:15], v[120:123]
	v_mfma_f32_16x16x128_f8f6f4 v[108:111], v[0:7], v[24:31], v[108:111]
	v_mfma_f32_16x16x128_f8f6f4 v[104:107], v[16:23], v[24:31], v[104:107]
	v_mfma_f32_16x16x128_f8f6f4 v[92:95], v[0:7], v[32:39], v[186:189]
	v_mfma_f32_16x16x128_f8f6f4 v[88:91], v[16:23], v[32:39], v[190:193]
	v_mfma_f32_16x16x128_f8f6f4 v[76:79], v[0:7], v[40:47], v[210:213]
	v_mfma_f32_16x16x128_f8f6f4 v[72:75], v[16:23], v[40:47], v[214:217]
	v_mfma_f32_16x16x128_f8f6f4 v[116:119], v[128:135], v[8:15], v[116:119]
	v_mfma_f32_16x16x128_f8f6f4 v[112:115], v[136:143], v[8:15], v[112:115]
	v_mfma_f32_16x16x128_f8f6f4 v[100:103], v[128:135], v[24:31], v[100:103]
	v_mfma_f32_16x16x128_f8f6f4 v[96:99], v[136:143], v[24:31], v[96:99]
	v_mfma_f32_16x16x128_f8f6f4 v[84:87], v[128:135], v[32:39], v[160:163]
	v_mfma_f32_16x16x128_f8f6f4 v[80:83], v[136:143], v[32:39], v[164:167]
	v_mfma_f32_16x16x128_f8f6f4 v[68:71], v[128:135], v[40:47], v[178:181]
	v_mfma_f32_16x16x128_f8f6f4 v[64:67], v[136:143], v[40:47], v[182:185]
	s_setprio 0
	s_barrier
	s_mov_b32 m0, s34
	s_bitset1_b32 s55, 7
	ds_read_b128 v[32:35], v177 offset:49152
	ds_read_b128 v[36:39], v177 offset:50176
	ds_read_b128 v[144:147], v177 offset:51200
	ds_read_b128 v[148:151], v177 offset:52224
	ds_read_b128 v[152:155], v177 offset:53248
	ds_read_b128 v[156:159], v177 offset:54272
	ds_read_b128 v[160:163], v177 offset:55296
	ds_read_b128 v[164:167], v177 offset:56320
	buffer_load_dwordx4 v171, s[4:7], s55 offen lds
	s_mov_b32 m0, s35
	s_nop 0
	buffer_load_dwordx4 v173, s[4:7], s55 offen lds
	s_add_i32 s55, s55, s24
	s_mov_b32 m0, s43
	s_nop 0
	buffer_load_dwordx4 v171, s[4:7], s55 offen lds
	s_mov_b32 m0, s44
	s_nop 0
	buffer_load_dwordx4 v173, s[4:7], s55 offen lds
	s_mov_b32 m0, s41
	s_nop 0
	buffer_load_dwordx4 v170, s[36:39], s54 offen lds
	s_mov_b32 m0, s42
	s_nop 0
	buffer_load_dwordx4 v172, s[36:39], s54 offen lds
	s_waitcnt vmcnt(8)
	s_waitcnt lgkmcnt(0)
	s_barrier
	s_setprio 1
	v_mfma_f32_16x16x128_f8f6f4 v[60:63], v[0:7], v[32:39], v[60:63]
	v_mfma_f32_16x16x128_f8f6f4 v[56:59], v[16:23], v[32:39], v[56:59]
	v_mfma_f32_16x16x128_f8f6f4 v[44:47], v[0:7], v[144:151], v[194:197]
	v_mfma_f32_16x16x128_f8f6f4 v[40:43], v[16:23], v[144:151], v[198:201]
	v_mfma_f32_16x16x128_f8f6f4 v[28:31], v[0:7], v[152:159], v[202:205]
	v_mfma_f32_16x16x128_f8f6f4 v[24:27], v[16:23], v[152:159], v[206:209]
	v_mfma_f32_16x16x128_f8f6f4 v[12:15], v[0:7], v[160:167], v[218:221]
	v_mfma_f32_16x16x128_f8f6f4 v[8:11], v[16:23], v[160:167], v[226:229]
	v_mfma_f32_16x16x128_f8f6f4 v[52:55], v[128:135], v[32:39], v[52:55]
	v_mfma_f32_16x16x128_f8f6f4 v[48:51], v[136:143], v[32:39], v[48:51]
	v_mfma_f32_16x16x128_f8f6f4 v[36:39], v[128:135], v[144:151], v[230:233]
	v_mfma_f32_16x16x128_f8f6f4 v[32:35], v[136:143], v[144:151], v[234:237]
	v_mfma_f32_16x16x128_f8f6f4 v[20:23], v[128:135], v[152:159], v[238:241]
	v_mfma_f32_16x16x128_f8f6f4 v[16:19], v[136:143], v[152:159], v[242:245]
	v_mfma_f32_16x16x128_f8f6f4 v[4:7], v[128:135], v[160:167], v[246:249]
	v_mfma_f32_16x16x128_f8f6f4 v[0:3], v[136:143], v[160:167], v[250:253]
	s_setprio 0
	s_barrier
	s_add_i32 s67, s67, 2
	s_addk_i32 s65, 0x100
	s_addk_i32 s66, 0x100
	s_cmp_ge_i32 s67, s47
	s_cbranch_scc0 .LBB0_1854
	v_readlane_b32 s68, v255, 22
	v_readlane_b32 s69, v255, 23
	v_mov_b32_e32 v230, v168
	v_mov_b32_e32 v233, v169
	v_mov_b32_e32 v231, v222
	v_mov_b32_e32 v234, v223
	s_and_b64 vcc, exec, s[16:17]
	s_cbranch_vccnz .LBB0_1857
	s_branch .LBB0_1858

; #define PG8_STAGE(bufoff, rs_, soff_, voff) do { _Pragma("unroll") for (int _i = 0; _i < 2; ++_i) \
;         __builtin_amdgcn_raw_ptr_buffer_load_lds(rs_, (LAS void*)(lds + (bufoff) + ldsw + _i * 8192), 16, (int)(voff)[_i], (int)(soff_), 0, 0); } while (0)
; #define PG8_LDA(dst, b, h) do { _Pragma("unroll") for (int m = 0; m < 4; ++m) dst[m] = PG8_LD2(lds + PG8_SA(b, h) + aoff + m * 2048); } while (0)
; #define PG8_LDB(dst, b, h) do { _Pragma("unroll") for (int n = 0; n < 2; ++n) dst[n] = PG8_LD2(lds + PG8_SB(b, h) + boff + n * 2048); } while (0)
; #define PG8_WAIT_V(n) asm volatile("s_waitcnt vmcnt(" #n ")" ::: "memory")
; #define PG8_WAIT_L(n) asm volatile("s_waitcnt lgkmcnt(" #n ")" ::: "memory")
; #define PG8_BAR __builtin_amdgcn_s_barrier()
; #define PG8_SCHED __builtin_amdgcn_sched_barrier(0)
; template <class Epi, class Sched, bool ALIGN_EPI = false, bool SP2 = false, bool FP8 = false>
; __device__ __forceinline__ void gemm_phase(LAS unsigned char* lds, const Gemm g, const Sched& S, const Epi& E, int wbase) {
;     ...
;             PG8_LDB(B0, 0, 0); PG8_LDB(B1, 0, 1); PG8_SCHED; PG8_LDA(At, 0, 0); PG8_STAGE(PG8_SA(1, 1), rAc, a1 + hstep, voffA);
;             PG8_WAIT_V(8); PG8_WAIT_L(0); PG8_BAR; PG8_MMA(0, 0, At, B0); PG8_MMA(0, 1, At, B1); PG8_BAR; PG8_SCHED;
;             PG8_LDA(At, 0, 1); PG8_STAGE(PG8_SB(0, 0), rB2, b2, voffB); PG8_STAGE(PG8_SB(0, 1), rB2, b2 + hstep, voffB); PG8_STAGE(PG8_SA(0, 0), rA2, a2, voffA);
;             PG8_WAIT_V(8); PG8_WAIT_L(0); PG8_BAR; PG8_MMA(1, 0, At, B0); PG8_MMA(1, 1, At, B1); PG8_BAR; PG8_SCHED;
.LBB0_1944:
	v_add_u32_e32 v136, 0x10000, v174
	v_add_u32_e32 v156, 0x14000, v174
	ds_read_b128 v[120:123], v136
	ds_read_b128 v[124:127], v136 offset:1024
	ds_read_b128 v[132:135], v136 offset:2048
	ds_read_b128 v[136:139], v136 offset:3072
	ds_read_b128 v[144:147], v156
	ds_read_b128 v[148:151], v156 offset:1024
	ds_read_b128 v[152:155], v156 offset:2048
	ds_read_b128 v[156:159], v156 offset:3072
	s_add_i32 s6, s61, 0x80
	s_cmp_eq_u32 s77, s63
	s_cselect_b32 s66, s29, s6
	s_cselect_b32 s55, s60, s62
	s_or_b32 s54, s66, 0x80
	s_add_i32 s6, s33, s61
	s_mov_b32 m0, s79
	ds_read_b128 v[160:163], v175
	ds_read_b128 v[164:167], v175 offset:1024
	ds_read_b128 v[176:179], v175 offset:2048
	ds_read_b128 v[180:183], v175 offset:3072
	ds_read_b128 v[184:187], v175 offset:4096
	ds_read_b128 v[188:191], v175 offset:5120
	ds_read_b128 v[192:195], v175 offset:6144
	ds_read_b128 v[196:199], v175 offset:7168
	buffer_load_dwordx4 v168, s[36:39], s6 offen lds
	s_mov_b32 m0, s82
	s_nop 0
	buffer_load_dwordx4 v170, s[36:39], s6 offen lds
	s_waitcnt vmcnt(8)
	s_waitcnt lgkmcnt(0)
	s_barrier
	s_setprio 1
	v_mfma_f32_16x16x32_bf16 v[140:143], v[120:123], v[160:163], v[140:143]
	v_mfma_f32_16x16x32_bf16 v[128:131], v[132:135], v[160:163], v[128:131]
	v_mfma_f32_16x16x32_bf16 v[108:111], v[120:123], v[176:179], v[108:111]
	v_mfma_f32_16x16x32_bf16 v[104:107], v[132:135], v[176:179], v[104:107]
	v_mfma_f32_16x16x32_bf16 v[92:95], v[120:123], v[184:187], v[92:95]
	v_mfma_f32_16x16x32_bf16 v[88:91], v[132:135], v[184:187], v[88:91]
	v_mfma_f32_16x16x32_bf16 v[76:79], v[120:123], v[192:195], v[76:79]
	v_mfma_f32_16x16x32_bf16 v[72:75], v[132:135], v[192:195], v[72:75]
	v_mfma_f32_16x16x32_bf16 v[140:143], v[124:127], v[164:167], v[140:143]
	v_mfma_f32_16x16x32_bf16 v[128:131], v[136:139], v[164:167], v[128:131]
	v_mfma_f32_16x16x32_bf16 v[108:111], v[124:127], v[180:183], v[108:111]
	v_mfma_f32_16x16x32_bf16 v[104:107], v[136:139], v[180:183], v[104:107]
	v_mfma_f32_16x16x32_bf16 v[92:95], v[124:127], v[188:191], v[92:95]
	v_mfma_f32_16x16x32_bf16 v[88:91], v[136:139], v[188:191], v[88:91]
	v_mfma_f32_16x16x32_bf16 v[76:79], v[124:127], v[196:199], v[76:79]
	v_mfma_f32_16x16x32_bf16 v[72:75], v[136:139], v[196:199], v[72:75]
	v_mfma_f32_16x16x32_bf16 v[116:119], v[144:147], v[160:163], v[116:119]
	v_mfma_f32_16x16x32_bf16 v[112:115], v[152:155], v[160:163], v[112:115]
	v_mfma_f32_16x16x32_bf16 v[100:103], v[144:147], v[176:179], v[100:103]
	v_mfma_f32_16x16x32_bf16 v[96:99], v[152:155], v[176:179], v[96:99]
	v_mfma_f32_16x16x32_bf16 v[84:87], v[144:147], v[184:187], v[84:87]
	v_mfma_f32_16x16x32_bf16 v[80:83], v[152:155], v[184:187], v[80:83]
	v_mfma_f32_16x16x32_bf16 v[68:71], v[144:147], v[192:195], v[68:71]
	v_mfma_f32_16x16x32_bf16 v[64:67], v[152:155], v[192:195], v[64:67]
	v_mfma_f32_16x16x32_bf16 v[116:119], v[148:151], v[164:167], v[116:119]
	v_mfma_f32_16x16x32_bf16 v[112:115], v[156:159], v[164:167], v[112:115]
	v_mfma_f32_16x16x32_bf16 v[100:103], v[148:151], v[180:183], v[100:103]
	v_mfma_f32_16x16x32_bf16 v[96:99], v[156:159], v[180:183], v[96:99]
	v_mfma_f32_16x16x32_bf16 v[84:87], v[148:151], v[188:191], v[84:87]
	v_mfma_f32_16x16x32_bf16 v[80:83], v[156:159], v[188:191], v[80:83]
	v_mfma_f32_16x16x32_bf16 v[68:71], v[148:151], v[196:199], v[68:71]
	v_mfma_f32_16x16x32_bf16 v[64:67], v[156:159], v[196:199], v[64:67]
	s_setprio 0
	s_barrier
	s_mov_b32 m0, s35
	s_mov_b32 s6, s38
	s_mov_b32 s7, s39
	ds_read_b128 v[160:163], v175 offset:16384
	ds_read_b128 v[164:167], v175 offset:17408
	ds_read_b128 v[176:179], v175 offset:18432
	ds_read_b128 v[180:183], v175 offset:19456
	ds_read_b128 v[184:187], v175 offset:20480
	ds_read_b128 v[188:191], v175 offset:21504
	ds_read_b128 v[192:195], v175 offset:22528
	ds_read_b128 v[196:199], v175 offset:23552
	buffer_load_dwordx4 v169, s[4:7], s55 offen lds
	s_mov_b32 m0, s41
	s_add_i32 s67, s55, s33
	buffer_load_dwordx4 v171, s[4:7], s55 offen lds
	s_mov_b32 m0, s42
	s_nop 0
	buffer_load_dwordx4 v169, s[4:7], s67 offen lds
	s_mov_b32 m0, s43
	s_nop 0
	buffer_load_dwordx4 v171, s[4:7], s67 offen lds
	s_mov_b32 m0, s34
	s_nop 0
	buffer_load_dwordx4 v168, s[36:39], s66 offen lds
	s_mov_b32 m0, s44
	s_nop 0
	buffer_load_dwordx4 v170, s[36:39], s66 offen lds
	s_waitcnt vmcnt(8)
	s_waitcnt lgkmcnt(0)
	s_barrier
	s_setprio 1
	v_mfma_f32_16x16x32_bf16 v[60:63], v[120:123], v[160:163], v[60:63]
	v_mfma_f32_16x16x32_bf16 v[56:59], v[132:135], v[160:163], v[56:59]
	v_mfma_f32_16x16x32_bf16 v[44:47], v[120:123], v[176:179], v[44:47]
	v_mfma_f32_16x16x32_bf16 v[40:43], v[132:135], v[176:179], v[40:43]
	v_mfma_f32_16x16x32_bf16 v[28:31], v[120:123], v[184:187], v[28:31]
	v_mfma_f32_16x16x32_bf16 v[24:27], v[132:135], v[184:187], v[24:27]
	v_mfma_f32_16x16x32_bf16 v[12:15], v[120:123], v[192:195], v[12:15]
	v_mfma_f32_16x16x32_bf16 v[8:11], v[132:135], v[192:195], v[8:11]
	v_mfma_f32_16x16x32_bf16 v[60:63], v[124:127], v[164:167], v[60:63]
	v_mfma_f32_16x16x32_bf16 v[56:59], v[136:139], v[164:167], v[56:59]
	v_mfma_f32_16x16x32_bf16 v[44:47], v[124:127], v[180:183], v[44:47]
	v_mfma_f32_16x16x32_bf16 v[40:43], v[136:139], v[180:183], v[40:43]
	v_mfma_f32_16x16x32_bf16 v[28:31], v[124:127], v[188:191], v[28:31]
	v_mfma_f32_16x16x32_bf16 v[24:27], v[136:139], v[188:191], v[24:27]
	v_mfma_f32_16x16x32_bf16 v[12:15], v[124:127], v[196:199], v[12:15]
	v_mfma_f32_16x16x32_bf16 v[8:11], v[136:139], v[196:199], v[8:11]
	v_mfma_f32_16x16x32_bf16 v[52:55], v[144:147], v[160:163], v[52:55]
	v_mfma_f32_16x16x32_bf16 v[48:51], v[152:155], v[160:163], v[48:51]
	v_mfma_f32_16x16x32_bf16 v[36:39], v[144:147], v[176:179], v[36:39]
	v_mfma_f32_16x16x32_bf16 v[32:35], v[152:155], v[176:179], v[32:35]
	v_mfma_f32_16x16x32_bf16 v[20:23], v[144:147], v[184:187], v[20:23]
	v_mfma_f32_16x16x32_bf16 v[16:19], v[152:155], v[184:187], v[16:19]
	v_mfma_f32_16x16x32_bf16 v[4:7], v[144:147], v[192:195], v[4:7]
	v_mfma_f32_16x16x32_bf16 v[0:3], v[152:155], v[192:195], v[0:3]
	v_mfma_f32_16x16x32_bf16 v[52:55], v[148:151], v[164:167], v[52:55]
	v_mfma_f32_16x16x32_bf16 v[48:51], v[156:159], v[164:167], v[48:51]
	v_mfma_f32_16x16x32_bf16 v[36:39], v[148:151], v[180:183], v[36:39]
	v_mfma_f32_16x16x32_bf16 v[32:35], v[156:159], v[180:183], v[32:35]
	v_mfma_f32_16x16x32_bf16 v[20:23], v[148:151], v[188:191], v[20:23]
	v_mfma_f32_16x16x32_bf16 v[16:19], v[156:159], v[188:191], v[16:19]
	v_mfma_f32_16x16x32_bf16 v[4:7], v[148:151], v[196:199], v[4:7]
	v_mfma_f32_16x16x32_bf16 v[0:3], v[156:159], v[196:199], v[0:3]
	s_setprio 0
	s_barrier
; #define PG8_STAGE(bufoff, rs_, soff_, voff) do { _Pragma("unroll") for (int _i = 0; _i < 2; ++_i) \
;         __builtin_amdgcn_raw_ptr_buffer_load_lds(rs_, (LAS void*)(lds + (bufoff) + ldsw + _i * 8192), 16, (int)(voff)[_i], (int)(soff_), 0, 0); } while (0)
; #define PG8_LDA(dst, b, h) do { _Pragma("unroll") for (int m = 0; m < 4; ++m) dst[m] = PG8_LD2(lds + PG8_SA(b, h) + aoff + m * 2048); } while (0)
; #define PG8_LDB(dst, b, h) do { _Pragma("unroll") for (int n = 0; n < 2; ++n) dst[n] = PG8_LD2(lds + PG8_SB(b, h) + boff + n * 2048); } while (0)
; #define PG8_WAIT_V(n) asm volatile("s_waitcnt vmcnt(" #n ")" ::: "memory")
; #define PG8_WAIT_L(n) asm volatile("s_waitcnt lgkmcnt(" #n ")" ::: "memory")
; #define PG8_BAR __builtin_amdgcn_s_barrier()
; #define PG8_SCHED __builtin_amdgcn_sched_barrier(0)
; template <class Epi, class Sched, bool ALIGN_EPI = false, bool SP2 = false, bool FP8 = false>
; __device__ __forceinline__ void gemm_phase(LAS unsigned char* lds, const Gemm g, const Sched& S, const Epi& E, int wbase) {
;     ...
;             PG8_LDB(B0, 1, 0); PG8_LDB(B1, 1, 1); PG8_SCHED; PG8_LDA(At, 1, 0); PG8_STAGE(PG8_SA(0, 1), rA2, a2 + hstep, voffA);
;             PG8_WAIT_V(8); PG8_WAIT_L(0); PG8_BAR; PG8_MMA(0, 0, At, B0); PG8_MMA(0, 1, At, B1); PG8_BAR; PG8_SCHED;
;             PG8_LDA(At, 1, 1); PG8_STAGE(PG8_SB(1, 0), rB2, b3, voffB); PG8_STAGE(PG8_SB(1, 1), rB2, b3 + hstep, voffB); PG8_STAGE(PG8_SA(1, 0), rA2, a3, voffA);
;             PG8_WAIT_V(8); PG8_WAIT_L(0); PG8_BAR; PG8_MMA(1, 0, At, B0); PG8_MMA(1, 1, At, B1); PG8_BAR; PG8_SCHED;
	v_add_u32_e32 v136, 0x18000, v174
	v_add_u32_e32 v156, 0x1c000, v174
	ds_read_b128 v[120:123], v136
	ds_read_b128 v[124:127], v136 offset:1024
	ds_read_b128 v[132:135], v136 offset:2048
	ds_read_b128 v[136:139], v136 offset:3072
	ds_read_b128 v[144:147], v156
	ds_read_b128 v[148:151], v156 offset:1024
	ds_read_b128 v[152:155], v156 offset:2048
	ds_read_b128 v[156:159], v156 offset:3072
	s_add_i32 s66, s66, s33
	s_mov_b32 m0, s45
	ds_read_b128 v[160:163], v175 offset:32768
	ds_read_b128 v[164:167], v175 offset:33792
	ds_read_b128 v[176:179], v175 offset:34816
	ds_read_b128 v[180:183], v175 offset:35840
	ds_read_b128 v[184:187], v175 offset:36864
	ds_read_b128 v[188:191], v175 offset:37888
	ds_read_b128 v[192:195], v175 offset:38912
	ds_read_b128 v[196:199], v175 offset:39936
	buffer_load_dwordx4 v168, s[36:39], s66 offen lds
	s_mov_b32 m0, s46
	s_nop 0
	buffer_load_dwordx4 v170, s[36:39], s66 offen lds
	s_waitcnt vmcnt(8)
	s_waitcnt lgkmcnt(0)
	s_barrier
	s_setprio 1
	v_mfma_f32_16x16x32_bf16 v[140:143], v[120:123], v[160:163], v[140:143]
	v_mfma_f32_16x16x32_bf16 v[128:131], v[132:135], v[160:163], v[128:131]
	v_mfma_f32_16x16x32_bf16 v[108:111], v[120:123], v[176:179], v[108:111]
	v_mfma_f32_16x16x32_bf16 v[104:107], v[132:135], v[176:179], v[104:107]
	v_mfma_f32_16x16x32_bf16 v[92:95], v[120:123], v[184:187], v[92:95]
	v_mfma_f32_16x16x32_bf16 v[88:91], v[132:135], v[184:187], v[88:91]
	v_mfma_f32_16x16x32_bf16 v[76:79], v[120:123], v[192:195], v[76:79]
	v_mfma_f32_16x16x32_bf16 v[72:75], v[132:135], v[192:195], v[72:75]
	v_mfma_f32_16x16x32_bf16 v[140:143], v[124:127], v[164:167], v[140:143]
	v_mfma_f32_16x16x32_bf16 v[128:131], v[136:139], v[164:167], v[128:131]
	v_mfma_f32_16x16x32_bf16 v[108:111], v[124:127], v[180:183], v[108:111]
	v_mfma_f32_16x16x32_bf16 v[104:107], v[136:139], v[180:183], v[104:107]
	v_mfma_f32_16x16x32_bf16 v[92:95], v[124:127], v[188:191], v[92:95]
	v_mfma_f32_16x16x32_bf16 v[88:91], v[136:139], v[188:191], v[88:91]
	v_mfma_f32_16x16x32_bf16 v[76:79], v[124:127], v[196:199], v[76:79]
	v_mfma_f32_16x16x32_bf16 v[72:75], v[136:139], v[196:199], v[72:75]
	v_mfma_f32_16x16x32_bf16 v[116:119], v[144:147], v[160:163], v[116:119]
	v_mfma_f32_16x16x32_bf16 v[112:115], v[152:155], v[160:163], v[112:115]
	v_mfma_f32_16x16x32_bf16 v[100:103], v[144:147], v[176:179], v[100:103]
	v_mfma_f32_16x16x32_bf16 v[96:99], v[152:155], v[176:179], v[96:99]
	v_mfma_f32_16x16x32_bf16 v[84:87], v[144:147], v[184:187], v[84:87]
	v_mfma_f32_16x16x32_bf16 v[80:83], v[152:155], v[184:187], v[80:83]
	v_mfma_f32_16x16x32_bf16 v[68:71], v[144:147], v[192:195], v[68:71]
	v_mfma_f32_16x16x32_bf16 v[64:67], v[152:155], v[192:195], v[64:67]
	v_mfma_f32_16x16x32_bf16 v[116:119], v[148:151], v[164:167], v[116:119]
	v_mfma_f32_16x16x32_bf16 v[112:115], v[156:159], v[164:167], v[112:115]
	v_mfma_f32_16x16x32_bf16 v[100:103], v[148:151], v[180:183], v[100:103]
	v_mfma_f32_16x16x32_bf16 v[96:99], v[156:159], v[180:183], v[96:99]
	v_mfma_f32_16x16x32_bf16 v[84:87], v[148:151], v[188:191], v[84:87]
	v_mfma_f32_16x16x32_bf16 v[80:83], v[156:159], v[188:191], v[80:83]
	v_mfma_f32_16x16x32_bf16 v[68:71], v[148:151], v[196:199], v[68:71]
	v_mfma_f32_16x16x32_bf16 v[64:67], v[156:159], v[196:199], v[64:67]
	s_setprio 0
	s_barrier
	s_mov_b32 m0, s47
	s_bitset1_b32 s55, 7
	ds_read_b128 v[160:163], v175 offset:49152
	ds_read_b128 v[164:167], v175 offset:50176
	ds_read_b128 v[176:179], v175 offset:51200
	ds_read_b128 v[180:183], v175 offset:52224
	ds_read_b128 v[184:187], v175 offset:53248
	ds_read_b128 v[188:191], v175 offset:54272
	ds_read_b128 v[192:195], v175 offset:55296
	ds_read_b128 v[196:199], v175 offset:56320
	buffer_load_dwordx4 v169, s[4:7], s55 offen lds
	s_mov_b32 m0, s48
	s_nop 0
	buffer_load_dwordx4 v171, s[4:7], s55 offen lds
	s_add_i32 s55, s55, s33
	s_mov_b32 m0, s56
	s_nop 0
	buffer_load_dwordx4 v169, s[4:7], s55 offen lds
	s_mov_b32 m0, s57
	s_nop 0
	buffer_load_dwordx4 v171, s[4:7], s55 offen lds
	s_mov_b32 m0, s52
	s_nop 0
	buffer_load_dwordx4 v168, s[36:39], s54 offen lds
	s_mov_b32 m0, s53
	s_nop 0
	buffer_load_dwordx4 v170, s[36:39], s54 offen lds
	s_waitcnt vmcnt(8)
	s_waitcnt lgkmcnt(0)
	s_barrier
	s_setprio 1
	v_mfma_f32_16x16x32_bf16 v[60:63], v[120:123], v[160:163], v[60:63]
	v_mfma_f32_16x16x32_bf16 v[56:59], v[132:135], v[160:163], v[56:59]
	v_mfma_f32_16x16x32_bf16 v[44:47], v[120:123], v[176:179], v[44:47]
	v_mfma_f32_16x16x32_bf16 v[40:43], v[132:135], v[176:179], v[40:43]
	v_mfma_f32_16x16x32_bf16 v[28:31], v[120:123], v[184:187], v[28:31]
	v_mfma_f32_16x16x32_bf16 v[24:27], v[132:135], v[184:187], v[24:27]
	v_mfma_f32_16x16x32_bf16 v[12:15], v[120:123], v[192:195], v[12:15]
	v_mfma_f32_16x16x32_bf16 v[8:11], v[132:135], v[192:195], v[8:11]
	v_mfma_f32_16x16x32_bf16 v[60:63], v[124:127], v[164:167], v[60:63]
	v_mfma_f32_16x16x32_bf16 v[56:59], v[136:139], v[164:167], v[56:59]
	v_mfma_f32_16x16x32_bf16 v[44:47], v[124:127], v[180:183], v[44:47]
	v_mfma_f32_16x16x32_bf16 v[40:43], v[136:139], v[180:183], v[40:43]
	v_mfma_f32_16x16x32_bf16 v[28:31], v[124:127], v[188:191], v[28:31]
	v_mfma_f32_16x16x32_bf16 v[24:27], v[136:139], v[188:191], v[24:27]
	v_mfma_f32_16x16x32_bf16 v[12:15], v[124:127], v[196:199], v[12:15]
	v_mfma_f32_16x16x32_bf16 v[8:11], v[136:139], v[196:199], v[8:11]
	v_mfma_f32_16x16x32_bf16 v[52:55], v[144:147], v[160:163], v[52:55]
	v_mfma_f32_16x16x32_bf16 v[48:51], v[152:155], v[160:163], v[48:51]
	v_mfma_f32_16x16x32_bf16 v[36:39], v[144:147], v[176:179], v[36:39]
	v_mfma_f32_16x16x32_bf16 v[32:35], v[152:155], v[176:179], v[32:35]
	v_mfma_f32_16x16x32_bf16 v[20:23], v[144:147], v[184:187], v[20:23]
	v_mfma_f32_16x16x32_bf16 v[16:19], v[152:155], v[184:187], v[16:19]
	v_mfma_f32_16x16x32_bf16 v[4:7], v[144:147], v[192:195], v[4:7]
	v_mfma_f32_16x16x32_bf16 v[0:3], v[152:155], v[192:195], v[0:3]
	v_mfma_f32_16x16x32_bf16 v[52:55], v[148:151], v[164:167], v[52:55]
	v_mfma_f32_16x16x32_bf16 v[48:51], v[156:159], v[164:167], v[48:51]
	v_mfma_f32_16x16x32_bf16 v[36:39], v[148:151], v[180:183], v[36:39]
	v_mfma_f32_16x16x32_bf16 v[32:35], v[156:159], v[180:183], v[32:35]
	v_mfma_f32_16x16x32_bf16 v[20:23], v[148:151], v[188:191], v[20:23]
	v_mfma_f32_16x16x32_bf16 v[16:19], v[156:159], v[188:191], v[16:19]
	v_mfma_f32_16x16x32_bf16 v[4:7], v[148:151], v[196:199], v[4:7]
	v_mfma_f32_16x16x32_bf16 v[0:3], v[156:159], v[196:199], v[0:3]
	s_setprio 0
	s_barrier
	s_add_i32 s63, s63, 2
	s_addk_i32 s61, 0x100
	s_addk_i32 s62, 0x100
	s_cmp_ge_i32 s63, s65
	s_cbranch_scc0 .LBB0_1944
	s_and_b64 vcc, exec, s[24:25]
	s_cbranch_vccz .LBB0_1947

; #define PG8_STAGE(bufoff, rs_, soff_, voff) do { _Pragma("unroll") for (int _i = 0; _i < 2; ++_i) \
;         __builtin_amdgcn_raw_ptr_buffer_load_lds(rs_, (LAS void*)(lds + (bufoff) + ldsw + _i * 8192), 16, (int)(voff)[_i], (int)(soff_), 0, 0); } while (0)
; #define PG8_LDA(dst, b, h) do { _Pragma("unroll") for (int m = 0; m < 4; ++m) dst[m] = PG8_LD2(lds + PG8_SA(b, h) + aoff + m * 2048); } while (0)
; #define PG8_LDB(dst, b, h) do { _Pragma("unroll") for (int n = 0; n < 2; ++n) dst[n] = PG8_LD2(lds + PG8_SB(b, h) + boff + n * 2048); } while (0)
; #define PG8_WAIT_V(n) asm volatile("s_waitcnt vmcnt(" #n ")" ::: "memory")
; #define PG8_WAIT_L(n) asm volatile("s_waitcnt lgkmcnt(" #n ")" ::: "memory")
; #define PG8_BAR __builtin_amdgcn_s_barrier()
; #define PG8_SCHED __builtin_amdgcn_sched_barrier(0)
; template <class Epi, class Sched, bool ALIGN_EPI = false, bool SP2 = false, bool FP8 = false>
; __device__ __forceinline__ void gemm_phase(LAS unsigned char* lds, const Gemm g, const Sched& S, const Epi& E, int wbase) {
;     ...
;             PG8_LDB(B0, 0, 0); PG8_LDB(B1, 0, 1); PG8_SCHED; PG8_LDA(At, 0, 0); PG8_STAGE(PG8_SA(1, 1), rAc, a1 + hstep, voffA);
;             PG8_WAIT_V(8); PG8_WAIT_L(0); PG8_BAR; PG8_MMA(0, 0, At, B0); PG8_MMA(0, 1, At, B1); PG8_BAR; PG8_SCHED;
;             PG8_LDA(At, 0, 1); PG8_STAGE(PG8_SB(0, 0), rB2, b2, voffB); PG8_STAGE(PG8_SB(0, 1), rB2, b2 + hstep, voffB); PG8_STAGE(PG8_SA(0, 0), rA2, a2, voffA);
;             PG8_WAIT_V(8); PG8_WAIT_L(0); PG8_BAR; PG8_MMA(1, 0, At, B0); PG8_MMA(1, 1, At, B1); PG8_BAR; PG8_SCHED;
.LBB0_1990:
	v_add_u32_e32 v136, 0x10000, v180
	v_add_u32_e32 v156, 0x14000, v180
	ds_read_b128 v[120:123], v136
	ds_read_b128 v[124:127], v136 offset:1024
	ds_read_b128 v[132:135], v136 offset:2048
	ds_read_b128 v[136:139], v136 offset:3072
	ds_read_b128 v[144:147], v156
	ds_read_b128 v[148:151], v156 offset:1024
	ds_read_b128 v[152:155], v156 offset:2048
	ds_read_b128 v[156:159], v156 offset:3072
	s_add_i32 s14, s4, 0x80
	s_cmp_eq_u32 s84, s61
	s_cselect_b32 s62, s2, s14
	s_cselect_b32 s55, s3, s5
	s_or_b32 s54, s62, 0x80
	s_add_i32 s14, s42, s4
	s_mov_b32 m0, s85
	ds_read_b128 v[160:163], v181
	ds_read_b128 v[164:167], v181 offset:1024
	ds_read_b128 v[182:185], v181 offset:2048
	ds_read_b128 v[186:189], v181 offset:3072
	ds_read_b128 v[194:197], v181 offset:4096
	ds_read_b128 v[198:201], v181 offset:5120
	ds_read_b128 v[202:205], v181 offset:6144
	ds_read_b128 v[206:209], v181 offset:7168
	buffer_load_dwordx4 v174, s[36:39], s14 offen lds
	s_mov_b32 m0, s8
	s_nop 0
	buffer_load_dwordx4 v176, s[36:39], s14 offen lds
	s_waitcnt vmcnt(8)
	s_waitcnt lgkmcnt(0)
	s_barrier
	s_setprio 1
	v_mfma_f32_16x16x128_f8f6f4 v[140:143], v[120:127], v[160:167], v[140:143]
	v_mfma_f32_16x16x128_f8f6f4 v[128:131], v[132:139], v[160:167], v[128:131]
	v_mfma_f32_16x16x128_f8f6f4 v[108:111], v[120:127], v[182:189], v[108:111]
	v_mfma_f32_16x16x128_f8f6f4 v[104:107], v[132:139], v[182:189], v[104:107]
	v_mfma_f32_16x16x128_f8f6f4 v[168:171], v[120:127], v[194:201], v[92:95]
	v_mfma_f32_16x16x128_f8f6f4 v[190:193], v[132:139], v[194:201], v[88:91]
	v_mfma_f32_16x16x128_f8f6f4 v[210:213], v[120:127], v[202:209], v[76:79]
	v_mfma_f32_16x16x128_f8f6f4 v[214:217], v[132:139], v[202:209], v[72:75]
	v_mfma_f32_16x16x128_f8f6f4 v[116:119], v[144:151], v[160:167], v[116:119]
	v_mfma_f32_16x16x128_f8f6f4 v[112:115], v[152:159], v[160:167], v[112:115]
	v_mfma_f32_16x16x128_f8f6f4 v[100:103], v[144:151], v[182:189], v[100:103]
	v_mfma_f32_16x16x128_f8f6f4 v[96:99], v[152:159], v[182:189], v[96:99]
	v_mfma_f32_16x16x128_f8f6f4 v[160:163], v[144:151], v[194:201], v[84:87]
	v_mfma_f32_16x16x128_f8f6f4 v[164:167], v[152:159], v[194:201], v[80:83]
	v_mfma_f32_16x16x128_f8f6f4 v[182:185], v[144:151], v[202:209], v[68:71]
	v_mfma_f32_16x16x128_f8f6f4 v[186:189], v[152:159], v[202:209], v[64:67]
	s_setprio 0
	s_barrier
	s_mov_b32 m0, s44
	s_mov_b32 s14, s38
	s_mov_b32 s15, s39
	s_nop 1
	ds_read_b128 v[64:67], v181 offset:16384
	ds_read_b128 v[68:71], v181 offset:17408
	ds_read_b128 v[72:75], v181 offset:18432
	ds_read_b128 v[76:79], v181 offset:19456
	ds_read_b128 v[80:83], v181 offset:20480
	ds_read_b128 v[84:87], v181 offset:21504
	ds_read_b128 v[88:91], v181 offset:22528
	ds_read_b128 v[92:95], v181 offset:23552
	buffer_load_dwordx4 v175, s[12:15], s55 offen lds
	s_mov_b32 m0, s45
	s_add_i32 s63, s55, s42
	buffer_load_dwordx4 v177, s[12:15], s55 offen lds
	s_mov_b32 m0, s46
	s_nop 0
	buffer_load_dwordx4 v175, s[12:15], s63 offen lds
	s_mov_b32 m0, s47
	s_nop 0
	buffer_load_dwordx4 v177, s[12:15], s63 offen lds
	s_mov_b32 m0, s43
	s_nop 0
	buffer_load_dwordx4 v174, s[36:39], s62 offen lds
	s_mov_b32 m0, s48
	s_nop 0
	buffer_load_dwordx4 v176, s[36:39], s62 offen lds
	s_waitcnt vmcnt(8)
	s_waitcnt lgkmcnt(0)
	s_barrier
	s_setprio 1
	v_mfma_f32_16x16x128_f8f6f4 v[60:63], v[120:127], v[64:71], v[60:63]
	v_mfma_f32_16x16x128_f8f6f4 v[56:59], v[132:139], v[64:71], v[56:59]
	v_mfma_f32_16x16x128_f8f6f4 v[194:197], v[120:127], v[72:79], v[44:47]
	v_mfma_f32_16x16x128_f8f6f4 v[198:201], v[132:139], v[72:79], v[40:43]
	v_mfma_f32_16x16x128_f8f6f4 v[202:205], v[120:127], v[80:87], v[28:31]
	v_mfma_f32_16x16x128_f8f6f4 v[206:209], v[132:139], v[80:87], v[24:27]
	v_mfma_f32_16x16x128_f8f6f4 v[218:221], v[120:127], v[88:95], v[12:15]
	v_mfma_f32_16x16x128_f8f6f4 v[226:229], v[132:139], v[88:95], v[8:11]
	v_mfma_f32_16x16x128_f8f6f4 v[52:55], v[144:151], v[64:71], v[52:55]
	v_mfma_f32_16x16x128_f8f6f4 v[48:51], v[152:159], v[64:71], v[48:51]
	v_mfma_f32_16x16x128_f8f6f4 v[230:233], v[144:151], v[72:79], v[36:39]
	v_mfma_f32_16x16x128_f8f6f4 v[234:237], v[152:159], v[72:79], v[32:35]
	v_mfma_f32_16x16x128_f8f6f4 v[238:241], v[144:151], v[80:87], v[20:23]
	v_mfma_f32_16x16x128_f8f6f4 v[242:245], v[152:159], v[80:87], v[16:19]
	v_mfma_f32_16x16x128_f8f6f4 v[246:249], v[144:151], v[88:95], v[4:7]
	v_mfma_f32_16x16x128_f8f6f4 v[250:253], v[152:159], v[88:95], v[0:3]
	s_setprio 0
	s_barrier
; #define PG8_STAGE(bufoff, rs_, soff_, voff) do { _Pragma("unroll") for (int _i = 0; _i < 2; ++_i) \
;         __builtin_amdgcn_raw_ptr_buffer_load_lds(rs_, (LAS void*)(lds + (bufoff) + ldsw + _i * 8192), 16, (int)(voff)[_i], (int)(soff_), 0, 0); } while (0)
; #define PG8_LDA(dst, b, h) do { _Pragma("unroll") for (int m = 0; m < 4; ++m) dst[m] = PG8_LD2(lds + PG8_SA(b, h) + aoff + m * 2048); } while (0)
; #define PG8_LDB(dst, b, h) do { _Pragma("unroll") for (int n = 0; n < 2; ++n) dst[n] = PG8_LD2(lds + PG8_SB(b, h) + boff + n * 2048); } while (0)
; #define PG8_WAIT_V(n) asm volatile("s_waitcnt vmcnt(" #n ")" ::: "memory")
; #define PG8_WAIT_L(n) asm volatile("s_waitcnt lgkmcnt(" #n ")" ::: "memory")
; #define PG8_BAR __builtin_amdgcn_s_barrier()
; #define PG8_SCHED __builtin_amdgcn_sched_barrier(0)
; template <class Epi, class Sched, bool ALIGN_EPI = false, bool SP2 = false, bool FP8 = false>
; __device__ __forceinline__ void gemm_phase(LAS unsigned char* lds, const Gemm g, const Sched& S, const Epi& E, int wbase) {
;     ...
;             PG8_LDB(B0, 1, 0); PG8_LDB(B1, 1, 1); PG8_SCHED; PG8_LDA(At, 1, 0); PG8_STAGE(PG8_SA(0, 1), rA2, a2 + hstep, voffA);
;             PG8_WAIT_V(8); PG8_WAIT_L(0); PG8_BAR; PG8_MMA(0, 0, At, B0); PG8_MMA(0, 1, At, B1); PG8_BAR; PG8_SCHED;
;             PG8_LDA(At, 1, 1); PG8_STAGE(PG8_SB(1, 0), rB2, b3, voffB); PG8_STAGE(PG8_SB(1, 1), rB2, b3 + hstep, voffB); PG8_STAGE(PG8_SA(1, 0), rA2, a3, voffA);
;             PG8_WAIT_V(8); PG8_WAIT_L(0); PG8_BAR; PG8_MMA(1, 0, At, B0); PG8_MMA(1, 1, At, B1); PG8_BAR; PG8_SCHED;
	v_add_u32_e32 v8, 0x18000, v180
	s_nop 3
	ds_read_b128 v[0:3], v8
	ds_read_b128 v[4:7], v8 offset:1024
	ds_read_b128 v[16:19], v8 offset:2048
	ds_read_b128 v[20:23], v8 offset:3072
	v_add_u32_e32 v8, 0x1c000, v180
	ds_read_b128 v[120:123], v8
	ds_read_b128 v[124:127], v8 offset:1024
	ds_read_b128 v[132:135], v8 offset:2048
	ds_read_b128 v[136:139], v8 offset:3072
	s_add_i32 s62, s62, s42
	s_mov_b32 m0, s52
	ds_read_b128 v[8:11], v181 offset:32768
	ds_read_b128 v[12:15], v181 offset:33792
	ds_read_b128 v[24:27], v181 offset:34816
	ds_read_b128 v[28:31], v181 offset:35840
	ds_read_b128 v[32:35], v181 offset:36864
	ds_read_b128 v[36:39], v181 offset:37888
	ds_read_b128 v[40:43], v181 offset:38912
	ds_read_b128 v[44:47], v181 offset:39936
	buffer_load_dwordx4 v174, s[36:39], s62 offen lds
	s_mov_b32 m0, s53
	s_nop 0
	buffer_load_dwordx4 v176, s[36:39], s62 offen lds
	s_waitcnt vmcnt(8)
	s_waitcnt lgkmcnt(0)
	s_barrier
	s_setprio 1
	v_mfma_f32_16x16x128_f8f6f4 v[140:143], v[0:7], v[8:15], v[140:143]
	v_mfma_f32_16x16x128_f8f6f4 v[128:131], v[16:23], v[8:15], v[128:131]
	v_mfma_f32_16x16x128_f8f6f4 v[108:111], v[0:7], v[24:31], v[108:111]
	v_mfma_f32_16x16x128_f8f6f4 v[104:107], v[16:23], v[24:31], v[104:107]
	v_mfma_f32_16x16x128_f8f6f4 v[92:95], v[0:7], v[32:39], v[168:171]
	v_mfma_f32_16x16x128_f8f6f4 v[88:91], v[16:23], v[32:39], v[190:193]
	v_mfma_f32_16x16x128_f8f6f4 v[76:79], v[0:7], v[40:47], v[210:213]
	v_mfma_f32_16x16x128_f8f6f4 v[72:75], v[16:23], v[40:47], v[214:217]
	v_mfma_f32_16x16x128_f8f6f4 v[116:119], v[120:127], v[8:15], v[116:119]
	v_mfma_f32_16x16x128_f8f6f4 v[112:115], v[132:139], v[8:15], v[112:115]
	v_mfma_f32_16x16x128_f8f6f4 v[100:103], v[120:127], v[24:31], v[100:103]
	v_mfma_f32_16x16x128_f8f6f4 v[96:99], v[132:139], v[24:31], v[96:99]
	v_mfma_f32_16x16x128_f8f6f4 v[84:87], v[120:127], v[32:39], v[160:163]
	v_mfma_f32_16x16x128_f8f6f4 v[80:83], v[132:139], v[32:39], v[164:167]
	v_mfma_f32_16x16x128_f8f6f4 v[68:71], v[120:127], v[40:47], v[182:185]
	v_mfma_f32_16x16x128_f8f6f4 v[64:67], v[132:139], v[40:47], v[186:189]
	s_setprio 0
	s_barrier
	s_mov_b32 m0, s56
	s_bitset1_b32 s55, 7
	ds_read_b128 v[32:35], v181 offset:49152
	ds_read_b128 v[36:39], v181 offset:50176
	ds_read_b128 v[144:147], v181 offset:51200
	ds_read_b128 v[148:151], v181 offset:52224
	ds_read_b128 v[152:155], v181 offset:53248
	ds_read_b128 v[156:159], v181 offset:54272
	ds_read_b128 v[160:163], v181 offset:55296
	ds_read_b128 v[164:167], v181 offset:56320
	buffer_load_dwordx4 v175, s[12:15], s55 offen lds
	s_mov_b32 m0, s57
	s_nop 0
	buffer_load_dwordx4 v177, s[12:15], s55 offen lds
	s_add_i32 s55, s55, s42
	s_mov_b32 m0, s65
	s_nop 0
	buffer_load_dwordx4 v175, s[12:15], s55 offen lds
	s_mov_b32 m0, s76
	s_nop 0
	buffer_load_dwordx4 v177, s[12:15], s55 offen lds
	s_mov_b32 m0, s58
	s_nop 0
	buffer_load_dwordx4 v174, s[36:39], s54 offen lds
	s_mov_b32 m0, s59
	s_nop 0
	buffer_load_dwordx4 v176, s[36:39], s54 offen lds
	s_waitcnt vmcnt(8)
	s_waitcnt lgkmcnt(0)
	s_barrier
	s_setprio 1
	v_mfma_f32_16x16x128_f8f6f4 v[60:63], v[0:7], v[32:39], v[60:63]
	v_mfma_f32_16x16x128_f8f6f4 v[56:59], v[16:23], v[32:39], v[56:59]
	v_mfma_f32_16x16x128_f8f6f4 v[44:47], v[0:7], v[144:151], v[194:197]
	v_mfma_f32_16x16x128_f8f6f4 v[40:43], v[16:23], v[144:151], v[198:201]
	v_mfma_f32_16x16x128_f8f6f4 v[28:31], v[0:7], v[152:159], v[202:205]
	v_mfma_f32_16x16x128_f8f6f4 v[24:27], v[16:23], v[152:159], v[206:209]
	v_mfma_f32_16x16x128_f8f6f4 v[12:15], v[0:7], v[160:167], v[218:221]
	v_mfma_f32_16x16x128_f8f6f4 v[8:11], v[16:23], v[160:167], v[226:229]
	v_mfma_f32_16x16x128_f8f6f4 v[52:55], v[120:127], v[32:39], v[52:55]
	v_mfma_f32_16x16x128_f8f6f4 v[48:51], v[132:139], v[32:39], v[48:51]
	v_mfma_f32_16x16x128_f8f6f4 v[36:39], v[120:127], v[144:151], v[230:233]
	v_mfma_f32_16x16x128_f8f6f4 v[32:35], v[132:139], v[144:151], v[234:237]
	v_mfma_f32_16x16x128_f8f6f4 v[20:23], v[120:127], v[152:159], v[238:241]
	v_mfma_f32_16x16x128_f8f6f4 v[16:19], v[132:139], v[152:159], v[242:245]
	v_mfma_f32_16x16x128_f8f6f4 v[4:7], v[120:127], v[160:167], v[246:249]
	v_mfma_f32_16x16x128_f8f6f4 v[0:3], v[132:139], v[160:167], v[250:253]
	s_setprio 0
	s_barrier
	s_add_i32 s61, s61, 2
	s_addk_i32 s4, 0x100
	s_addk_i32 s5, 0x100
	s_cmp_ge_i32 s61, s82
	s_cbranch_scc0 .LBB0_1990
	v_mov_b32_e32 v230, v172
	v_mov_b32_e32 v233, v173
	v_mov_b32_e32 v231, v222
	v_mov_b32_e32 v234, v223
	s_and_b64 vcc, exec, s[28:29]
	s_cbranch_vccnz .LBB0_1993
	s_branch .LBB0_1994
